# bundle9 + all global_store_dwordx4 made write-through (sc1) so the grid-barrier L2 write-back finds little dirty data
# speedup vs baseline: 1.0193x; 1.0122x over previous
.LBB0_23:
	s_andn2_b64 vcc, exec, s[4:5]
	s_cbranch_vccnz .LBB0_25
	s_ashr_i32 s17, s16, 31
	s_lshl_b64 s[4:5], s[16:17], 22
	s_add_u32 s82, s8, s4
	s_addc_u32 s83, s9, s5
	s_lshl_b64 s[18:19], s[16:17], 21
	v_readlane_b32 s4, v254, 6
	s_add_u32 s5, s4, s18
	v_readlane_b32 s4, v254, 7
	s_addc_u32 s17, s4, s19
	s_mul_i32 s4, s16, 0xffffe200
	s_add_i32 s4, s28, s4
	s_and_b32 s4, s4, 0xfc0
	s_add_i32 s14, s4, 0xfffff600
	s_and_b32 s4, s26, 0x3e0
	s_lshl_b32 s18, s4, 2
	v_or_b32_e32 v2, s14, v26
	s_add_u32 s18, s82, s18
	s_addc_u32 s19, s83, 0
	v_mov_b32_e32 v7, v3
	v_or_b32_e32 v12, 2, v2
	v_mov_b32_e32 v13, v3
	v_or_b32_e32 v14, 4, v2
	v_mov_b32_e32 v15, v3
	v_or_b32_e32 v16, 6, v2
	v_mov_b32_e32 v17, v3
	v_or_b32_e32 v18, 8, v2
	v_mov_b32_e32 v19, v3
	v_or_b32_e32 v20, 10, v2
	v_mov_b32_e32 v21, v3
	v_or_b32_e32 v22, 12, v2
	v_mov_b32_e32 v23, v3
	v_lshl_add_u64 v[8:9], s[18:19], 0, v[6:7]
	v_lshlrev_b64 v[10:11], 12, v[2:3]
	v_lshlrev_b64 v[12:13], 12, v[12:13]
	v_lshlrev_b64 v[14:15], 12, v[14:15]
	v_lshlrev_b64 v[16:17], 12, v[16:17]
	v_lshlrev_b64 v[18:19], 12, v[18:19]
	v_lshlrev_b64 v[20:21], 12, v[20:21]
	v_lshlrev_b64 v[22:23], 12, v[22:23]
	v_or_b32_e32 v24, 14, v2
	v_mov_b32_e32 v25, v3
	v_lshl_add_u64 v[10:11], v[8:9], 0, v[10:11]
	v_lshl_add_u64 v[12:13], v[8:9], 0, v[12:13]
	v_lshl_add_u64 v[14:15], v[8:9], 0, v[14:15]
	v_lshl_add_u64 v[16:17], v[8:9], 0, v[16:17]
	v_lshl_add_u64 v[18:19], v[8:9], 0, v[18:19]
	v_lshl_add_u64 v[20:21], v[8:9], 0, v[20:21]
	v_lshl_add_u64 v[22:23], v[8:9], 0, v[22:23]
	v_lshlrev_b64 v[24:25], 12, v[24:25]
	v_lshl_add_u64 v[24:25], v[8:9], 0, v[24:25]
	global_load_dword v7, v[10:11], off nt
	global_load_dword v77, v[12:13], off nt
	global_load_dword v78, v[14:15], off nt
	global_load_dword v79, v[16:17], off nt
	global_load_dword v80, v[18:19], off nt
	global_load_dword v81, v[20:21], off nt
	global_load_dword v82, v[22:23], off nt
	global_load_dword v83, v[24:25], off nt
	v_or_b32_e32 v10, 16, v2
	v_mov_b32_e32 v11, v3
	v_or_b32_e32 v12, 18, v2
	v_mov_b32_e32 v13, v3
	v_or_b32_e32 v14, 20, v2
	v_mov_b32_e32 v15, v3
	v_or_b32_e32 v16, 22, v2
	v_mov_b32_e32 v17, v3
	v_or_b32_e32 v18, 24, v2
	v_mov_b32_e32 v19, v3
	v_or_b32_e32 v20, 26, v2
	v_mov_b32_e32 v21, v3
	v_or_b32_e32 v22, 28, v2
	v_mov_b32_e32 v23, v3
	v_lshlrev_b64 v[10:11], 12, v[10:11]
	v_lshlrev_b64 v[12:13], 12, v[12:13]
	v_lshlrev_b64 v[14:15], 12, v[14:15]
	v_lshlrev_b64 v[16:17], 12, v[16:17]
	v_lshlrev_b64 v[18:19], 12, v[18:19]
	v_lshlrev_b64 v[20:21], 12, v[20:21]
	v_lshlrev_b64 v[22:23], 12, v[22:23]
	v_or_b32_e32 v24, 30, v2
	v_mov_b32_e32 v25, v3
	v_lshl_add_u64 v[10:11], v[8:9], 0, v[10:11]
	v_lshl_add_u64 v[12:13], v[8:9], 0, v[12:13]
	v_lshl_add_u64 v[14:15], v[8:9], 0, v[14:15]
	v_lshl_add_u64 v[16:17], v[8:9], 0, v[16:17]
	v_lshl_add_u64 v[18:19], v[8:9], 0, v[18:19]
	v_lshl_add_u64 v[20:21], v[8:9], 0, v[20:21]
	v_lshl_add_u64 v[22:23], v[8:9], 0, v[22:23]
	v_lshlrev_b64 v[24:25], 12, v[24:25]
	v_lshl_add_u64 v[24:25], v[8:9], 0, v[24:25]
	global_load_dword v84, v[10:11], off nt
	global_load_dword v85, v[12:13], off nt
	global_load_dword v86, v[14:15], off nt
	global_load_dword v87, v[16:17], off nt
	global_load_dword v88, v[18:19], off nt
	global_load_dword v89, v[20:21], off nt
	global_load_dword v90, v[22:23], off nt
	global_load_dword v91, v[24:25], off nt
	v_or_b32_e32 v10, 32, v2
	v_mov_b32_e32 v11, v3
	v_or_b32_e32 v12, 34, v2
	v_mov_b32_e32 v13, v3
	v_or_b32_e32 v14, 36, v2
	v_mov_b32_e32 v15, v3
	v_or_b32_e32 v16, 38, v2
	v_mov_b32_e32 v17, v3
	v_or_b32_e32 v18, 40, v2
	v_mov_b32_e32 v19, v3
	v_or_b32_e32 v20, 42, v2
	v_mov_b32_e32 v21, v3
	v_or_b32_e32 v22, 44, v2
	v_mov_b32_e32 v23, v3
	v_lshlrev_b64 v[10:11], 12, v[10:11]
	v_lshlrev_b64 v[12:13], 12, v[12:13]
	v_lshlrev_b64 v[14:15], 12, v[14:15]
	v_lshlrev_b64 v[16:17], 12, v[16:17]
	v_lshlrev_b64 v[18:19], 12, v[18:19]
	v_lshlrev_b64 v[20:21], 12, v[20:21]
	v_lshlrev_b64 v[22:23], 12, v[22:23]
	v_or_b32_e32 v24, 46, v2
	v_mov_b32_e32 v25, v3
	v_lshl_add_u64 v[10:11], v[8:9], 0, v[10:11]
	v_lshl_add_u64 v[12:13], v[8:9], 0, v[12:13]
	v_lshl_add_u64 v[14:15], v[8:9], 0, v[14:15]
	v_lshl_add_u64 v[16:17], v[8:9], 0, v[16:17]
	v_lshl_add_u64 v[18:19], v[8:9], 0, v[18:19]
	v_lshl_add_u64 v[20:21], v[8:9], 0, v[20:21]
	v_lshl_add_u64 v[22:23], v[8:9], 0, v[22:23]
	v_lshlrev_b64 v[24:25], 12, v[24:25]
	v_lshl_add_u64 v[24:25], v[8:9], 0, v[24:25]
	global_load_dword v92, v[10:11], off nt
	global_load_dword v93, v[12:13], off nt
	global_load_dword v94, v[14:15], off nt
	global_load_dword v95, v[16:17], off nt
	global_load_dword v96, v[18:19], off nt
	global_load_dword v97, v[20:21], off nt
	global_load_dword v98, v[22:23], off nt
	global_load_dword v99, v[24:25], off nt
	v_or_b32_e32 v10, 48, v2
	v_mov_b32_e32 v11, v3
	v_or_b32_e32 v12, 50, v2
	v_mov_b32_e32 v13, v3
	v_or_b32_e32 v14, 52, v2
	v_mov_b32_e32 v15, v3
	v_or_b32_e32 v16, 54, v2
	v_mov_b32_e32 v17, v3
	v_or_b32_e32 v18, 56, v2
	v_mov_b32_e32 v19, v3
	v_or_b32_e32 v20, 58, v2
	v_mov_b32_e32 v21, v3
	v_or_b32_e32 v22, 60, v2
	v_mov_b32_e32 v23, v3
	v_or_b32_e32 v2, 62, v2
	v_lshlrev_b64 v[10:11], 12, v[10:11]
	v_lshlrev_b64 v[12:13], 12, v[12:13]
	v_lshlrev_b64 v[14:15], 12, v[14:15]
	v_lshlrev_b64 v[16:17], 12, v[16:17]
	v_lshlrev_b64 v[18:19], 12, v[18:19]
	v_lshlrev_b64 v[20:21], 12, v[20:21]
	v_lshlrev_b64 v[22:23], 12, v[22:23]
	v_lshlrev_b64 v[24:25], 12, v[2:3]
	v_lshl_add_u64 v[10:11], v[8:9], 0, v[10:11]
	v_lshl_add_u64 v[12:13], v[8:9], 0, v[12:13]
	v_lshl_add_u64 v[14:15], v[8:9], 0, v[14:15]
	v_lshl_add_u64 v[16:17], v[8:9], 0, v[16:17]
	v_lshl_add_u64 v[18:19], v[8:9], 0, v[18:19]
	v_lshl_add_u64 v[20:21], v[8:9], 0, v[20:21]
	v_lshl_add_u64 v[22:23], v[8:9], 0, v[22:23]
	v_lshl_add_u64 v[8:9], v[8:9], 0, v[24:25]
	global_load_dword v2, v[10:11], off nt
	s_nop 0
	global_load_dword v10, v[12:13], off nt
	global_load_dword v11, v[14:15], off nt
	s_nop 0
	global_load_dword v12, v[16:17], off nt
	global_load_dword v13, v[18:19], off nt
	global_load_dword v14, v[20:21], off nt
	global_load_dword v15, v[22:23], off nt
	s_nop 0
	global_load_dword v8, v[8:9], off nt
	s_waitcnt vmcnt(30)
	ds_write2_b32 v27, v7, v77 offset1:66
	s_waitcnt vmcnt(28)
	ds_write2_b32 v27, v78, v79 offset0:132 offset1:198
	s_waitcnt vmcnt(26)
	ds_write2_b32 v38, v80, v81 offset0:8 offset1:74
	s_waitcnt vmcnt(24)
	ds_write2_b32 v38, v82, v83 offset0:140 offset1:206
	s_waitcnt vmcnt(22)
	ds_write2_b32 v39, v84, v85 offset0:16 offset1:82
	s_waitcnt vmcnt(20)
	ds_write2_b32 v39, v86, v87 offset0:148 offset1:214
	s_waitcnt vmcnt(18)
	ds_write2_b32 v40, v88, v89 offset0:24 offset1:90
	s_waitcnt vmcnt(16)
	ds_write2_b32 v40, v90, v91 offset0:156 offset1:222
	s_waitcnt vmcnt(14)
	ds_write2_b32 v41, v92, v93 offset0:32 offset1:98
	s_waitcnt vmcnt(12)
	ds_write2_b32 v41, v94, v95 offset0:164 offset1:230
	s_waitcnt vmcnt(10)
	ds_write2_b32 v42, v96, v97 offset0:40 offset1:106
	s_waitcnt vmcnt(8)
	ds_write2_b32 v42, v98, v99 offset0:172 offset1:238
	s_waitcnt vmcnt(6)
	ds_write2_b32 v43, v2, v10 offset0:48 offset1:114
	s_waitcnt vmcnt(4)
	ds_write2_b32 v43, v11, v12 offset0:180 offset1:246
	s_waitcnt vmcnt(2)
	ds_write2_b32 v44, v13, v14 offset0:56 offset1:122
	s_waitcnt vmcnt(0)
	ds_write2_b32 v44, v15, v8 offset0:188 offset1:254
	s_waitcnt lgkmcnt(0)
	s_lshl_b64 s[18:19], s[14:15], 1
	ds_read2_b32 v[12:13], v29 offset0:33 offset1:41
	ds_read2_b32 v[14:15], v29 offset1:8
	ds_read2_b32 v[16:17], v29 offset0:66 offset1:74
	ds_read2_b32 v[18:19], v29 offset0:99 offset1:107
	ds_read2_b32 v[20:21], v29 offset0:132 offset1:140
	ds_read2_b32 v[22:23], v29 offset0:165 offset1:173
	ds_read2_b32 v[24:25], v29 offset0:198 offset1:206
	ds_read2_b32 v[78:79], v29 offset0:231 offset1:239
	s_add_u32 s18, s5, s18
	s_addc_u32 s19, s17, s19
	v_lshlrev_b32_e32 v2, 1, v4
	v_lshl_add_u64 v[80:81], s[18:19], 0, v[2:3]
	v_or_b32_e32 v2, s4, v28
	v_lshlrev_b32_e32 v2, 11, v2
	s_waitcnt lgkmcnt(6)
	v_cvt_pk_bf16_f32 v8, v14, v12
	s_waitcnt lgkmcnt(4)
	v_cvt_pk_bf16_f32 v9, v16, v18
	s_waitcnt lgkmcnt(2)
	v_cvt_pk_bf16_f32 v10, v20, v22
	s_waitcnt lgkmcnt(0)
	v_cvt_pk_bf16_f32 v11, v24, v78
	v_lshl_add_u64 v[82:83], v[80:81], 0, v[2:3]
	global_store_dwordx4 v[82:83], v[8:11], off sc1
	v_or_b32_e32 v2, s4, v30
	v_lshlrev_b32_e32 v2, 11, v2
	v_cvt_pk_bf16_f32 v8, v15, v13
	v_cvt_pk_bf16_f32 v9, v17, v19
	v_cvt_pk_bf16_f32 v10, v21, v23
	v_cvt_pk_bf16_f32 v11, v25, v79
	ds_read2_b32 v[14:15], v29 offset0:49 offset1:57
	ds_read2_b32 v[16:17], v29 offset0:16 offset1:24
	ds_read2_b32 v[18:19], v29 offset0:82 offset1:90
	ds_read2_b32 v[20:21], v29 offset0:115 offset1:123
	ds_read2_b32 v[22:23], v29 offset0:148 offset1:156
	ds_read2_b32 v[24:25], v29 offset0:181 offset1:189
	ds_read2_b32 v[78:79], v29 offset0:214 offset1:222
	ds_read2_b32 v[82:83], v29 offset0:247 offset1:255
	v_lshl_add_u64 v[12:13], v[80:81], 0, v[2:3]
	v_or_b32_e32 v2, s4, v31
	v_lshlrev_b32_e32 v2, 11, v2
	global_store_dwordx4 v[12:13], v[8:11], off sc1
	v_lshl_add_u64 v[12:13], v[80:81], 0, v[2:3]
	v_or_b32_e32 v2, s4, v32
	s_waitcnt lgkmcnt(6)
	v_cvt_pk_bf16_f32 v8, v16, v14
	s_waitcnt lgkmcnt(4)
	v_cvt_pk_bf16_f32 v9, v18, v20
	s_waitcnt lgkmcnt(2)
	v_cvt_pk_bf16_f32 v10, v22, v24
	s_waitcnt lgkmcnt(0)
	v_cvt_pk_bf16_f32 v11, v78, v82
	v_lshlrev_b32_e32 v2, 11, v2
	global_store_dwordx4 v[12:13], v[8:11], off sc1
	v_lshl_add_u64 v[12:13], v[80:81], 0, v[2:3]
	s_nop 0
	v_cvt_pk_bf16_f32 v8, v17, v15
	v_cvt_pk_bf16_f32 v9, v19, v21
	v_cvt_pk_bf16_f32 v10, v23, v25
	v_cvt_pk_bf16_f32 v11, v79, v83
	global_store_dwordx4 v[12:13], v[8:11], off sc1
	s_waitcnt lgkmcnt(0)

.LBB0_26:
	s_andn2_b64 vcc, exec, s[4:5]
	s_cbranch_vccnz .LBB0_28
	s_mul_i32 s5, s16, 0xa10000
	s_mul_hi_i32 s4, s16, 0xa10000
	s_add_u32 s18, s6, s5
	s_addc_u32 s19, s7, s4
	s_mul_i32 s5, s16, 0x580000
	s_mul_hi_i32 s4, s16, 0x580000
	s_add_u32 s5, s86, s5
	s_addc_u32 s17, s87, s4
	s_mul_i32 s4, s16, 0xffffe200
	s_add_i32 s4, s28, s4
	s_and_b32 s4, s4, 0xfc0
	s_add_i32 s14, s4, 0xfffffa00
	s_mul_i32 s4, s16, 0xfffe2000
	s_add_i32 s4, s26, s4
	s_and_b32 s82, s4, 0x3e0
	s_lshl_b32 s82, s82, 2
	s_add_u32 s18, s18, s82
	v_or_b32_e32 v2, s14, v26
	s_addc_u32 s19, s19, 0
	v_mov_b32_e32 v7, v3
	v_lshl_add_u64 v[8:9], s[18:19], 0, v[6:7]
	v_mul_i32_i24_e32 v2, 0x2840, v2
	v_lshl_add_u64 v[8:9], v[8:9], 0, v[2:3]
	v_add_co_u32_e32 v10, vcc, s53, v8
	s_lshl_b64 s[18:19], s[14:15], 1
	s_nop 0
	v_addc_co_u32_e32 v11, vcc, 0, v9, vcc
	v_add_co_u32_e32 v12, vcc, s31, v8
	s_add_u32 s18, s5, s18
	s_nop 0
	v_addc_co_u32_e32 v13, vcc, 0, v9, vcc
	v_add_co_u32_e32 v14, vcc, s54, v8
	s_addc_u32 s19, s17, s19
	s_nop 0
	v_addc_co_u32_e32 v15, vcc, 0, v9, vcc
	v_add_co_u32_e32 v16, vcc, s55, v8
	s_and_b32 s5, s24, 0x300
	s_nop 0
	v_addc_co_u32_e32 v17, vcc, 0, v9, vcc
	v_add_co_u32_e32 v18, vcc, s56, v8
	s_and_b32 s14, s22, 0x80
	s_nop 0
	v_addc_co_u32_e32 v19, vcc, 0, v9, vcc
	v_add_co_u32_e32 v20, vcc, s57, v8
	s_and_b32 s4, s4, 0x60
	s_nop 0
	v_addc_co_u32_e32 v21, vcc, 0, v9, vcc
	v_add_co_u32_e32 v22, vcc, s58, v8
	s_or_b32 s5, s5, s14
	s_nop 0
	v_addc_co_u32_e32 v23, vcc, 0, v9, vcc
	v_add_co_u32_e32 v24, vcc, s33, v8
	s_addk_i32 s5, 0x700
	s_nop 0
	v_addc_co_u32_e32 v25, vcc, 0, v9, vcc
	global_load_dword v2, v[10:11], off offset:2112 nt
	global_load_dword v7, v[12:13], off offset:2240 nt
	global_load_dword v77, v[14:15], off offset:2368 nt
	global_load_dword v78, v[16:17], off offset:2496 nt
	global_load_dword v79, v[18:19], off offset:2624 nt
	global_load_dword v80, v[20:21], off offset:2752 nt
	global_load_dword v81, v[22:23], off offset:2880 nt
	global_load_dword v82, v[24:25], off offset:3008 nt
	v_add_co_u32_e32 v10, vcc, s60, v8
	s_nop 1
	v_addc_co_u32_e32 v11, vcc, 0, v9, vcc
	v_add_co_u32_e32 v12, vcc, s61, v8
	s_nop 1
	v_addc_co_u32_e32 v13, vcc, 0, v9, vcc
	v_add_co_u32_e32 v14, vcc, s62, v8
	s_nop 1
	v_addc_co_u32_e32 v15, vcc, 0, v9, vcc
	v_add_co_u32_e32 v16, vcc, s63, v8
	s_nop 1
	v_addc_co_u32_e32 v17, vcc, 0, v9, vcc
	v_add_co_u32_e32 v18, vcc, s64, v8
	s_nop 1
	v_addc_co_u32_e32 v19, vcc, 0, v9, vcc
	v_add_co_u32_e32 v20, vcc, s34, v8
	s_nop 1
	v_addc_co_u32_e32 v21, vcc, 0, v9, vcc
	v_add_co_u32_e32 v22, vcc, s65, v8
	s_nop 1
	v_addc_co_u32_e32 v23, vcc, 0, v9, vcc
	v_add_co_u32_e32 v24, vcc, s66, v8
	s_nop 1
	v_addc_co_u32_e32 v25, vcc, 0, v9, vcc
	global_load_dword v83, v[10:11], off offset:3136 nt
	global_load_dword v84, v[12:13], off offset:3264 nt
	global_load_dword v85, v[14:15], off offset:3392 nt
	global_load_dword v86, v[16:17], off offset:3520 nt
	global_load_dword v87, v[18:19], off offset:3648 nt
	global_load_dword v88, v[20:21], off offset:3776 nt
	global_load_dword v89, v[22:23], off offset:3904 nt
	global_load_dword v90, v[24:25], off offset:4032 nt
	v_add_co_u32_e32 v10, vcc, s67, v8
	s_nop 1
	v_addc_co_u32_e32 v11, vcc, 0, v9, vcc
	v_add_co_u32_e32 v12, vcc, s68, v8
	s_nop 1
	v_addc_co_u32_e32 v13, vcc, 0, v9, vcc
	v_add_co_u32_e32 v14, vcc, s69, v8
	s_nop 1
	v_addc_co_u32_e32 v15, vcc, 0, v9, vcc
	v_add_co_u32_e32 v16, vcc, s70, v8
	s_nop 1
	v_addc_co_u32_e32 v17, vcc, 0, v9, vcc
	v_add_co_u32_e32 v18, vcc, s35, v8
	s_nop 1
	v_addc_co_u32_e32 v19, vcc, 0, v9, vcc
	v_add_co_u32_e32 v20, vcc, s71, v8
	s_nop 1
	v_addc_co_u32_e32 v21, vcc, 0, v9, vcc
	v_add_co_u32_e32 v22, vcc, s72, v8
	s_nop 1
	v_addc_co_u32_e32 v23, vcc, 0, v9, vcc
	v_add_co_u32_e32 v24, vcc, s73, v8
	s_nop 1
	v_addc_co_u32_e32 v25, vcc, 0, v9, vcc
	global_load_dword v91, v[10:11], off offset:64 nt
	global_load_dword v92, v[12:13], off offset:192 nt
	global_load_dword v93, v[14:15], off offset:320 nt
	global_load_dword v94, v[16:17], off offset:448 nt
	global_load_dword v95, v[18:19], off offset:576 nt
	global_load_dword v96, v[20:21], off offset:704 nt
	global_load_dword v97, v[22:23], off offset:832 nt
	s_nop 0
	global_load_dword v24, v[24:25], off offset:960 nt
	v_add_co_u32_e32 v10, vcc, s74, v8
	s_nop 1
	v_addc_co_u32_e32 v11, vcc, 0, v9, vcc
	v_add_co_u32_e32 v12, vcc, s75, v8
	s_nop 1
	v_addc_co_u32_e32 v13, vcc, 0, v9, vcc
	v_add_co_u32_e32 v14, vcc, s38, v8
	s_nop 1
	v_addc_co_u32_e32 v15, vcc, 0, v9, vcc
	v_add_co_u32_e32 v16, vcc, s76, v8
	s_nop 1
	v_addc_co_u32_e32 v17, vcc, 0, v9, vcc
	v_add_co_u32_e32 v18, vcc, s77, v8
	s_nop 1
	v_addc_co_u32_e32 v19, vcc, 0, v9, vcc
	v_add_co_u32_e32 v20, vcc, s78, v8
	s_nop 1
	v_addc_co_u32_e32 v21, vcc, 0, v9, vcc
	v_add_co_u32_e32 v22, vcc, s79, v8
	s_nop 1
	v_addc_co_u32_e32 v23, vcc, 0, v9, vcc
	v_add_co_u32_e32 v8, vcc, s80, v8
	s_nop 1
	v_addc_co_u32_e32 v9, vcc, 0, v9, vcc
	global_load_dword v10, v[10:11], off offset:1088 nt
	s_nop 0
	global_load_dword v11, v[12:13], off offset:1216 nt
	s_nop 0
	global_load_dword v12, v[14:15], off offset:1344 nt
	global_load_dword v13, v[16:17], off offset:1472 nt
	s_nop 0
	global_load_dword v14, v[18:19], off offset:1600 nt
	global_load_dword v15, v[20:21], off offset:1728 nt
	global_load_dword v16, v[22:23], off offset:1856 nt
	s_nop 0
	global_load_dword v8, v[8:9], off offset:1984 nt
	s_waitcnt vmcnt(30)
	ds_write2_b32 v27, v2, v7 offset1:66
	s_waitcnt vmcnt(28)
	ds_write2_b32 v27, v77, v78 offset0:132 offset1:198
	s_waitcnt vmcnt(26)
	ds_write2_b32 v38, v79, v80 offset0:8 offset1:74
	s_waitcnt vmcnt(24)
	ds_write2_b32 v38, v81, v82 offset0:140 offset1:206
	s_waitcnt vmcnt(22)
	ds_write2_b32 v39, v83, v84 offset0:16 offset1:82
	s_waitcnt vmcnt(20)
	ds_write2_b32 v39, v85, v86 offset0:148 offset1:214
	s_waitcnt vmcnt(18)
	ds_write2_b32 v40, v87, v88 offset0:24 offset1:90
	s_waitcnt vmcnt(16)
	ds_write2_b32 v40, v89, v90 offset0:156 offset1:222
	s_waitcnt vmcnt(14)
	ds_write2_b32 v41, v91, v92 offset0:32 offset1:98
	s_waitcnt vmcnt(12)
	ds_write2_b32 v41, v93, v94 offset0:164 offset1:230
	s_waitcnt vmcnt(10)
	ds_write2_b32 v42, v95, v96 offset0:40 offset1:106
	s_waitcnt vmcnt(8)
	ds_write2_b32 v42, v97, v24 offset0:172 offset1:238
	s_waitcnt vmcnt(6)
	ds_write2_b32 v43, v10, v11 offset0:48 offset1:114
	s_waitcnt vmcnt(4)
	ds_write2_b32 v43, v12, v13 offset0:180 offset1:246
	s_waitcnt vmcnt(2)
	ds_write2_b32 v44, v14, v15 offset0:56 offset1:122
	s_waitcnt vmcnt(0)
	ds_write2_b32 v44, v16, v8 offset0:188 offset1:254
	s_waitcnt lgkmcnt(0)
	v_lshlrev_b32_e32 v2, 1, v4
	ds_read2_b32 v[12:13], v29 offset0:33 offset1:41
	ds_read2_b32 v[14:15], v29 offset1:8
	ds_read2_b32 v[16:17], v29 offset0:66 offset1:74
	ds_read2_b32 v[18:19], v29 offset0:99 offset1:107
	ds_read2_b32 v[20:21], v29 offset0:132 offset1:140
	ds_read2_b32 v[22:23], v29 offset0:165 offset1:173
	ds_read2_b32 v[24:25], v29 offset0:198 offset1:206
	ds_read2_b32 v[78:79], v29 offset0:231 offset1:239
	v_lshl_add_u64 v[80:81], s[18:19], 0, v[2:3]
	v_or_b32_e32 v2, s4, v28
	v_or_b32_e32 v2, s5, v2
	v_lshlrev_b32_e32 v2, 11, v2
	v_lshl_add_u64 v[82:83], v[80:81], 0, v[2:3]
	v_or_b32_e32 v2, s4, v30
	s_waitcnt lgkmcnt(6)
	v_cvt_pk_bf16_f32 v8, v14, v12
	s_waitcnt lgkmcnt(4)
	v_cvt_pk_bf16_f32 v9, v16, v18
	s_waitcnt lgkmcnt(2)
	v_cvt_pk_bf16_f32 v10, v20, v22
	s_waitcnt lgkmcnt(0)
	v_cvt_pk_bf16_f32 v11, v24, v78
	v_or_b32_e32 v2, s5, v2
	global_store_dwordx4 v[82:83], v[8:11], off sc1
	v_lshlrev_b32_e32 v2, 11, v2
	s_nop 0
	v_cvt_pk_bf16_f32 v8, v15, v13
	v_cvt_pk_bf16_f32 v9, v17, v19
	v_cvt_pk_bf16_f32 v10, v21, v23
	v_cvt_pk_bf16_f32 v11, v25, v79
	v_lshl_add_u64 v[12:13], v[80:81], 0, v[2:3]
	ds_read2_b32 v[14:15], v29 offset0:49 offset1:57
	ds_read2_b32 v[16:17], v29 offset0:16 offset1:24
	ds_read2_b32 v[18:19], v29 offset0:82 offset1:90
	ds_read2_b32 v[20:21], v29 offset0:115 offset1:123
	ds_read2_b32 v[22:23], v29 offset0:148 offset1:156
	ds_read2_b32 v[24:25], v29 offset0:181 offset1:189
	ds_read2_b32 v[78:79], v29 offset0:214 offset1:222
	ds_read2_b32 v[82:83], v29 offset0:247 offset1:255
	v_or_b32_e32 v2, s4, v31
	v_or_b32_e32 v2, s5, v2
	v_lshlrev_b32_e32 v2, 11, v2
	global_store_dwordx4 v[12:13], v[8:11], off sc1
	v_lshl_add_u64 v[12:13], v[80:81], 0, v[2:3]
	v_or_b32_e32 v2, s4, v32
	v_or_b32_e32 v2, s5, v2
	s_waitcnt lgkmcnt(6)
	v_cvt_pk_bf16_f32 v8, v16, v14
	s_waitcnt lgkmcnt(4)
	v_cvt_pk_bf16_f32 v9, v18, v20
	s_waitcnt lgkmcnt(2)
	v_cvt_pk_bf16_f32 v10, v22, v24
	s_waitcnt lgkmcnt(0)
	v_cvt_pk_bf16_f32 v11, v78, v82
	v_lshlrev_b32_e32 v2, 11, v2
	global_store_dwordx4 v[12:13], v[8:11], off sc1
	v_lshl_add_u64 v[12:13], v[80:81], 0, v[2:3]
	s_nop 0
	v_cvt_pk_bf16_f32 v8, v17, v15
	v_cvt_pk_bf16_f32 v9, v19, v21
	v_cvt_pk_bf16_f32 v10, v23, v25
	v_cvt_pk_bf16_f32 v11, v79, v83
	global_store_dwordx4 v[12:13], v[8:11], off sc1
	s_waitcnt lgkmcnt(0)

.LBB0_29:
	s_andn2_b64 vcc, exec, s[4:5]
	s_cbranch_vccnz .LBB0_8
	s_mul_i32 s5, s16, 0xa10000
	s_mul_hi_i32 s4, s16, 0xa10000
	s_add_u32 s17, s6, s5
	s_addc_u32 s19, s7, s4
	s_mul_i32 s5, s16, 0x580000
	s_mul_hi_i32 s4, s16, 0x580000
	s_add_u32 s18, s86, s5
	s_addc_u32 s14, s87, s4
	s_mul_i32 s4, s81, 0x2aab
	s_lshr_b32 s5, s4, 31
	s_ashr_i32 s4, s4, 19
	s_add_i32 s4, s4, s5
	s_mul_i32 s5, s4, 48
	s_sub_i32 s5, s81, s5
	s_sext_i32_i16 s5, s5
	s_lshl_b32 s16, s4, 6
	s_lshl_b32 s4, s5, 5
	s_ashr_i32 s5, s4, 31
	s_lshl_b64 s[82:83], s[4:5], 2
	v_or_b32_e32 v2, s16, v26
	s_add_u32 s82, s17, s82
	s_addc_u32 s83, s19, s83
	v_mov_b32_e32 v7, v3
	v_mul_i32_i24_e32 v10, 0x2840, v2
	v_mad_i32_i24 v12, v2, s52, v46
	v_mad_i32_i24 v14, v2, s52, v47
	v_mad_i32_i24 v16, v2, s52, v48
	v_mad_i32_i24 v18, v2, s52, v49
	v_mad_i32_i24 v20, v2, s52, v50
	v_mad_i32_i24 v22, v2, s52, v51
	v_mad_i32_i24 v24, v2, s52, v52
	v_mad_i32_i24 v78, v2, s52, v53
	v_mad_i32_i24 v80, v2, s52, v54
	v_mad_i32_i24 v82, v2, s52, v55
	v_mad_i32_i24 v84, v2, s52, v56
	v_mad_i32_i24 v86, v2, s52, v57
	v_mad_i32_i24 v88, v2, s52, v58
	v_mad_i32_i24 v90, v2, s52, v59
	v_mad_i32_i24 v92, v2, s52, v60
	v_mad_i32_i24 v94, v2, s52, v61
	v_mad_i32_i24 v96, v2, s52, v62
	v_mad_i32_i24 v98, v2, s52, v63
	v_mad_i32_i24 v100, v2, s52, v64
	v_mad_i32_i24 v102, v2, s52, v65
	v_mad_i32_i24 v104, v2, s52, v66
	v_mad_i32_i24 v106, v2, s52, v67
	v_mad_i32_i24 v108, v2, s52, v68
	v_mad_i32_i24 v110, v2, s52, v69
	v_mad_i32_i24 v112, v2, s52, v70
	v_mad_i32_i24 v114, v2, s52, v71
	v_mad_i32_i24 v116, v2, s52, v72
	v_mad_i32_i24 v118, v2, s52, v73
	v_mad_i32_i24 v120, v2, s52, v74
	v_mad_i32_i24 v122, v2, s52, v75
	v_mad_i32_i24 v124, v2, s52, v76
	v_lshl_add_u64 v[8:9], s[82:83], 0, v[6:7]
	v_ashrrev_i32_e32 v11, 31, v10
	v_ashrrev_i32_e32 v13, 31, v12
	v_ashrrev_i32_e32 v15, 31, v14
	v_ashrrev_i32_e32 v17, 31, v16
	v_ashrrev_i32_e32 v19, 31, v18
	v_ashrrev_i32_e32 v21, 31, v20
	v_ashrrev_i32_e32 v23, 31, v22
	v_ashrrev_i32_e32 v25, 31, v24
	v_ashrrev_i32_e32 v79, 31, v78
	v_ashrrev_i32_e32 v81, 31, v80
	v_ashrrev_i32_e32 v83, 31, v82
	v_ashrrev_i32_e32 v85, 31, v84
	v_ashrrev_i32_e32 v87, 31, v86
	v_ashrrev_i32_e32 v89, 31, v88
	v_ashrrev_i32_e32 v91, 31, v90
	v_ashrrev_i32_e32 v93, 31, v92
	v_ashrrev_i32_e32 v95, 31, v94
	v_ashrrev_i32_e32 v97, 31, v96
	v_ashrrev_i32_e32 v99, 31, v98
	v_ashrrev_i32_e32 v101, 31, v100
	v_ashrrev_i32_e32 v103, 31, v102
	v_ashrrev_i32_e32 v105, 31, v104
	v_ashrrev_i32_e32 v107, 31, v106
	v_ashrrev_i32_e32 v109, 31, v108
	v_ashrrev_i32_e32 v111, 31, v110
	v_ashrrev_i32_e32 v113, 31, v112
	v_ashrrev_i32_e32 v115, 31, v114
	v_ashrrev_i32_e32 v117, 31, v116
	v_ashrrev_i32_e32 v119, 31, v118
	v_ashrrev_i32_e32 v121, 31, v120
	v_ashrrev_i32_e32 v123, 31, v122
	v_ashrrev_i32_e32 v125, 31, v124
	v_lshl_add_u64 v[10:11], v[8:9], 0, v[10:11]
	v_lshl_add_u64 v[12:13], v[8:9], 0, v[12:13]
	v_lshl_add_u64 v[14:15], v[8:9], 0, v[14:15]
	v_lshl_add_u64 v[16:17], v[8:9], 0, v[16:17]
	v_lshl_add_u64 v[18:19], v[8:9], 0, v[18:19]
	v_lshl_add_u64 v[20:21], v[8:9], 0, v[20:21]
	v_lshl_add_u64 v[22:23], v[8:9], 0, v[22:23]
	v_lshl_add_u64 v[24:25], v[8:9], 0, v[24:25]
	v_lshl_add_u64 v[78:79], v[8:9], 0, v[78:79]
	v_lshl_add_u64 v[80:81], v[8:9], 0, v[80:81]
	v_lshl_add_u64 v[82:83], v[8:9], 0, v[82:83]
	v_lshl_add_u64 v[84:85], v[8:9], 0, v[84:85]
	v_lshl_add_u64 v[86:87], v[8:9], 0, v[86:87]
	v_lshl_add_u64 v[88:89], v[8:9], 0, v[88:89]
	v_lshl_add_u64 v[90:91], v[8:9], 0, v[90:91]
	v_lshl_add_u64 v[92:93], v[8:9], 0, v[92:93]
	v_lshl_add_u64 v[94:95], v[8:9], 0, v[94:95]
	v_lshl_add_u64 v[96:97], v[8:9], 0, v[96:97]
	v_lshl_add_u64 v[98:99], v[8:9], 0, v[98:99]
	v_lshl_add_u64 v[100:101], v[8:9], 0, v[100:101]
	v_lshl_add_u64 v[102:103], v[8:9], 0, v[102:103]
	v_lshl_add_u64 v[104:105], v[8:9], 0, v[104:105]
	v_lshl_add_u64 v[106:107], v[8:9], 0, v[106:107]
	v_lshl_add_u64 v[108:109], v[8:9], 0, v[108:109]
	v_lshl_add_u64 v[110:111], v[8:9], 0, v[110:111]
	v_lshl_add_u64 v[112:113], v[8:9], 0, v[112:113]
	v_lshl_add_u64 v[114:115], v[8:9], 0, v[114:115]
	v_lshl_add_u64 v[116:117], v[8:9], 0, v[116:117]
	v_lshl_add_u64 v[118:119], v[8:9], 0, v[118:119]
	v_lshl_add_u64 v[120:121], v[8:9], 0, v[120:121]
	v_lshl_add_u64 v[122:123], v[8:9], 0, v[122:123]
	v_lshl_add_u64 v[8:9], v[8:9], 0, v[124:125]
	global_load_dword v2, v[10:11], off nt
	global_load_dword v7, v[12:13], off nt
	s_nop 0
	global_load_dword v10, v[14:15], off nt
	global_load_dword v11, v[16:17], off nt
	global_load_dword v12, v[18:19], off nt
	global_load_dword v13, v[20:21], off nt
	s_nop 0
	global_load_dword v14, v[22:23], off nt
	global_load_dword v15, v[24:25], off nt
	global_load_dword v16, v[78:79], off nt
	global_load_dword v17, v[80:81], off nt
	global_load_dword v18, v[82:83], off nt
	global_load_dword v19, v[84:85], off nt
	global_load_dword v20, v[86:87], off nt
	global_load_dword v21, v[88:89], off nt
	global_load_dword v22, v[90:91], off nt
	global_load_dword v23, v[92:93], off nt
	global_load_dword v24, v[94:95], off nt
	global_load_dword v25, v[96:97], off nt
	global_load_dword v77, v[98:99], off nt
	global_load_dword v78, v[100:101], off nt
	global_load_dword v79, v[102:103], off nt
	global_load_dword v80, v[104:105], off nt
	global_load_dword v81, v[106:107], off nt
	global_load_dword v82, v[108:109], off nt
	global_load_dword v83, v[110:111], off nt
	global_load_dword v84, v[112:113], off nt
	global_load_dword v85, v[114:115], off nt
	global_load_dword v86, v[116:117], off nt
	global_load_dword v87, v[118:119], off nt
	global_load_dword v88, v[120:121], off nt
	global_load_dword v89, v[122:123], off nt
	s_nop 0
	global_load_dword v8, v[8:9], off nt
	s_waitcnt vmcnt(30)
	ds_write2_b32 v27, v2, v7 offset1:66
	s_waitcnt vmcnt(28)
	ds_write2_b32 v27, v10, v11 offset0:132 offset1:198
	s_waitcnt vmcnt(26)
	ds_write2_b32 v38, v12, v13 offset0:8 offset1:74
	s_waitcnt vmcnt(24)
	ds_write2_b32 v38, v14, v15 offset0:140 offset1:206
	s_waitcnt vmcnt(22)
	ds_write2_b32 v39, v16, v17 offset0:16 offset1:82
	s_waitcnt vmcnt(20)
	ds_write2_b32 v39, v18, v19 offset0:148 offset1:214
	s_waitcnt vmcnt(18)
	ds_write2_b32 v40, v20, v21 offset0:24 offset1:90
	s_waitcnt vmcnt(16)
	ds_write2_b32 v40, v22, v23 offset0:156 offset1:222
	s_waitcnt vmcnt(14)
	ds_write2_b32 v41, v24, v25 offset0:32 offset1:98
	s_waitcnt vmcnt(12)
	ds_write2_b32 v41, v77, v78 offset0:164 offset1:230
	s_waitcnt vmcnt(10)
	ds_write2_b32 v42, v79, v80 offset0:40 offset1:106
	s_waitcnt vmcnt(8)
	ds_write2_b32 v42, v81, v82 offset0:172 offset1:238
	s_waitcnt vmcnt(6)
	ds_write2_b32 v43, v83, v84 offset0:48 offset1:114
	s_waitcnt vmcnt(4)
	ds_write2_b32 v43, v85, v86 offset0:180 offset1:246
	s_waitcnt vmcnt(2)
	ds_write2_b32 v44, v87, v88 offset0:56 offset1:122
	s_waitcnt vmcnt(0)
	ds_write2_b32 v44, v89, v8 offset0:188 offset1:254
	s_waitcnt lgkmcnt(0)
	s_ashr_i32 s17, s16, 31
	ds_read2_b32 v[12:13], v29 offset0:33 offset1:41
	ds_read2_b32 v[14:15], v29 offset1:8
	ds_read2_b32 v[16:17], v29 offset0:66 offset1:74
	ds_read2_b32 v[18:19], v29 offset0:99 offset1:107
	ds_read2_b32 v[20:21], v29 offset0:132 offset1:140
	ds_read2_b32 v[22:23], v29 offset0:165 offset1:173
	ds_read2_b32 v[24:25], v29 offset0:198 offset1:206
	ds_read2_b32 v[78:79], v29 offset0:231 offset1:239
	s_lshl_b64 s[16:17], s[16:17], 1
	s_add_u32 s16, s18, s16
	v_or_b32_e32 v80, s4, v28
	s_addc_u32 s17, s14, s17
	v_lshlrev_b32_e32 v2, 1, v4
	v_ashrrev_i32_e32 v81, 31, v80
	v_lshlrev_b64 v[80:81], 11, v[80:81]
	v_lshl_add_u64 v[82:83], s[16:17], 0, v[2:3]
	s_waitcnt lgkmcnt(6)
	v_cvt_pk_bf16_f32 v8, v14, v12
	s_waitcnt lgkmcnt(4)
	v_cvt_pk_bf16_f32 v9, v16, v18
	s_waitcnt lgkmcnt(2)
	v_cvt_pk_bf16_f32 v10, v20, v22
	s_waitcnt lgkmcnt(0)
	v_cvt_pk_bf16_f32 v11, v24, v78
	v_lshl_add_u64 v[80:81], v[82:83], 0, v[80:81]
	v_or_b32_e32 v12, s4, v30
	global_store_dwordx4 v[80:81], v[8:11], off sc1
	s_nop 1
	v_cvt_pk_bf16_f32 v8, v15, v13
	v_ashrrev_i32_e32 v13, 31, v12
	v_cvt_pk_bf16_f32 v9, v17, v19
	v_cvt_pk_bf16_f32 v10, v21, v23
	v_cvt_pk_bf16_f32 v11, v25, v79
	ds_read2_b32 v[14:15], v29 offset0:49 offset1:57
	ds_read2_b32 v[16:17], v29 offset0:16 offset1:24
	ds_read2_b32 v[18:19], v29 offset0:82 offset1:90
	ds_read2_b32 v[20:21], v29 offset0:115 offset1:123
	v_lshlrev_b64 v[12:13], 11, v[12:13]
	ds_read2_b32 v[22:23], v29 offset0:148 offset1:156
	ds_read2_b32 v[24:25], v29 offset0:181 offset1:189
	ds_read2_b32 v[78:79], v29 offset0:214 offset1:222
	ds_read2_b32 v[80:81], v29 offset0:247 offset1:255
	v_lshl_add_u64 v[12:13], v[82:83], 0, v[12:13]
	global_store_dwordx4 v[12:13], v[8:11], off sc1
	v_or_b32_e32 v12, s4, v31
	v_ashrrev_i32_e32 v13, 31, v12
	v_lshlrev_b64 v[12:13], 11, v[12:13]
	s_waitcnt lgkmcnt(6)
	v_cvt_pk_bf16_f32 v8, v16, v14
	s_waitcnt lgkmcnt(4)
	v_cvt_pk_bf16_f32 v9, v18, v20
	s_waitcnt lgkmcnt(2)
	v_cvt_pk_bf16_f32 v10, v22, v24
	s_waitcnt lgkmcnt(0)
	v_cvt_pk_bf16_f32 v11, v78, v80
	v_lshl_add_u64 v[12:13], v[82:83], 0, v[12:13]
	global_store_dwordx4 v[12:13], v[8:11], off sc1
	v_or_b32_e32 v12, s4, v32
	v_ashrrev_i32_e32 v13, 31, v12
	v_lshlrev_b64 v[12:13], 11, v[12:13]
	v_cvt_pk_bf16_f32 v8, v17, v15
	v_cvt_pk_bf16_f32 v9, v19, v21
	v_cvt_pk_bf16_f32 v10, v23, v25
	v_cvt_pk_bf16_f32 v11, v79, v81
	v_lshl_add_u64 v[12:13], v[82:83], 0, v[12:13]
	global_store_dwordx4 v[12:13], v[8:11], off sc1
	s_waitcnt lgkmcnt(0)
	s_branch .LBB0_8

.LBB0_33:
	v_ashrrev_i32_e32 v12, 15, v14
	v_bfe_u32 v15, v14, 7, 8
	v_add_u32_e32 v14, s63, v14
	v_mad_i64_i32 v[16:17], s[38:39], v12, s25, v[4:5]
	v_mul_hi_i32_i24_e32 v19, 0x580000, v12
	v_mul_i32_i24_e32 v18, 0x580000, v12
	v_cmp_lt_i32_e32 vcc, s36, v14
	v_lshl_add_u64 v[16:17], v[16:17], 0, v[6:7]
	v_lshl_add_u64 v[144:145], s[86:87], 0, v[18:19]
	s_or_b64 s[8:9], vcc, s[8:9]
	v_add_co_u32_e32 v18, vcc, s26, v16
	v_ashrrev_i32_e32 v13, 31, v12
	s_nop 0
	v_addc_co_u32_e32 v19, vcc, 0, v17, vcc
	v_add_co_u32_e32 v20, vcc, s29, v16
	v_lshl_add_u64 v[40:41], v[16:17], 0, s[6:7]
	s_nop 0
	v_addc_co_u32_e32 v21, vcc, 0, v17, vcc
	v_add_co_u32_e32 v48, vcc, s30, v16
	v_lshl_add_u64 v[44:45], v[16:17], 0, s[10:11]
	s_nop 0
	v_addc_co_u32_e32 v49, vcc, 0, v17, vcc
	v_add_co_u32_e32 v64, vcc, s31, v16
	v_lshl_add_u64 v[60:61], v[16:17], 0, s[12:13]
	s_nop 0
	v_addc_co_u32_e32 v65, vcc, 0, v17, vcc
	v_add_co_u32_e32 v80, vcc, s33, v16
	v_lshl_add_u64 v[76:77], v[16:17], 0, s[14:15]
	s_nop 0
	v_addc_co_u32_e32 v81, vcc, 0, v17, vcc
	v_add_co_u32_e32 v96, vcc, s34, v16
	v_lshl_add_u64 v[92:93], v[16:17], 0, s[16:17]
	s_nop 0
	v_addc_co_u32_e32 v97, vcc, 0, v17, vcc
	v_add_co_u32_e32 v112, vcc, s24, v16
	v_lshl_add_u64 v[108:109], v[16:17], 0, s[18:19]
	s_nop 0
	v_addc_co_u32_e32 v113, vcc, 0, v17, vcc
	v_add_co_u32_e32 v128, vcc, s35, v16
	v_lshl_add_u64 v[124:125], v[16:17], 0, s[20:21]
	v_lshl_add_u64 v[140:141], v[16:17], 0, s[22:23]
	v_addc_co_u32_e32 v129, vcc, 0, v17, vcc
	global_load_dwordx4 v[16:19], v[18:19], off offset:2048
	s_nop 0
	global_load_dwordx4 v[20:23], v[20:21], off offset:64
	s_nop 0
	global_load_dwordx4 v[24:27], v[40:41], off offset:16
	global_load_dwordx4 v[28:31], v[44:45], off offset:16
	global_load_dwordx4 v[32:35], v[40:41], off offset:32
	global_load_dwordx4 v[36:39], v[44:45], off offset:32
	v_lshlrev_b64 v[12:13], 14, v[12:13]
	global_load_dwordx4 v[40:43], v[40:41], off offset:48
	s_nop 0
	global_load_dwordx4 v[44:47], v[44:45], off offset:48
	s_nop 0
	global_load_dwordx4 v[48:51], v[48:49], off offset:2176
	s_nop 0
	global_load_dwordx4 v[52:55], v[60:61], off offset:48
	global_load_dwordx4 v[56:59], v[60:61], off offset:16
	s_nop 0
	global_load_dwordx4 v[60:63], v[60:61], off offset:32
	s_nop 0
	global_load_dwordx4 v[64:67], v[64:65], off offset:192
	s_nop 0
	global_load_dwordx4 v[68:71], v[76:77], off offset:48
	global_load_dwordx4 v[72:75], v[76:77], off offset:16
	s_nop 0
	global_load_dwordx4 v[76:79], v[76:77], off offset:32
	s_nop 0
	global_load_dwordx4 v[80:83], v[80:81], off offset:2304
	s_nop 0
	global_load_dwordx4 v[84:87], v[92:93], off offset:48
	global_load_dwordx4 v[88:91], v[92:93], off offset:16
	s_nop 0
	global_load_dwordx4 v[92:95], v[92:93], off offset:32
	s_nop 0
	global_load_dwordx4 v[96:99], v[96:97], off offset:320
	s_nop 0
	global_load_dwordx4 v[100:103], v[108:109], off offset:48
	global_load_dwordx4 v[104:107], v[108:109], off offset:16
	s_nop 0
	global_load_dwordx4 v[108:111], v[108:109], off offset:32
	s_nop 0
	global_load_dwordx4 v[112:115], v[112:113], off offset:2432
	s_nop 0
	global_load_dwordx4 v[116:119], v[124:125], off offset:48
	global_load_dwordx4 v[120:123], v[124:125], off offset:16
	s_nop 0
	global_load_dwordx4 v[124:127], v[124:125], off offset:32
	s_nop 0
	global_load_dwordx4 v[128:131], v[128:129], off offset:448
	s_nop 0
	global_load_dwordx4 v[132:135], v[140:141], off offset:48
	global_load_dwordx4 v[136:139], v[140:141], off offset:16
	s_nop 0
	global_load_dwordx4 v[140:143], v[140:141], off offset:32
	v_lshlrev_b32_e32 v2, 2, v15
	v_lshl_add_u64 v[12:13], s[0:1], 0, v[12:13]
	v_lshl_add_u64 v[12:13], v[12:13], 0, v[2:3]
	global_load_dword v146, v[12:13], off
	global_load_dword v148, v[12:13], off offset:1024
	global_load_dword v150, v[12:13], off offset:2048
	global_load_dword v152, v[12:13], off offset:3072
	v_add_co_u32_e32 v154, vcc, s26, v12
	v_lshlrev_b32_e32 v2, 11, v15
	s_nop 0
	v_addc_co_u32_e32 v155, vcc, 0, v13, vcc
	v_add_co_u32_e32 v156, vcc, s27, v12
	v_lshl_add_u64 v[144:145], v[144:145], 0, v[2:3]
	s_nop 0
	v_addc_co_u32_e32 v157, vcc, 0, v13, vcc
	global_load_dword v2, v[154:155], off offset:1024
	global_load_dword v158, v[154:155], off offset:2048
	s_nop 0
	global_load_dword v154, v[154:155], off offset:3072
	s_nop 0
	global_load_dword v160, v[156:157], off offset:-4096
	global_load_dword v162, v[156:157], off
	global_load_dword v164, v[156:157], off offset:1024
	global_load_dword v166, v[156:157], off offset:2048
	s_nop 0
	global_load_dword v156, v[156:157], off offset:3072
	v_add_co_u32_e32 v12, vcc, s28, v12
	v_lshl_add_u64 v[144:145], v[144:145], 0, v[10:11]
	s_nop 0
	v_addc_co_u32_e32 v13, vcc, 0, v13, vcc
	global_load_dword v168, v[12:13], off
	global_load_dword v170, v[12:13], off offset:1024
	global_load_dword v172, v[12:13], off offset:2048
	s_nop 0
	global_load_dword v12, v[12:13], off offset:3072
	v_add_co_u32_e32 v144, vcc, 0x300000, v144
	s_waitcnt vmcnt(47)
	v_mov_b32_e32 v174, v16
	s_waitcnt vmcnt(46)
	v_mov_b32_e32 v175, v20
	v_mov_b32_e32 v20, v17
	v_mov_b32_e32 v16, v18
	v_mov_b32_e32 v17, v22
	v_mov_b32_e32 v22, v19
	s_waitcnt vmcnt(45)
	v_mov_b32_e32 v18, v24
	s_waitcnt vmcnt(44)
	v_mov_b32_e32 v19, v28
	v_mov_b32_e32 v28, v25
	v_mov_b32_e32 v24, v26
	v_mov_b32_e32 v25, v30
	v_mov_b32_e32 v30, v27
	s_waitcnt vmcnt(43)
	v_mov_b32_e32 v26, v32
	s_waitcnt vmcnt(42)
	v_mov_b32_e32 v27, v36
	v_mov_b32_e32 v36, v33
	v_mov_b32_e32 v32, v34
	v_mov_b32_e32 v33, v38
	v_mov_b32_e32 v38, v35
	s_waitcnt vmcnt(41)
	v_mov_b32_e32 v34, v40
	s_waitcnt vmcnt(40)
	v_mov_b32_e32 v35, v44
	v_mov_b32_e32 v44, v41
	v_mov_b32_e32 v40, v42
	v_mov_b32_e32 v41, v46
	v_mov_b32_e32 v46, v43
	s_waitcnt vmcnt(39)
	v_mov_b32_e32 v42, v48
	s_waitcnt vmcnt(35)
	v_mov_b32_e32 v43, v64
	v_mov_b32_e32 v64, v49
	v_mov_b32_e32 v48, v50
	v_mov_b32_e32 v49, v66
	v_mov_b32_e32 v66, v51
	v_mov_b32_e32 v50, v56
	s_waitcnt vmcnt(33)
	v_mov_b32_e32 v51, v72
	v_mov_b32_e32 v72, v57
	v_mov_b32_e32 v56, v58
	v_mov_b32_e32 v57, v74
	v_mov_b32_e32 v74, v59
	v_mov_b32_e32 v58, v60
	s_waitcnt vmcnt(32)
	v_mov_b32_e32 v59, v76
	v_mov_b32_e32 v76, v61
	v_mov_b32_e32 v60, v62
	v_mov_b32_e32 v61, v78
	v_mov_b32_e32 v78, v63
	v_mov_b32_e32 v62, v52
	v_mov_b32_e32 v63, v68
	v_mov_b32_e32 v68, v53
	v_mov_b32_e32 v52, v54
	v_mov_b32_e32 v53, v70
	v_mov_b32_e32 v70, v55
	s_waitcnt vmcnt(31)
	v_mov_b32_e32 v54, v80
	s_waitcnt vmcnt(27)
	v_mov_b32_e32 v55, v96
	v_mov_b32_e32 v96, v81
	v_mov_b32_e32 v80, v82
	v_mov_b32_e32 v81, v98
	v_mov_b32_e32 v98, v83
	v_mov_b32_e32 v82, v88
	s_waitcnt vmcnt(25)
	v_mov_b32_e32 v83, v104
	v_mov_b32_e32 v104, v89
	v_mov_b32_e32 v88, v90
	v_mov_b32_e32 v89, v106
	v_mov_b32_e32 v106, v91
	v_mov_b32_e32 v90, v92
	s_waitcnt vmcnt(24)
	v_mov_b32_e32 v91, v108
	v_mov_b32_e32 v108, v93
	v_mov_b32_e32 v92, v94
	v_mov_b32_e32 v93, v110
	v_mov_b32_e32 v110, v95
	v_mov_b32_e32 v94, v84
	v_mov_b32_e32 v95, v100
	v_mov_b32_e32 v100, v85
	v_mov_b32_e32 v84, v86
	v_mov_b32_e32 v85, v102
	v_mov_b32_e32 v102, v87
	s_waitcnt vmcnt(23)
	v_mov_b32_e32 v86, v112
	s_waitcnt vmcnt(19)
	v_mov_b32_e32 v87, v128
	v_mov_b32_e32 v128, v113
	v_mov_b32_e32 v112, v114
	v_mov_b32_e32 v113, v130
	v_mov_b32_e32 v130, v115
	v_mov_b32_e32 v114, v120
	s_waitcnt vmcnt(17)
	v_mov_b32_e32 v115, v136
	v_mov_b32_e32 v136, v121
	v_mov_b32_e32 v120, v122
	v_mov_b32_e32 v121, v138
	v_mov_b32_e32 v138, v123
	v_mov_b32_e32 v122, v124
	s_waitcnt vmcnt(16)
	v_mov_b32_e32 v123, v140
	v_mov_b32_e32 v140, v125
	v_mov_b32_e32 v124, v126
	v_mov_b32_e32 v125, v142
	v_mov_b32_e32 v142, v127
	v_mov_b32_e32 v126, v116
	v_mov_b32_e32 v127, v132
	v_mov_b32_e32 v132, v117
	v_mov_b32_e32 v116, v118
	v_mov_b32_e32 v117, v134
	v_mov_b32_e32 v134, v119
	s_waitcnt vmcnt(15)
	v_pk_fma_f32 v[118:119], v[146:147], v[174:175], 0 op_sel_hi:[0,1,0]
	v_pk_fma_f32 v[42:43], v[146:147], v[42:43], 0 op_sel_hi:[0,1,0]
	v_pk_fma_f32 v[54:55], v[146:147], v[54:55], 0 op_sel_hi:[0,1,0]
	v_pk_fma_f32 v[86:87], v[146:147], v[86:87], 0 op_sel_hi:[0,1,0]
	s_waitcnt vmcnt(14)
	v_pk_fma_f32 v[20:21], v[148:149], v[20:21], v[118:119] op_sel_hi:[0,1,1]
	v_pk_fma_f32 v[42:43], v[148:149], v[64:65], v[42:43] op_sel_hi:[0,1,1]
	v_pk_fma_f32 v[54:55], v[148:149], v[96:97], v[54:55] op_sel_hi:[0,1,1]
	v_pk_fma_f32 v[64:65], v[148:149], v[128:129], v[86:87] op_sel_hi:[0,1,1]
	s_waitcnt vmcnt(13)
	v_pk_fma_f32 v[16:17], v[150:151], v[16:17], v[20:21] op_sel_hi:[0,1,1]
	v_pk_fma_f32 v[20:21], v[150:151], v[48:49], v[42:43] op_sel_hi:[0,1,1]
	v_pk_fma_f32 v[42:43], v[150:151], v[80:81], v[54:55] op_sel_hi:[0,1,1]
	v_pk_fma_f32 v[48:49], v[150:151], v[112:113], v[64:65] op_sel_hi:[0,1,1]
	s_waitcnt vmcnt(12)
	v_pk_fma_f32 v[16:17], v[152:153], v[22:23], v[16:17] op_sel_hi:[0,1,1]
	v_pk_fma_f32 v[20:21], v[152:153], v[66:67], v[20:21] op_sel_hi:[0,1,1]
	v_pk_fma_f32 v[22:23], v[152:153], v[98:99], v[42:43] op_sel_hi:[0,1,1]
	v_pk_fma_f32 v[42:43], v[152:153], v[130:131], v[48:49] op_sel_hi:[0,1,1]
	s_waitcnt vmcnt(8)
	v_pk_fma_f32 v[16:17], v[160:161], v[18:19], v[16:17] op_sel_hi:[0,1,1]
	v_pk_fma_f32 v[18:19], v[160:161], v[50:51], v[20:21] op_sel_hi:[0,1,1]
	v_pk_fma_f32 v[20:21], v[160:161], v[82:83], v[22:23] op_sel_hi:[0,1,1]
	v_pk_fma_f32 v[22:23], v[160:161], v[114:115], v[42:43] op_sel_hi:[0,1,1]
	v_pk_fma_f32 v[16:17], v[2:3], v[28:29], v[16:17] op_sel_hi:[0,1,1]
	v_pk_fma_f32 v[18:19], v[2:3], v[72:73], v[18:19] op_sel_hi:[0,1,1]
	v_pk_fma_f32 v[20:21], v[2:3], v[104:105], v[20:21] op_sel_hi:[0,1,1]
	v_pk_fma_f32 v[22:23], v[2:3], v[136:137], v[22:23] op_sel_hi:[0,1,1]
	v_pk_fma_f32 v[16:17], v[158:159], v[24:25], v[16:17] op_sel_hi:[0,1,1]
	v_pk_fma_f32 v[18:19], v[158:159], v[56:57], v[18:19] op_sel_hi:[0,1,1]
	v_pk_fma_f32 v[20:21], v[158:159], v[88:89], v[20:21] op_sel_hi:[0,1,1]
	v_pk_fma_f32 v[22:23], v[158:159], v[120:121], v[22:23] op_sel_hi:[0,1,1]
	v_pk_fma_f32 v[16:17], v[154:155], v[30:31], v[16:17] op_sel_hi:[0,1,1]
	v_pk_fma_f32 v[18:19], v[154:155], v[74:75], v[18:19] op_sel_hi:[0,1,1]
	v_pk_fma_f32 v[20:21], v[154:155], v[106:107], v[20:21] op_sel_hi:[0,1,1]
	v_pk_fma_f32 v[22:23], v[154:155], v[138:139], v[22:23] op_sel_hi:[0,1,1]
	s_waitcnt vmcnt(7)
	v_pk_fma_f32 v[16:17], v[162:163], v[26:27], v[16:17] op_sel_hi:[0,1,1]
	v_pk_fma_f32 v[18:19], v[162:163], v[58:59], v[18:19] op_sel_hi:[0,1,1]
	v_pk_fma_f32 v[20:21], v[162:163], v[90:91], v[20:21] op_sel_hi:[0,1,1]
	v_pk_fma_f32 v[22:23], v[162:163], v[122:123], v[22:23] op_sel_hi:[0,1,1]
	s_waitcnt vmcnt(6)
	v_pk_fma_f32 v[16:17], v[164:165], v[36:37], v[16:17] op_sel_hi:[0,1,1]
	v_pk_fma_f32 v[18:19], v[164:165], v[76:77], v[18:19] op_sel_hi:[0,1,1]
	v_pk_fma_f32 v[20:21], v[164:165], v[108:109], v[20:21] op_sel_hi:[0,1,1]
	v_pk_fma_f32 v[22:23], v[164:165], v[140:141], v[22:23] op_sel_hi:[0,1,1]
	s_waitcnt vmcnt(5)
	v_pk_fma_f32 v[16:17], v[166:167], v[32:33], v[16:17] op_sel_hi:[0,1,1]
	v_pk_fma_f32 v[18:19], v[166:167], v[60:61], v[18:19] op_sel_hi:[0,1,1]
	v_pk_fma_f32 v[20:21], v[166:167], v[92:93], v[20:21] op_sel_hi:[0,1,1]
	v_pk_fma_f32 v[22:23], v[166:167], v[124:125], v[22:23] op_sel_hi:[0,1,1]
	s_waitcnt vmcnt(4)
	v_pk_fma_f32 v[16:17], v[156:157], v[38:39], v[16:17] op_sel_hi:[0,1,1]
	v_pk_fma_f32 v[18:19], v[156:157], v[78:79], v[18:19] op_sel_hi:[0,1,1]
	v_pk_fma_f32 v[20:21], v[156:157], v[110:111], v[20:21] op_sel_hi:[0,1,1]
	v_pk_fma_f32 v[22:23], v[156:157], v[142:143], v[22:23] op_sel_hi:[0,1,1]
	s_waitcnt vmcnt(3)
	v_pk_fma_f32 v[16:17], v[168:169], v[34:35], v[16:17] op_sel_hi:[0,1,1]
	v_pk_fma_f32 v[18:19], v[168:169], v[62:63], v[18:19] op_sel_hi:[0,1,1]
	v_pk_fma_f32 v[20:21], v[168:169], v[94:95], v[20:21] op_sel_hi:[0,1,1]
	v_pk_fma_f32 v[22:23], v[168:169], v[126:127], v[22:23] op_sel_hi:[0,1,1]
	s_waitcnt vmcnt(2)
	v_pk_fma_f32 v[16:17], v[170:171], v[44:45], v[16:17] op_sel_hi:[0,1,1]
	v_pk_fma_f32 v[18:19], v[170:171], v[68:69], v[18:19] op_sel_hi:[0,1,1]
	v_pk_fma_f32 v[20:21], v[170:171], v[100:101], v[20:21] op_sel_hi:[0,1,1]
	v_pk_fma_f32 v[22:23], v[170:171], v[132:133], v[22:23] op_sel_hi:[0,1,1]
	s_waitcnt vmcnt(1)
	v_pk_fma_f32 v[16:17], v[172:173], v[40:41], v[16:17] op_sel_hi:[0,1,1]
	v_pk_fma_f32 v[18:19], v[172:173], v[52:53], v[18:19] op_sel_hi:[0,1,1]
	v_pk_fma_f32 v[20:21], v[172:173], v[84:85], v[20:21] op_sel_hi:[0,1,1]
	v_pk_fma_f32 v[22:23], v[172:173], v[116:117], v[22:23] op_sel_hi:[0,1,1]
	s_waitcnt vmcnt(0)
	v_pk_fma_f32 v[16:17], v[12:13], v[46:47], v[16:17] op_sel_hi:[0,1,1]
	v_pk_fma_f32 v[18:19], v[12:13], v[70:71], v[18:19] op_sel_hi:[0,1,1]
	v_pk_fma_f32 v[20:21], v[12:13], v[102:103], v[20:21] op_sel_hi:[0,1,1]
	v_pk_fma_f32 v[12:13], v[12:13], v[134:135], v[22:23] op_sel_hi:[0,1,1]
	v_addc_co_u32_e32 v145, vcc, 0, v145, vcc
	v_cvt_pk_bf16_f32 v16, v16, v17
	v_cvt_pk_bf16_f32 v17, v18, v19
	v_cvt_pk_bf16_f32 v18, v20, v21
	v_cvt_pk_bf16_f32 v19, v12, v13
	global_store_dwordx4 v[144:145], v[16:19], off sc1
	s_andn2_b64 exec, exec, s[8:9]
	s_cbranch_execnz .LBB0_33

.LBB0_36:
	s_or_b64 exec, exec, s[4:5]
	s_waitcnt vmcnt(0)
	v_bfe_u32 v10, v19, 16, 1
	v_add3_u32 v10, v19, v10, s18
	v_and_b32_e32 v10, 0xffff0000, v10
	v_sub_f32_e32 v26, v19, v10
	v_bfe_u32 v10, v16, 16, 1
	v_add3_u32 v10, v16, v10, s18
	v_and_b32_e32 v10, 0xffff0000, v10
	v_sub_f32_e32 v27, v16, v10
	v_bfe_u32 v10, v17, 16, 1
	v_add3_u32 v10, v17, v10, s18
	v_and_b32_e32 v10, 0xffff0000, v10
	v_sub_f32_e32 v28, v17, v10
	v_bfe_u32 v10, v15, 16, 1
	v_add3_u32 v10, v15, v10, s18
	v_and_b32_e32 v10, 0xffff0000, v10
	v_sub_f32_e32 v29, v15, v10
	v_bfe_u32 v10, v5, 16, 1
	v_add3_u32 v10, v5, v10, s18
	v_and_b32_e32 v10, 0xffff0000, v10
	v_sub_f32_e32 v30, v5, v10
	v_bfe_u32 v10, v21, 16, 1
	v_add3_u32 v10, v21, v10, s18
	v_bfe_u32 v6, v20, 16, 1
	v_and_b32_e32 v10, 0xffff0000, v10
	v_add3_u32 v6, v20, v6, s18
	v_sub_f32_e32 v31, v21, v10
	v_mad_i32_i24 v10, v4, s19, v2
	v_and_b32_e32 v6, 0xffff0000, v6
	v_ashrrev_i32_e32 v11, 31, v10
	v_sub_f32_e32 v7, v20, v6
	v_bfe_u32 v6, v18, 16, 1
	v_cvt_pk_bf16_f32 v22, v15, v5
	v_lshlrev_b64 v[4:5], 11, v[10:11]
	v_readlane_b32 s4, v255, 26
	v_add_u32_e32 v10, 48, v10
	v_add3_u32 v6, v18, v6, s18
	v_readlane_b32 s5, v255, 27
	v_ashrrev_i32_e32 v11, 31, v10
	v_and_b32_e32 v6, 0xffff0000, v6
	v_lshl_add_u64 v[4:5], s[4:5], 0, v[4:5]
	v_lshlrev_b32_e32 v2, 1, v14
	v_lshlrev_b64 v[10:11], 11, v[10:11]
	v_add_u32_e32 v13, s63, v13
	v_sub_f32_e32 v6, v18, v6
	v_cvt_pk_bf16_f32 v23, v16, v17
	v_cvt_pk_bf16_f32 v24, v18, v19
	v_cvt_pk_bf16_f32 v25, v20, v21
	v_lshl_add_u64 v[4:5], v[4:5], 0, v[2:3]
	v_lshl_add_u64 v[10:11], s[4:5], 0, v[10:11]
	v_cmp_lt_i32_e32 vcc, s20, v13
	global_store_dwordx4 v[4:5], v[22:25], off sc1
	v_cvt_pk_bf16_f32 v4, v29, v30
	v_cvt_pk_bf16_f32 v5, v27, v28
	v_cvt_pk_bf16_f32 v6, v6, v26
	v_cvt_pk_bf16_f32 v7, v7, v31
	v_lshl_add_u64 v[10:11], v[10:11], 0, v[2:3]
	s_or_b64 s[10:11], vcc, s[10:11]
	v_add_u32_e32 v12, s16, v12
	global_store_dwordx4 v[10:11], v[4:7], off sc1
	s_andn2_b64 exec, exec, s[10:11]
	s_cbranch_execz .LBB0_85

.LBB0_110:
	s_add_i32 s30, s29, s3
	s_lshl_b64 s[20:21], s[8:9], 2
	s_add_u32 s18, s18, s20
	s_addc_u32 s19, s19, s21
	v_lshl_add_u64 v[22:23], s[18:19], 0, v[2:3]
	s_ashr_i32 s18, s30, 31
	s_mul_i32 s31, s16, s18
	s_mul_hi_u32 s18, s16, s30
	s_add_i32 s18, s18, s31
	s_mul_i32 s19, s17, s30
	s_add_i32 s19, s18, s19
	s_mul_i32 s18, s16, s30
	v_lshl_add_u64 v[24:25], s[18:19], 2, v[22:23]
	s_lshl_b64 s[18:19], s[16:17], 2
	v_lshl_add_u64 v[26:27], v[24:25], 0, s[18:19]
	global_load_dword v30, v[26:27], off nt
	s_or_b32 s20, s30, 2
	s_mul_hi_u32 s21, s16, s20
	s_add_i32 s21, s21, s31
	s_mul_i32 s33, s17, s20
	s_add_i32 s21, s21, s33
	s_mul_i32 s20, s16, s20
	v_lshl_add_u64 v[28:29], s[20:21], 2, v[22:23]
	global_load_dword v31, v[28:29], off nt
	global_load_dword v32, v[24:25], off nt
	global_load_dword v33, v[24:25], off offset:256 nt
	global_load_dword v34, v[24:25], off offset:512 nt
	global_load_dword v35, v[24:25], off offset:768 nt
	global_load_dword v36, v[24:25], off offset:1024 nt
	global_load_dword v37, v[24:25], off offset:1280 nt
	global_load_dword v38, v[24:25], off offset:1536 nt
	global_load_dword v39, v[24:25], off offset:1792 nt
	v_lshl_add_u64 v[24:25], v[28:29], 0, s[18:19]
	global_load_dword v40, v[24:25], off nt
	global_load_dword v41, v[28:29], off offset:256 nt
	global_load_dword v42, v[26:27], off offset:256 nt
	global_load_dword v43, v[26:27], off offset:512 nt
	global_load_dword v44, v[26:27], off offset:768 nt
	global_load_dword v45, v[26:27], off offset:1024 nt
	global_load_dword v46, v[26:27], off offset:1280 nt
	global_load_dword v47, v[26:27], off offset:1536 nt
	global_load_dword v48, v[26:27], off offset:1792 nt
	global_load_dword v49, v[24:25], off offset:256 nt
	global_load_dword v50, v[28:29], off offset:512 nt
	global_load_dword v51, v[28:29], off offset:768 nt
	global_load_dword v52, v[28:29], off offset:1024 nt
	global_load_dword v53, v[28:29], off offset:1280 nt
	global_load_dword v54, v[28:29], off offset:1536 nt
	s_nop 0
	global_load_dword v29, v[28:29], off offset:1792 nt
	s_nop 0
	global_load_dword v28, v[24:25], off offset:512 nt
	global_load_dword v55, v[24:25], off offset:768 nt
	global_load_dword v56, v[24:25], off offset:1024 nt
	global_load_dword v57, v[24:25], off offset:1280 nt
	global_load_dword v58, v[24:25], off offset:1536 nt
	global_load_dword v59, v[24:25], off offset:1792 nt
	s_or_b32 s20, s30, 4
	s_mul_hi_u32 s21, s16, s20
	s_add_i32 s21, s21, s31
	s_mul_i32 s33, s17, s20
	s_add_i32 s21, s21, s33
	s_mul_i32 s20, s16, s20
	v_lshl_add_u64 v[24:25], s[20:21], 2, v[22:23]
	s_or_b32 s20, s30, 6
	v_lshl_add_u64 v[26:27], v[24:25], 0, s[18:19]
	global_load_dword v60, v[24:25], off nt
	global_load_dword v61, v[24:25], off offset:256 nt
	global_load_dword v62, v[24:25], off offset:512 nt
	global_load_dword v63, v[24:25], off offset:768 nt
	global_load_dword v64, v[24:25], off offset:1024 nt
	global_load_dword v65, v[24:25], off offset:1280 nt
	global_load_dword v66, v[24:25], off offset:1536 nt
	global_load_dword v67, v[24:25], off offset:1792 nt
	global_load_dword v68, v[26:27], off nt
	global_load_dword v69, v[26:27], off offset:256 nt
	global_load_dword v70, v[26:27], off offset:512 nt
	global_load_dword v71, v[26:27], off offset:768 nt
	global_load_dword v72, v[26:27], off offset:1024 nt
	global_load_dword v73, v[26:27], off offset:1280 nt
	global_load_dword v74, v[26:27], off offset:1536 nt
	global_load_dword v75, v[26:27], off offset:1792 nt
	s_mul_hi_u32 s21, s16, s20
	s_add_i32 s21, s21, s31
	s_mul_i32 s17, s17, s20
	s_add_i32 s17, s21, s17
	s_mul_i32 s16, s16, s20
	v_lshl_add_u64 v[22:23], s[16:17], 2, v[22:23]
	v_lshl_add_u64 v[24:25], v[22:23], 0, s[18:19]
	global_load_dword v27, v[22:23], off nt
	global_load_dword v76, v[22:23], off offset:256 nt
	global_load_dword v77, v[22:23], off offset:512 nt
	global_load_dword v78, v[22:23], off offset:768 nt
	global_load_dword v79, v[22:23], off offset:1024 nt
	global_load_dword v80, v[22:23], off offset:1280 nt
	global_load_dword v81, v[22:23], off offset:1536 nt
	global_load_dword v82, v[22:23], off offset:1792 nt
	global_load_dword v83, v[24:25], off nt
	global_load_dword v84, v[24:25], off offset:256 nt
	global_load_dword v85, v[24:25], off offset:512 nt
	global_load_dword v86, v[24:25], off offset:768 nt
	global_load_dword v87, v[24:25], off offset:1024 nt
	global_load_dword v88, v[24:25], off offset:1280 nt
	global_load_dword v89, v[24:25], off offset:1536 nt
	global_load_dword v90, v[24:25], off offset:1792 nt
	s_lshl_b64 s[12:13], s[12:13], 20
	v_readlane_b32 s16, v255, 30
	s_add_u32 s16, s16, s12
	v_readlane_b32 s12, v255, 31
	s_addc_u32 s17, s12, s13
	v_readlane_b32 s12, v255, 32
	s_add_u32 s14, s12, s14
	v_readlane_b32 s12, v255, 33
	s_addc_u32 s15, s12, s15
	s_and_b64 s[12:13], s[10:11], exec
	s_cselect_b32 s12, s14, s16
	s_waitcnt vmcnt(63) expcnt(7) lgkmcnt(15)
	s_barrier
	s_cselect_b32 s13, s15, s17
	s_add_u32 s12, s12, s29
	s_addc_u32 s13, s13, 0
	s_waitcnt vmcnt(62)
	v_mul_f32_e32 v24, 0x42000000, v31
	s_waitcnt vmcnt(61)
	v_mul_f32_e32 v22, 0x42000000, v32
	v_mul_f32_e32 v23, 0x42000000, v30
	v_med3_f32 v25, v22, s25, v16
	v_med3_f32 v23, v23, s25, v16
	v_mov_b32_e32 v22, 0
	v_cvt_pk_fp8_f32 v22, v25, v23
	s_waitcnt vmcnt(53)
	v_mul_f32_e32 v23, 0x42000000, v40
	v_med3_f32 v24, v24, s25, v16
	v_med3_f32 v23, v23, s25, v16
	v_cvt_pk_fp8_f32 v22, v24, v23 op_sel:[0,0,1]
	v_mul_f32_e32 v23, 0x42000000, v33
	s_waitcnt vmcnt(51)
	v_mul_f32_e32 v24, 0x42000000, v42
	v_med3_f32 v23, v23, s25, v16
	v_med3_f32 v26, v24, s25, v16
	v_mov_b32_e32 v24, 0
	v_cvt_pk_fp8_f32 v24, v23, v26
	v_mul_f32_e32 v25, 0x42000000, v41
	s_waitcnt vmcnt(44)
	v_mul_f32_e32 v23, 0x42000000, v49
	v_med3_f32 v25, v25, s25, v16
	v_med3_f32 v23, v23, s25, v16
	v_cvt_pk_fp8_f32 v24, v25, v23 op_sel:[0,0,1]
	v_mul_f32_e32 v23, 0x42000000, v34
	v_mul_f32_e32 v25, 0x42000000, v43
	v_med3_f32 v23, v23, s25, v16
	v_med3_f32 v25, v25, s25, v16
	v_mov_b32_e32 v26, 0
	v_cvt_pk_fp8_f32 v26, v23, v25
	s_waitcnt vmcnt(43)
	v_mul_f32_e32 v30, 0x42000000, v50
	s_waitcnt vmcnt(37)
	v_mul_f32_e32 v23, 0x42000000, v28
	v_med3_f32 v25, v30, s25, v16
	v_med3_f32 v23, v23, s25, v16
	v_cvt_pk_fp8_f32 v26, v25, v23 op_sel:[0,0,1]
	v_mul_f32_e32 v23, 0x42000000, v35
	v_mul_f32_e32 v25, 0x42000000, v44
	v_med3_f32 v23, v23, s25, v16
	v_med3_f32 v25, v25, s25, v16
	v_mov_b32_e32 v28, 0
	v_cvt_pk_fp8_f32 v28, v23, v25
	v_mul_f32_e32 v30, 0x42000000, v51
	s_waitcnt vmcnt(36)
	v_mul_f32_e32 v23, 0x42000000, v55
	v_med3_f32 v25, v30, s25, v16
	v_med3_f32 v23, v23, s25, v16
	v_cvt_pk_fp8_f32 v28, v25, v23 op_sel:[0,0,1]
	v_mul_f32_e32 v23, 0x42000000, v36
	v_mul_f32_e32 v25, 0x42000000, v45
	v_med3_f32 v23, v23, s25, v16
	v_med3_f32 v25, v25, s25, v16
	v_mov_b32_e32 v30, 0
	v_cvt_pk_fp8_f32 v30, v23, v25
	v_mul_f32_e32 v31, 0x42000000, v52
	s_waitcnt vmcnt(35)
	v_mul_f32_e32 v23, 0x42000000, v56
	v_med3_f32 v25, v31, s25, v16
	v_med3_f32 v23, v23, s25, v16
	v_cvt_pk_fp8_f32 v30, v25, v23 op_sel:[0,0,1]
	v_mul_f32_e32 v23, 0x42000000, v37
	v_mul_f32_e32 v25, 0x42000000, v46
	v_med3_f32 v23, v23, s25, v16
	v_med3_f32 v25, v25, s25, v16
	v_mov_b32_e32 v32, 0
	v_cvt_pk_fp8_f32 v32, v23, v25
	v_mul_f32_e32 v31, 0x42000000, v53
	s_waitcnt vmcnt(34)
	v_mul_f32_e32 v23, 0x42000000, v57
	v_med3_f32 v25, v31, s25, v16
	v_med3_f32 v23, v23, s25, v16
	v_cvt_pk_fp8_f32 v32, v25, v23 op_sel:[0,0,1]
	v_mul_f32_e32 v23, 0x42000000, v38
	v_mul_f32_e32 v25, 0x42000000, v47
	v_med3_f32 v23, v23, s25, v16
	v_med3_f32 v25, v25, s25, v16
	v_mov_b32_e32 v34, 0
	v_cvt_pk_fp8_f32 v34, v23, v25
	v_mul_f32_e32 v31, 0x42000000, v54
	s_waitcnt vmcnt(33)
	v_mul_f32_e32 v23, 0x42000000, v58
	v_med3_f32 v25, v31, s25, v16
	v_med3_f32 v23, v23, s25, v16
	v_cvt_pk_fp8_f32 v34, v25, v23 op_sel:[0,0,1]
	v_mul_f32_e32 v23, 0x42000000, v39
	v_mul_f32_e32 v25, 0x42000000, v48
	v_med3_f32 v23, v23, s25, v16
	v_med3_f32 v25, v25, s25, v16
	v_mov_b32_e32 v36, 0
	v_cvt_pk_fp8_f32 v36, v23, v25
	v_mul_f32_e32 v29, 0x42000000, v29
	s_waitcnt vmcnt(32)
	v_mul_f32_e32 v23, 0x42000000, v59
	v_med3_f32 v25, v29, s25, v16
	v_med3_f32 v23, v23, s25, v16
	v_cvt_pk_fp8_f32 v36, v25, v23 op_sel:[0,0,1]
	s_waitcnt vmcnt(31)
	v_mul_f32_e32 v23, 0x42000000, v60
	s_waitcnt vmcnt(23)
	v_mul_f32_e32 v25, 0x42000000, v68
	v_med3_f32 v29, v23, s25, v16
	v_med3_f32 v25, v25, s25, v16
	v_mov_b32_e32 v23, 0
	v_cvt_pk_fp8_f32 v23, v29, v25
	s_waitcnt vmcnt(15)
	v_mul_f32_e32 v27, 0x42000000, v27
	s_waitcnt vmcnt(7)
	v_mul_f32_e32 v25, 0x42000000, v83
	v_med3_f32 v27, v27, s25, v16
	v_med3_f32 v25, v25, s25, v16
	v_cvt_pk_fp8_f32 v23, v27, v25 op_sel:[0,0,1]
	v_mul_f32_e32 v25, 0x42000000, v61
	v_mul_f32_e32 v27, 0x42000000, v69
	v_med3_f32 v31, v25, s25, v16
	v_med3_f32 v27, v27, s25, v16
	v_mov_b32_e32 v25, 0
	v_cvt_pk_fp8_f32 v25, v31, v27
	v_mul_f32_e32 v29, 0x42000000, v76
	s_waitcnt vmcnt(6)
	v_mul_f32_e32 v27, 0x42000000, v84
	v_med3_f32 v29, v29, s25, v16
	v_med3_f32 v27, v27, s25, v16
	v_cvt_pk_fp8_f32 v25, v29, v27 op_sel:[0,0,1]
	v_mul_f32_e32 v27, 0x42000000, v62
	v_mul_f32_e32 v29, 0x42000000, v70
	v_med3_f32 v33, v27, s25, v16
	v_med3_f32 v29, v29, s25, v16
	v_mov_b32_e32 v27, 0
	v_cvt_pk_fp8_f32 v27, v33, v29
	v_mul_f32_e32 v31, 0x42000000, v77
	s_waitcnt vmcnt(5)
	v_mul_f32_e32 v29, 0x42000000, v85
	v_med3_f32 v31, v31, s25, v16
	v_med3_f32 v29, v29, s25, v16
	v_cvt_pk_fp8_f32 v27, v31, v29 op_sel:[0,0,1]
	v_mul_f32_e32 v29, 0x42000000, v63
	v_mul_f32_e32 v31, 0x42000000, v71
	v_med3_f32 v35, v29, s25, v16
	v_med3_f32 v31, v31, s25, v16
	v_mov_b32_e32 v29, 0
	v_cvt_pk_fp8_f32 v29, v35, v31
	v_mul_f32_e32 v33, 0x42000000, v78
	s_waitcnt vmcnt(4)
	v_mul_f32_e32 v31, 0x42000000, v86
	v_med3_f32 v33, v33, s25, v16
	v_med3_f32 v31, v31, s25, v16
	v_cvt_pk_fp8_f32 v29, v33, v31 op_sel:[0,0,1]
	v_mul_f32_e32 v31, 0x42000000, v64
	v_mul_f32_e32 v33, 0x42000000, v72
	v_med3_f32 v37, v31, s25, v16
	v_med3_f32 v33, v33, s25, v16
	v_mov_b32_e32 v31, 0
	v_cvt_pk_fp8_f32 v31, v37, v33
	v_mul_f32_e32 v35, 0x42000000, v79
	s_waitcnt vmcnt(3)
	v_mul_f32_e32 v33, 0x42000000, v87
	v_med3_f32 v35, v35, s25, v16
	v_med3_f32 v33, v33, s25, v16
	v_cvt_pk_fp8_f32 v31, v35, v33 op_sel:[0,0,1]
	v_mul_f32_e32 v33, 0x42000000, v65
	v_mul_f32_e32 v35, 0x42000000, v73
	v_med3_f32 v38, v33, s25, v16
	v_med3_f32 v35, v35, s25, v16
	v_mov_b32_e32 v33, 0
	v_cvt_pk_fp8_f32 v33, v38, v35
	v_mul_f32_e32 v37, 0x42000000, v80
	s_waitcnt vmcnt(2)
	v_mul_f32_e32 v35, 0x42000000, v88
	v_med3_f32 v37, v37, s25, v16
	v_med3_f32 v35, v35, s25, v16
	v_cvt_pk_fp8_f32 v33, v37, v35 op_sel:[0,0,1]
	v_mul_f32_e32 v35, 0x42000000, v66
	v_mul_f32_e32 v37, 0x42000000, v74
	v_med3_f32 v39, v35, s25, v16
	v_med3_f32 v37, v37, s25, v16
	v_mov_b32_e32 v35, 0
	v_cvt_pk_fp8_f32 v35, v39, v37
	v_mul_f32_e32 v38, 0x42000000, v81
	s_waitcnt vmcnt(1)
	v_mul_f32_e32 v37, 0x42000000, v89
	v_med3_f32 v38, v38, s25, v16
	v_med3_f32 v37, v37, s25, v16
	v_cvt_pk_fp8_f32 v35, v38, v37 op_sel:[0,0,1]
	v_mul_f32_e32 v37, 0x42000000, v67
	v_mul_f32_e32 v38, 0x42000000, v75
	v_med3_f32 v40, v37, s25, v16
	v_med3_f32 v38, v38, s25, v16
	v_mov_b32_e32 v37, 0
	v_cvt_pk_fp8_f32 v37, v40, v38
	v_mul_f32_e32 v39, 0x42000000, v82
	s_waitcnt vmcnt(0)
	v_mul_f32_e32 v38, 0x42000000, v90
	v_med3_f32 v39, v39, s25, v16
	v_med3_f32 v38, v38, s25, v16
	v_cvt_pk_fp8_f32 v37, v39, v38 op_sel:[0,0,1]
	ds_write2st64_b64 v17, v[22:23], v[24:25] offset1:9
	ds_write2st64_b64 v17, v[26:27], v[28:29] offset0:18 offset1:27
	ds_write2st64_b64 v17, v[30:31], v[32:33] offset0:36 offset1:45
	ds_write2st64_b64 v17, v[34:35], v[36:37] offset0:54 offset1:63
	v_add_u32_e32 v27, s8, v4
	s_waitcnt lgkmcnt(0)
	s_barrier
	ds_read2_b64 v[22:25], v18 offset1:1
	v_or_b32_e32 v26, s28, v5
	v_and_or_b32 v27, v27, s22, v6
	v_cndmask_b32_e64 v26, v26, v27, s[10:11]
	v_lshl_add_u64 v[30:31], s[12:13], 0, v[0:1]
	s_and_b64 s[12:13], s[10:11], exec
	v_ashrrev_i32_e32 v27, 31, v26
	s_cselect_b32 s12, 9, 10
	v_lshlrev_b64 v[26:27], s12, v[26:27]
	v_lshl_add_u64 v[32:33], v[30:31], 0, v[26:27]
	ds_read2_b64 v[26:29], v19 offset1:1
	s_waitcnt lgkmcnt(1)
	global_store_dwordx4 v[32:33], v[22:25], off sc1
	s_add_i32 s27, s27, s44
	s_add_i32 s23, s23, s24
	v_add_u32_e32 v22, s8, v7
	v_and_or_b32 v22, v22, s22, v9
	v_or_b32_e32 v23, s28, v8
	v_cndmask_b32_e64 v22, v23, v22, s[10:11]
	v_ashrrev_i32_e32 v23, 31, v22
	v_lshlrev_b64 v[22:23], s12, v[22:23]
	v_lshl_add_u64 v[22:23], v[30:31], 0, v[22:23]
	s_waitcnt lgkmcnt(0)
	global_store_dwordx4 v[22:23], v[26:29], off sc1
	ds_read2_b64 v[22:25], v20 offset1:1
	s_add_i32 s26, s26, s63
	v_add_u32_e32 v26, s8, v10
	v_and_or_b32 v26, v26, s22, v12
	v_or_b32_e32 v27, s28, v11
	v_cndmask_b32_e64 v26, v27, v26, s[10:11]
	v_ashrrev_i32_e32 v27, 31, v26
	v_lshlrev_b64 v[26:27], s12, v[26:27]
	v_lshl_add_u64 v[32:33], v[30:31], 0, v[26:27]
	ds_read2_b64 v[26:29], v21 offset1:1
	s_waitcnt lgkmcnt(1)
	global_store_dwordx4 v[32:33], v[22:25], off sc1
	s_cmpk_lt_i32 s27, 0x600
	s_nop 0
	v_add_u32_e32 v22, s8, v13
	v_and_or_b32 v22, v22, s22, v15
	v_or_b32_e32 v23, s28, v14
	v_cndmask_b32_e64 v22, v23, v22, s[10:11]
	v_ashrrev_i32_e32 v23, 31, v22
	v_lshlrev_b64 v[22:23], s12, v[22:23]
	v_lshl_add_u64 v[22:23], v[30:31], 0, v[22:23]
	s_waitcnt lgkmcnt(0)
	global_store_dwordx4 v[22:23], v[26:29], off sc1
	s_cbranch_scc0 .LBB0_119

.LBB0_172:
	s_add_i32 s15, s29, s7
	s_lshl_b64 s[20:21], s[66:67], 2
	s_add_u32 s18, s18, s20
	s_addc_u32 s19, s19, s21
	v_lshl_add_u64 v[20:21], s[18:19], 0, v[0:1]
	s_ashr_i32 s18, s15, 31
	s_mul_i32 s22, s16, s18
	s_mul_hi_u32 s18, s16, s15
	s_add_i32 s18, s18, s22
	s_mul_i32 s19, s17, s15
	s_add_i32 s19, s18, s19
	s_mul_i32 s18, s16, s15
	v_lshl_add_u64 v[22:23], s[18:19], 2, v[20:21]
	s_lshl_b64 s[18:19], s[16:17], 2
	v_lshl_add_u64 v[24:25], v[22:23], 0, s[18:19]
	global_load_dword v19, v[24:25], off nt
	s_or_b32 s20, s15, 2
	s_mul_hi_u32 s21, s16, s20
	s_add_i32 s21, s21, s22
	s_mul_i32 s23, s17, s20
	s_add_i32 s21, s21, s23
	s_mul_i32 s20, s16, s20
	v_lshl_add_u64 v[26:27], s[20:21], 2, v[20:21]
	global_load_dword v28, v[26:27], off nt
	global_load_dword v29, v[22:23], off nt
	global_load_dword v30, v[22:23], off offset:256 nt
	global_load_dword v31, v[22:23], off offset:512 nt
	global_load_dword v32, v[22:23], off offset:768 nt
	global_load_dword v33, v[22:23], off offset:1024 nt
	global_load_dword v34, v[22:23], off offset:1280 nt
	global_load_dword v35, v[22:23], off offset:1536 nt
	global_load_dword v36, v[22:23], off offset:1792 nt
	v_lshl_add_u64 v[22:23], v[26:27], 0, s[18:19]
	global_load_dword v37, v[22:23], off nt
	global_load_dword v38, v[26:27], off offset:256 nt
	global_load_dword v39, v[24:25], off offset:256 nt
	global_load_dword v40, v[24:25], off offset:512 nt
	global_load_dword v41, v[24:25], off offset:768 nt
	global_load_dword v42, v[24:25], off offset:1024 nt
	global_load_dword v43, v[24:25], off offset:1280 nt
	global_load_dword v44, v[24:25], off offset:1536 nt
	global_load_dword v45, v[24:25], off offset:1792 nt
	global_load_dword v46, v[22:23], off offset:256 nt
	global_load_dword v47, v[26:27], off offset:512 nt
	global_load_dword v48, v[26:27], off offset:768 nt
	global_load_dword v49, v[26:27], off offset:1024 nt
	global_load_dword v50, v[26:27], off offset:1280 nt
	global_load_dword v51, v[26:27], off offset:1536 nt
	s_nop 0
	global_load_dword v27, v[26:27], off offset:1792 nt
	s_nop 0
	global_load_dword v26, v[22:23], off offset:512 nt
	global_load_dword v52, v[22:23], off offset:768 nt
	global_load_dword v53, v[22:23], off offset:1024 nt
	global_load_dword v54, v[22:23], off offset:1280 nt
	global_load_dword v55, v[22:23], off offset:1536 nt
	global_load_dword v56, v[22:23], off offset:1792 nt
	s_or_b32 s20, s15, 4
	s_mul_hi_u32 s21, s16, s20
	s_add_i32 s21, s21, s22
	s_mul_i32 s23, s17, s20
	s_add_i32 s21, s21, s23
	s_mul_i32 s20, s16, s20
	v_lshl_add_u64 v[22:23], s[20:21], 2, v[20:21]
	s_or_b32 s15, s15, 6
	v_lshl_add_u64 v[24:25], v[22:23], 0, s[18:19]
	global_load_dword v57, v[22:23], off nt
	global_load_dword v58, v[22:23], off offset:256 nt
	global_load_dword v59, v[22:23], off offset:512 nt
	global_load_dword v60, v[22:23], off offset:768 nt
	global_load_dword v61, v[22:23], off offset:1024 nt
	global_load_dword v62, v[22:23], off offset:1280 nt
	global_load_dword v63, v[22:23], off offset:1536 nt
	global_load_dword v66, v[22:23], off offset:1792 nt
	global_load_dword v67, v[24:25], off nt
	global_load_dword v68, v[24:25], off offset:256 nt
	global_load_dword v69, v[24:25], off offset:512 nt
	global_load_dword v70, v[24:25], off offset:768 nt
	global_load_dword v71, v[24:25], off offset:1024 nt
	global_load_dword v72, v[24:25], off offset:1280 nt
	global_load_dword v73, v[24:25], off offset:1536 nt
	global_load_dword v74, v[24:25], off offset:1792 nt
	s_mul_hi_u32 s20, s16, s15
	s_add_i32 s20, s20, s22
	s_mul_i32 s17, s17, s15
	s_add_i32 s17, s20, s17
	s_mul_i32 s16, s16, s15
	v_lshl_add_u64 v[20:21], s[16:17], 2, v[20:21]
	v_lshl_add_u64 v[22:23], v[20:21], 0, s[18:19]
	global_load_dword v25, v[20:21], off nt
	global_load_dword v75, v[20:21], off offset:256 nt
	global_load_dword v76, v[20:21], off offset:512 nt
	global_load_dword v77, v[20:21], off offset:768 nt
	global_load_dword v78, v[20:21], off offset:1024 nt
	global_load_dword v79, v[20:21], off offset:1280 nt
	global_load_dword v80, v[20:21], off offset:1536 nt
	global_load_dword v81, v[20:21], off offset:1792 nt
	global_load_dword v82, v[22:23], off nt
	global_load_dword v83, v[22:23], off offset:256 nt
	global_load_dword v84, v[22:23], off offset:512 nt
	global_load_dword v85, v[22:23], off offset:768 nt
	global_load_dword v86, v[22:23], off offset:1024 nt
	global_load_dword v87, v[22:23], off offset:1280 nt
	global_load_dword v88, v[22:23], off offset:1536 nt
	global_load_dword v89, v[22:23], off offset:1792 nt
	v_mov_b32_e32 v24, v65
	s_ashr_i32 s15, s14, 31
	s_lshl_b64 s[16:17], s[14:15], 20
	v_readlane_b32 s18, v255, 30
	s_add_u32 s16, s18, s16
	v_readlane_b32 s18, v255, 31
	s_addc_u32 s17, s18, s17
	s_lshl_b64 s[14:15], s[14:15], 19
	v_readlane_b32 s18, v255, 32
	s_add_u32 s18, s18, s14
	v_readlane_b32 s14, v255, 33
	s_addc_u32 s19, s14, s15
	s_and_b64 s[14:15], s[12:13], exec
	s_cselect_b32 s14, s18, s16
	s_waitcnt vmcnt(63) expcnt(7) lgkmcnt(15)
	s_barrier
	s_movk_i32 s20, 0xff00
	s_cselect_b32 s15, s19, s17
	s_add_u32 s14, s14, s29
	s_addc_u32 s15, s15, 0
	s_waitcnt vmcnt(52)
	v_mul_f32_e32 v23, 0x42000000, v38
	v_mul_f32_e32 v21, 0x42000000, v28
	v_mul_f32_e32 v20, 0x42000000, v29
	v_mul_f32_e32 v19, 0x42000000, v19
	v_med3_f32 v22, v20, s55, v228
	v_med3_f32 v19, v19, s55, v228
	v_mov_b32_e32 v20, v65
	v_cvt_pk_fp8_f32 v20, v22, v19
	v_mul_f32_e32 v19, 0x42000000, v37
	v_med3_f32 v21, v21, s55, v228
	v_med3_f32 v19, v19, s55, v228
	v_cvt_pk_fp8_f32 v20, v21, v19 op_sel:[0,0,1]
	v_mul_f32_e32 v19, 0x42000000, v30
	s_waitcnt vmcnt(51)
	v_mul_f32_e32 v21, 0x42000000, v39
	v_med3_f32 v19, v19, s55, v228
	v_med3_f32 v21, v21, s55, v228
	v_mov_b32_e32 v22, v65
	v_cvt_pk_fp8_f32 v22, v19, v21
	s_waitcnt vmcnt(44)
	v_mul_f32_e32 v19, 0x42000000, v46
	v_med3_f32 v21, v23, s55, v228
	v_med3_f32 v19, v19, s55, v228
	v_cvt_pk_fp8_f32 v22, v21, v19 op_sel:[0,0,1]
	v_mul_f32_e32 v19, 0x42000000, v31
	v_mul_f32_e32 v21, 0x42000000, v40
	v_med3_f32 v19, v19, s55, v228
	v_med3_f32 v21, v21, s55, v228
	v_cvt_pk_fp8_f32 v24, v19, v21
	s_waitcnt vmcnt(43)
	v_mul_f32_e32 v23, 0x42000000, v47
	s_waitcnt vmcnt(37)
	v_mul_f32_e32 v19, 0x42000000, v26
	v_med3_f32 v21, v23, s55, v228
	v_med3_f32 v19, v19, s55, v228
	v_cvt_pk_fp8_f32 v24, v21, v19 op_sel:[0,0,1]
	v_mul_f32_e32 v19, 0x42000000, v32
	v_mul_f32_e32 v21, 0x42000000, v41
	v_med3_f32 v19, v19, s55, v228
	v_med3_f32 v21, v21, s55, v228
	v_mov_b32_e32 v26, v65
	v_cvt_pk_fp8_f32 v26, v19, v21
	v_mul_f32_e32 v23, 0x42000000, v48
	s_waitcnt vmcnt(36)
	v_mul_f32_e32 v19, 0x42000000, v52
	v_med3_f32 v21, v23, s55, v228
	v_med3_f32 v19, v19, s55, v228
	v_cvt_pk_fp8_f32 v26, v21, v19 op_sel:[0,0,1]
	v_mul_f32_e32 v19, 0x42000000, v33
	v_mul_f32_e32 v21, 0x42000000, v42
	v_med3_f32 v19, v19, s55, v228
	v_med3_f32 v21, v21, s55, v228
	v_mov_b32_e32 v28, v65
	v_cvt_pk_fp8_f32 v28, v19, v21
	v_mul_f32_e32 v23, 0x42000000, v49
	s_waitcnt vmcnt(35)
	v_mul_f32_e32 v19, 0x42000000, v53
	v_med3_f32 v21, v23, s55, v228
	v_med3_f32 v19, v19, s55, v228
	v_cvt_pk_fp8_f32 v28, v21, v19 op_sel:[0,0,1]
	v_mul_f32_e32 v19, 0x42000000, v34
	v_mul_f32_e32 v21, 0x42000000, v43
	v_med3_f32 v19, v19, s55, v228
	v_med3_f32 v21, v21, s55, v228
	v_mov_b32_e32 v30, v65
	v_cvt_pk_fp8_f32 v30, v19, v21
	v_mul_f32_e32 v23, 0x42000000, v50
	s_waitcnt vmcnt(34)
	v_mul_f32_e32 v19, 0x42000000, v54
	v_med3_f32 v21, v23, s55, v228
	v_med3_f32 v19, v19, s55, v228
	v_cvt_pk_fp8_f32 v30, v21, v19 op_sel:[0,0,1]
	v_mul_f32_e32 v19, 0x42000000, v35
	v_mul_f32_e32 v21, 0x42000000, v44
	v_med3_f32 v19, v19, s55, v228
	v_med3_f32 v21, v21, s55, v228
	v_mov_b32_e32 v32, v65
	v_cvt_pk_fp8_f32 v32, v19, v21
	v_mul_f32_e32 v23, 0x42000000, v51
	s_waitcnt vmcnt(33)
	v_mul_f32_e32 v19, 0x42000000, v55
	v_med3_f32 v21, v23, s55, v228
	v_med3_f32 v19, v19, s55, v228
	v_cvt_pk_fp8_f32 v32, v21, v19 op_sel:[0,0,1]
	v_mul_f32_e32 v19, 0x42000000, v36
	v_mul_f32_e32 v21, 0x42000000, v45
	v_med3_f32 v19, v19, s55, v228
	v_med3_f32 v21, v21, s55, v228
	v_mov_b32_e32 v34, v65
	v_cvt_pk_fp8_f32 v34, v19, v21
	v_mul_f32_e32 v23, 0x42000000, v27
	s_waitcnt vmcnt(32)
	v_mul_f32_e32 v19, 0x42000000, v56
	v_med3_f32 v21, v23, s55, v228
	v_med3_f32 v19, v19, s55, v228
	v_cvt_pk_fp8_f32 v34, v21, v19 op_sel:[0,0,1]
	s_waitcnt vmcnt(31)
	v_mul_f32_e32 v19, 0x42000000, v57
	s_waitcnt vmcnt(23)
	v_mul_f32_e32 v21, 0x42000000, v67
	s_waitcnt vmcnt(15)
	v_mul_f32_e32 v23, 0x42000000, v25
	v_med3_f32 v19, v19, s55, v228
	v_med3_f32 v25, v21, s55, v228
	v_mov_b32_e32 v21, v65
	v_cvt_pk_fp8_f32 v21, v19, v25
	s_waitcnt vmcnt(7)
	v_mul_f32_e32 v19, 0x42000000, v82
	v_med3_f32 v23, v23, s55, v228
	v_med3_f32 v19, v19, s55, v228
	v_cvt_pk_fp8_f32 v21, v23, v19 op_sel:[0,0,1]
	v_mul_f32_e32 v19, 0x42000000, v58
	v_mul_f32_e32 v23, 0x42000000, v68
	v_med3_f32 v19, v19, s55, v228
	v_med3_f32 v27, v23, s55, v228
	v_mov_b32_e32 v23, v65
	v_cvt_pk_fp8_f32 v23, v19, v27
	v_mul_f32_e32 v25, 0x42000000, v75
	s_waitcnt vmcnt(6)
	v_mul_f32_e32 v19, 0x42000000, v83
	v_med3_f32 v25, v25, s55, v228
	v_med3_f32 v19, v19, s55, v228
	v_cvt_pk_fp8_f32 v23, v25, v19 op_sel:[0,0,1]
	v_mul_f32_e32 v19, 0x42000000, v59
	v_mul_f32_e32 v25, 0x42000000, v69
	v_med3_f32 v19, v19, s55, v228
	v_med3_f32 v29, v25, s55, v228
	v_mov_b32_e32 v25, v65
	v_cvt_pk_fp8_f32 v25, v19, v29
	v_mul_f32_e32 v27, 0x42000000, v76
	s_waitcnt vmcnt(5)
	v_mul_f32_e32 v19, 0x42000000, v84
	v_med3_f32 v27, v27, s55, v228
	v_med3_f32 v19, v19, s55, v228
	v_cvt_pk_fp8_f32 v25, v27, v19 op_sel:[0,0,1]
	v_mul_f32_e32 v19, 0x42000000, v60
	v_mul_f32_e32 v27, 0x42000000, v70
	v_med3_f32 v19, v19, s55, v228
	v_med3_f32 v31, v27, s55, v228
	v_mov_b32_e32 v27, v65
	v_cvt_pk_fp8_f32 v27, v19, v31
	v_mul_f32_e32 v29, 0x42000000, v77
	s_waitcnt vmcnt(4)
	v_mul_f32_e32 v19, 0x42000000, v85
	v_med3_f32 v29, v29, s55, v228
	v_med3_f32 v19, v19, s55, v228
	v_cvt_pk_fp8_f32 v27, v29, v19 op_sel:[0,0,1]
	v_mul_f32_e32 v19, 0x42000000, v61
	v_mul_f32_e32 v29, 0x42000000, v71
	v_med3_f32 v19, v19, s55, v228
	v_med3_f32 v33, v29, s55, v228
	v_mov_b32_e32 v29, v65
	v_cvt_pk_fp8_f32 v29, v19, v33
	v_mul_f32_e32 v31, 0x42000000, v78
	s_waitcnt vmcnt(3)
	v_mul_f32_e32 v19, 0x42000000, v86
	v_med3_f32 v31, v31, s55, v228
	v_med3_f32 v19, v19, s55, v228
	v_cvt_pk_fp8_f32 v29, v31, v19 op_sel:[0,0,1]
	v_mul_f32_e32 v19, 0x42000000, v62
	v_mul_f32_e32 v31, 0x42000000, v72
	v_med3_f32 v19, v19, s55, v228
	v_med3_f32 v35, v31, s55, v228
	v_mov_b32_e32 v31, v65
	v_cvt_pk_fp8_f32 v31, v19, v35
	v_mul_f32_e32 v33, 0x42000000, v79
	s_waitcnt vmcnt(2)
	v_mul_f32_e32 v19, 0x42000000, v87
	v_med3_f32 v33, v33, s55, v228
	v_med3_f32 v19, v19, s55, v228
	v_cvt_pk_fp8_f32 v31, v33, v19 op_sel:[0,0,1]
	v_mul_f32_e32 v19, 0x42000000, v63
	v_mul_f32_e32 v33, 0x42000000, v73
	v_med3_f32 v19, v19, s55, v228
	v_med3_f32 v36, v33, s55, v228
	v_mov_b32_e32 v33, v65
	v_cvt_pk_fp8_f32 v33, v19, v36
	v_mul_f32_e32 v35, 0x42000000, v80
	s_waitcnt vmcnt(1)
	v_mul_f32_e32 v19, 0x42000000, v88
	v_med3_f32 v35, v35, s55, v228
	v_med3_f32 v19, v19, s55, v228
	v_cvt_pk_fp8_f32 v33, v35, v19 op_sel:[0,0,1]
	v_mul_f32_e32 v19, 0x42000000, v66
	v_mul_f32_e32 v35, 0x42000000, v74
	v_med3_f32 v19, v19, s55, v228
	v_med3_f32 v37, v35, s55, v228
	v_mov_b32_e32 v35, v65
	v_cvt_pk_fp8_f32 v35, v19, v37
	v_mul_f32_e32 v36, 0x42000000, v81
	s_waitcnt vmcnt(0)
	v_mul_f32_e32 v19, 0x42000000, v89
	v_med3_f32 v36, v36, s55, v228
	v_med3_f32 v19, v19, s55, v228
	v_cvt_pk_fp8_f32 v35, v36, v19 op_sel:[0,0,1]
	ds_write2st64_b64 v14, v[20:21], v[22:23] offset1:9
	ds_write2st64_b64 v14, v[24:25], v[26:27] offset0:18 offset1:27
	ds_write2st64_b64 v14, v[28:29], v[30:31] offset0:36 offset1:45
	ds_write2st64_b64 v14, v[32:33], v[34:35] offset0:54 offset1:63
	v_add_u32_e32 v24, s66, v2
	s_waitcnt lgkmcnt(0)
	s_barrier
	ds_read2_b64 v[20:23], v15 offset1:1
	v_or_b32_e32 v19, s28, v3
	v_and_or_b32 v24, v24, s20, v4
	v_cndmask_b32_e64 v24, v19, v24, s[12:13]
	v_lshl_add_u64 v[28:29], s[14:15], 0, v[64:65]
	s_and_b64 s[14:15], s[12:13], exec
	v_ashrrev_i32_e32 v25, 31, v24
	s_cselect_b32 s14, 9, 10
	v_lshlrev_b64 v[24:25], s14, v[24:25]
	v_lshl_add_u64 v[30:31], v[28:29], 0, v[24:25]
	v_add_u32_e32 v19, s66, v5
	ds_read2_b64 v[24:27], v16 offset1:1
	s_waitcnt lgkmcnt(1)
	global_store_dwordx4 v[30:31], v[20:23], off sc1
	v_and_or_b32 v19, v19, s20, v7
	s_add_i32 s27, s27, s44
	v_or_b32_e32 v20, s28, v6
	v_cndmask_b32_e64 v20, v20, v19, s[12:13]
	v_ashrrev_i32_e32 v21, 31, v20
	v_lshlrev_b64 v[20:21], s14, v[20:21]
	v_lshl_add_u64 v[20:21], v[28:29], 0, v[20:21]
	v_add_u32_e32 v19, s66, v8
	s_waitcnt lgkmcnt(0)
	global_store_dwordx4 v[20:21], v[24:27], off sc1
	ds_read2_b64 v[20:23], v17 offset1:1
	v_and_or_b32 v19, v19, s20, v10
	v_or_b32_e32 v24, s28, v9
	v_cndmask_b32_e64 v24, v24, v19, s[12:13]
	v_ashrrev_i32_e32 v25, 31, v24
	v_lshlrev_b64 v[24:25], s14, v[24:25]
	v_lshl_add_u64 v[30:31], v[28:29], 0, v[24:25]
	v_add_u32_e32 v19, s66, v11
	ds_read2_b64 v[24:27], v18 offset1:1
	s_waitcnt lgkmcnt(1)
	global_store_dwordx4 v[30:31], v[20:23], off sc1
	v_and_or_b32 v19, v19, s20, v13
	s_add_i32 s26, s26, s24
	v_or_b32_e32 v20, s28, v12
	v_cndmask_b32_e64 v20, v20, v19, s[12:13]
	v_ashrrev_i32_e32 v21, 31, v20
	v_lshlrev_b64 v[20:21], s14, v[20:21]
	s_add_i32 s25, s25, s63
	v_lshl_add_u64 v[20:21], v[28:29], 0, v[20:21]
	s_cmpk_lt_i32 s27, 0x600
	s_waitcnt lgkmcnt(0)
	global_store_dwordx4 v[20:21], v[24:27], off sc1
	s_cbranch_scc0 .LBB0_181

.LBB0_271:
	s_lshl_b32 s20, s38, 2
	s_waitcnt lgkmcnt(0)
	v_lshl_add_u32 v154, s22, 8, v64
	s_and_b32 s20, s20, 12
	v_lshrrev_b32_e32 v149, 9, v154
	s_or_b32 s39, s20, s35
	v_and_b32_e32 v149, 0x7fff0, v149
	s_lshr_b32 s66, s38, 2
	v_and_b32_e32 v148, 0x1fff, v154
	v_or_b32_e32 v149, s39, v149
	s_cmp_lt_u32 s38, 4
	v_lshl_or_b32 v152, v149, 13, v148
	s_cselect_b64 vcc, -1, 0
	v_mov_b32_e32 v149, 0x3d000000
	v_mov_b32_e32 v150, 0x3bb8aa3b
	v_cndmask_b32_e32 v150, v149, v150, vcc
	s_lshl_b64 s[20:21], s[66:67], 27
	v_pk_mul_f32 v[126:127], v[150:151], v[126:127] op_sel_hi:[0,1]
	s_add_u32 s20, s64, s20
	v_ashrrev_i32_e32 v153, 31, v152
	v_lshl_add_u32 v148, v164, 3, s36
	v_pk_mul_f32 v[164:165], v[150:151], v[124:125] op_sel_hi:[0,1]
	v_pk_mul_f32 v[124:125], v[150:151], v[122:123] op_sel_hi:[0,1]
	v_cvt_pk_bf16_f32 v122, v126, v127
	s_addc_u32 s21, s65, s21
	v_lshlrev_b64 v[126:127], 7, v[152:153]
	v_ashrrev_i32_e32 v149, 31, v148
	v_lshl_add_u64 v[126:127], s[20:21], 0, v[126:127]
	v_lshl_add_u64 v[126:127], v[148:149], 1, v[126:127]
	s_and_b64 vcc, exec, s[6:7]
	v_pk_mul_f32 v[128:129], v[150:151], v[128:129] op_sel_hi:[0,1]
	v_cvt_pk_bf16_f32 v123, v128, v129
	v_cvt_pk_bf16_f32 v124, v124, v125
	v_cvt_pk_bf16_f32 v125, v164, v165
	global_store_dwordx4 v[126:127], v[122:125], off nt sc1
	s_cbranch_vccnz .LBB0_275
	ds_swizzle_b32 v126, v118 offset:swizzle(SWAP,16)
	ds_swizzle_b32 v122, v114 offset:swizzle(SWAP,16)
	ds_swizzle_b32 v127, v119 offset:swizzle(SWAP,16)
	ds_swizzle_b32 v123, v115 offset:swizzle(SWAP,16)
	ds_swizzle_b32 v128, v120 offset:swizzle(SWAP,16)
	ds_swizzle_b32 v124, v116 offset:swizzle(SWAP,16)
	ds_swizzle_b32 v129, v121 offset:swizzle(SWAP,16)
	ds_swizzle_b32 v125, v117 offset:swizzle(SWAP,16)
	s_and_saveexec_b64 s[22:23], s[8:9]
	s_cbranch_execz .LBB0_274
	s_waitcnt lgkmcnt(0)
	v_pk_mul_f32 v[128:129], v[144:145], v[128:129]
	v_pk_mul_f32 v[126:127], v[142:143], v[126:127]
	v_mov_b32_e32 v142, v146
	v_mov_b32_e32 v143, v146
	v_pk_mul_f32 v[124:125], v[140:141], v[124:125]
	v_pk_mul_f32 v[122:123], v[138:139], v[122:123]
	v_pk_mul_f32 v[128:129], v[142:143], v[128:129]
	v_pk_mul_f32 v[126:127], v[146:147], v[126:127]
	v_pk_mul_f32 v[124:125], v[142:143], v[124:125]
	v_pk_mul_f32 v[122:123], v[146:147], v[122:123]
	v_pk_fma_f32 v[120:121], v[120:121], v[136:137], v[128:129]
	v_pk_fma_f32 v[118:119], v[118:119], v[134:135], v[126:127]
	v_pk_fma_f32 v[116:117], v[116:117], v[132:133], v[124:125]
	v_pk_fma_f32 v[114:115], v[114:115], v[130:131], v[122:123]

.LBB0_275:
	v_mov_b32_e32 v151, v150
	s_waitcnt lgkmcnt(0)
	v_mov_b32_e32 v122, v150
	v_mov_b32_e32 v123, v150
	v_pk_mul_f32 v[118:119], v[150:151], v[118:119]
	v_pk_mul_f32 v[120:121], v[122:123], v[120:121]
	v_pk_mul_f32 v[122:123], v[122:123], v[116:117]
	v_pk_mul_f32 v[116:117], v[150:151], v[114:115]
	v_cvt_pk_bf16_f32 v114, v118, v119
	v_or_b32_e32 v118, 0x4000, v152
	v_ashrrev_i32_e32 v119, 31, v118
	v_lshlrev_b64 v[118:119], 7, v[118:119]
	v_lshl_add_u64 v[118:119], s[20:21], 0, v[118:119]
	v_lshl_add_u64 v[118:119], v[148:149], 1, v[118:119]
	v_cvt_pk_bf16_f32 v115, v120, v121
	v_cvt_pk_bf16_f32 v116, v116, v117
	v_cvt_pk_bf16_f32 v117, v122, v123
	global_store_dwordx4 v[118:119], v[114:117], off nt sc1
	s_and_b64 vcc, exec, s[6:7]
	s_cbranch_vccnz .LBB0_277
	s_add_i32 s22, 0, 0x20000
	v_lshl_add_u32 v122, v64, 6, s22
	ds_read_b128 v[118:121], v122 offset:1024
	ds_read_b128 v[114:117], v122 offset:1040
	ds_read_b128 v[126:129], v122 offset:1056
	ds_read_b128 v[122:125], v122 offset:1072
	s_and_b64 vcc, exec, s[6:7]
	s_cbranch_vccz .LBB0_278
	s_branch .LBB0_281

.LBB0_281:
	s_waitcnt lgkmcnt(0)
	v_add_u32_e32 v130, 16, v154
	v_and_b32_e32 v131, 0x1fff, v130
	v_lshrrev_b32_e32 v130, 9, v130
	v_and_b32_e32 v130, 0x7fff0, v130
	v_or_b32_e32 v130, s39, v130
	v_lshl_or_b32 v130, v130, 13, v131
	v_mov_b32_e32 v132, v150
	v_mov_b32_e32 v133, v150
	v_pk_mul_f32 v[110:111], v[150:151], v[110:111]
	v_ashrrev_i32_e32 v131, 31, v130
	v_pk_mul_f32 v[134:135], v[132:133], v[108:109]
	v_pk_mul_f32 v[108:109], v[150:151], v[106:107]
	v_cvt_pk_bf16_f32 v106, v110, v111
	v_lshlrev_b64 v[110:111], 7, v[130:131]
	v_lshl_add_u64 v[110:111], s[20:21], 0, v[110:111]
	v_lshl_add_u64 v[110:111], v[148:149], 1, v[110:111]
	s_and_b64 vcc, exec, s[6:7]
	v_pk_mul_f32 v[112:113], v[132:133], v[112:113]
	s_nop 0
	v_cvt_pk_bf16_f32 v107, v112, v113
	v_cvt_pk_bf16_f32 v108, v108, v109
	v_cvt_pk_bf16_f32 v109, v134, v135
	global_store_dwordx4 v[110:111], v[106:109], off nt sc1
	s_cbranch_vccnz .LBB0_285
	ds_swizzle_b32 v110, v102 offset:swizzle(SWAP,16)
	ds_swizzle_b32 v106, v98 offset:swizzle(SWAP,16)
	ds_swizzle_b32 v111, v103 offset:swizzle(SWAP,16)
	ds_swizzle_b32 v107, v99 offset:swizzle(SWAP,16)
	ds_swizzle_b32 v112, v104 offset:swizzle(SWAP,16)
	ds_swizzle_b32 v108, v100 offset:swizzle(SWAP,16)
	ds_swizzle_b32 v113, v105 offset:swizzle(SWAP,16)
	ds_swizzle_b32 v109, v101 offset:swizzle(SWAP,16)
	s_and_saveexec_b64 s[22:23], s[8:9]
	s_cbranch_execz .LBB0_284
	s_waitcnt lgkmcnt(0)
	v_pk_mul_f32 v[112:113], v[128:129], v[112:113]
	v_pk_mul_f32 v[110:111], v[126:127], v[110:111]
	v_mov_b32_e32 v126, v146
	v_mov_b32_e32 v127, v146
	v_pk_mul_f32 v[108:109], v[124:125], v[108:109]
	v_pk_mul_f32 v[106:107], v[122:123], v[106:107]
	v_pk_mul_f32 v[112:113], v[126:127], v[112:113]
	v_pk_mul_f32 v[110:111], v[146:147], v[110:111]
	v_pk_mul_f32 v[108:109], v[126:127], v[108:109]
	v_pk_mul_f32 v[106:107], v[146:147], v[106:107]
	v_pk_fma_f32 v[104:105], v[104:105], v[120:121], v[112:113]
	v_pk_fma_f32 v[102:103], v[102:103], v[118:119], v[110:111]
	v_pk_fma_f32 v[100:101], v[100:101], v[116:117], v[108:109]
	v_pk_fma_f32 v[98:99], v[98:99], v[114:115], v[106:107]

.LBB0_285:
	v_pk_mul_f32 v[102:103], v[150:151], v[102:103]
	s_waitcnt lgkmcnt(0)
	v_pk_mul_f32 v[106:107], v[132:133], v[100:101]
	v_pk_mul_f32 v[100:101], v[150:151], v[98:99]
	v_cvt_pk_bf16_f32 v98, v102, v103
	v_or_b32_e32 v102, 0x4000, v130
	v_ashrrev_i32_e32 v103, 31, v102
	v_lshlrev_b64 v[102:103], 7, v[102:103]
	v_lshl_add_u64 v[102:103], s[20:21], 0, v[102:103]
	v_lshl_add_u64 v[102:103], v[148:149], 1, v[102:103]
	v_pk_mul_f32 v[104:105], v[132:133], v[104:105]
	s_nop 0
	v_cvt_pk_bf16_f32 v99, v104, v105
	v_cvt_pk_bf16_f32 v100, v100, v101
	v_cvt_pk_bf16_f32 v101, v106, v107
	global_store_dwordx4 v[102:103], v[98:101], off nt sc1
	s_and_b64 vcc, exec, s[6:7]
	s_cbranch_vccnz .LBB0_287
	s_add_i32 s22, 0, 0x20000
	v_lshl_add_u32 v106, v64, 6, s22
	ds_read_b128 v[102:105], v106 offset:2048
	ds_read_b128 v[98:101], v106 offset:2064
	ds_read_b128 v[110:113], v106 offset:2080
	ds_read_b128 v[106:109], v106 offset:2096
	s_and_b64 vcc, exec, s[6:7]
	s_cbranch_vccz .LBB0_288
	s_branch .LBB0_291

.LBB0_291:
	s_waitcnt lgkmcnt(0)
	v_add_u32_e32 v114, 32, v154
	v_and_b32_e32 v115, 0x1fff, v114
	v_lshrrev_b32_e32 v114, 9, v114
	v_and_b32_e32 v114, 0x7fff0, v114
	v_or_b32_e32 v114, s39, v114
	v_lshl_or_b32 v114, v114, 13, v115
	v_mov_b32_e32 v116, v150
	v_mov_b32_e32 v117, v150
	v_pk_mul_f32 v[94:95], v[150:151], v[94:95]
	v_ashrrev_i32_e32 v115, 31, v114
	v_pk_mul_f32 v[118:119], v[116:117], v[92:93]
	v_pk_mul_f32 v[92:93], v[150:151], v[90:91]
	v_cvt_pk_bf16_f32 v90, v94, v95
	v_lshlrev_b64 v[94:95], 7, v[114:115]
	v_lshl_add_u64 v[94:95], s[20:21], 0, v[94:95]
	v_lshl_add_u64 v[94:95], v[148:149], 1, v[94:95]
	s_and_b64 vcc, exec, s[6:7]
	v_pk_mul_f32 v[96:97], v[116:117], v[96:97]
	s_nop 0
	v_cvt_pk_bf16_f32 v91, v96, v97
	v_cvt_pk_bf16_f32 v92, v92, v93
	v_cvt_pk_bf16_f32 v93, v118, v119
	global_store_dwordx4 v[94:95], v[90:93], off nt sc1
	s_cbranch_vccnz .LBB0_295
	ds_swizzle_b32 v94, v86 offset:swizzle(SWAP,16)
	ds_swizzle_b32 v90, v82 offset:swizzle(SWAP,16)
	ds_swizzle_b32 v95, v87 offset:swizzle(SWAP,16)
	ds_swizzle_b32 v91, v83 offset:swizzle(SWAP,16)
	ds_swizzle_b32 v96, v88 offset:swizzle(SWAP,16)
	ds_swizzle_b32 v92, v84 offset:swizzle(SWAP,16)
	ds_swizzle_b32 v97, v89 offset:swizzle(SWAP,16)
	ds_swizzle_b32 v93, v85 offset:swizzle(SWAP,16)
	s_and_saveexec_b64 s[22:23], s[8:9]
	s_cbranch_execz .LBB0_294
	s_waitcnt lgkmcnt(0)
	v_pk_mul_f32 v[96:97], v[112:113], v[96:97]
	v_pk_mul_f32 v[94:95], v[110:111], v[94:95]
	v_mov_b32_e32 v110, v146
	v_mov_b32_e32 v111, v146
	v_pk_mul_f32 v[92:93], v[108:109], v[92:93]
	v_pk_mul_f32 v[90:91], v[106:107], v[90:91]
	v_pk_mul_f32 v[96:97], v[110:111], v[96:97]
	v_pk_mul_f32 v[94:95], v[146:147], v[94:95]
	v_pk_mul_f32 v[92:93], v[110:111], v[92:93]
	v_pk_mul_f32 v[90:91], v[146:147], v[90:91]
	v_pk_fma_f32 v[88:89], v[88:89], v[104:105], v[96:97]
	v_pk_fma_f32 v[86:87], v[86:87], v[102:103], v[94:95]
	v_pk_fma_f32 v[84:85], v[84:85], v[100:101], v[92:93]
	v_pk_fma_f32 v[82:83], v[82:83], v[98:99], v[90:91]

.LBB0_295:
	v_pk_mul_f32 v[86:87], v[150:151], v[86:87]
	s_waitcnt lgkmcnt(0)
	v_pk_mul_f32 v[90:91], v[116:117], v[84:85]
	v_pk_mul_f32 v[84:85], v[150:151], v[82:83]
	v_cvt_pk_bf16_f32 v82, v86, v87
	v_or_b32_e32 v86, 0x4000, v114
	v_ashrrev_i32_e32 v87, 31, v86
	v_lshlrev_b64 v[86:87], 7, v[86:87]
	v_lshl_add_u64 v[86:87], s[20:21], 0, v[86:87]
	v_lshl_add_u64 v[86:87], v[148:149], 1, v[86:87]
	v_pk_mul_f32 v[88:89], v[116:117], v[88:89]
	s_nop 0
	v_cvt_pk_bf16_f32 v83, v88, v89
	v_cvt_pk_bf16_f32 v84, v84, v85
	v_cvt_pk_bf16_f32 v85, v90, v91
	global_store_dwordx4 v[86:87], v[82:85], off nt sc1
	s_and_b64 vcc, exec, s[6:7]
	s_cbranch_vccnz .LBB0_297
	s_add_i32 s22, 0, 0x20000
	v_lshl_add_u32 v90, v64, 6, s22
	ds_read_b128 v[86:89], v90 offset:3072
	ds_read_b128 v[82:85], v90 offset:3088
	ds_read_b128 v[94:97], v90 offset:3104
	ds_read_b128 v[90:93], v90 offset:3120
	s_and_b64 vcc, exec, s[6:7]
	s_cbranch_vccz .LBB0_298
	s_branch .LBB0_301

.LBB0_301:
	s_waitcnt lgkmcnt(0)
	v_add_u32_e32 v98, 48, v154
	v_and_b32_e32 v99, 0x1fff, v98
	v_lshrrev_b32_e32 v98, 9, v98
	v_and_b32_e32 v98, 0x7fff0, v98
	v_or_b32_e32 v98, s39, v98
	v_lshl_or_b32 v98, v98, 13, v99
	v_mov_b32_e32 v100, v150
	v_mov_b32_e32 v101, v150
	v_pk_mul_f32 v[78:79], v[150:151], v[78:79]
	v_ashrrev_i32_e32 v99, 31, v98
	v_pk_mul_f32 v[102:103], v[100:101], v[76:77]
	v_pk_mul_f32 v[76:77], v[150:151], v[74:75]
	v_cvt_pk_bf16_f32 v74, v78, v79
	v_lshlrev_b64 v[78:79], 7, v[98:99]
	v_lshl_add_u64 v[78:79], s[20:21], 0, v[78:79]
	v_lshl_add_u64 v[78:79], v[148:149], 1, v[78:79]
	s_and_b64 vcc, exec, s[6:7]
	v_pk_mul_f32 v[80:81], v[100:101], v[80:81]
	s_nop 0
	v_cvt_pk_bf16_f32 v75, v80, v81
	v_cvt_pk_bf16_f32 v76, v76, v77
	v_cvt_pk_bf16_f32 v77, v102, v103
	global_store_dwordx4 v[78:79], v[74:77], off nt sc1
	s_cbranch_vccnz .LBB0_305
	ds_swizzle_b32 v78, v70 offset:swizzle(SWAP,16)
	ds_swizzle_b32 v74, v66 offset:swizzle(SWAP,16)
	ds_swizzle_b32 v79, v71 offset:swizzle(SWAP,16)
	ds_swizzle_b32 v75, v67 offset:swizzle(SWAP,16)
	ds_swizzle_b32 v80, v72 offset:swizzle(SWAP,16)
	ds_swizzle_b32 v76, v68 offset:swizzle(SWAP,16)
	ds_swizzle_b32 v81, v73 offset:swizzle(SWAP,16)
	ds_swizzle_b32 v77, v69 offset:swizzle(SWAP,16)
	s_and_saveexec_b64 s[22:23], s[8:9]
	s_cbranch_execz .LBB0_304
	s_waitcnt lgkmcnt(0)
	v_pk_mul_f32 v[80:81], v[96:97], v[80:81]
	v_pk_mul_f32 v[78:79], v[94:95], v[78:79]
	v_mov_b32_e32 v94, v146
	v_mov_b32_e32 v95, v146
	v_pk_mul_f32 v[76:77], v[92:93], v[76:77]
	v_pk_mul_f32 v[74:75], v[90:91], v[74:75]
	v_pk_mul_f32 v[80:81], v[94:95], v[80:81]
	v_pk_mul_f32 v[78:79], v[146:147], v[78:79]
	v_pk_mul_f32 v[76:77], v[94:95], v[76:77]
	v_pk_mul_f32 v[74:75], v[146:147], v[74:75]
	v_pk_fma_f32 v[72:73], v[72:73], v[88:89], v[80:81]
	v_pk_fma_f32 v[70:71], v[70:71], v[86:87], v[78:79]
	v_pk_fma_f32 v[68:69], v[68:69], v[84:85], v[76:77]
	v_pk_fma_f32 v[66:67], v[66:67], v[82:83], v[74:75]

.LBB0_305:
	v_pk_mul_f32 v[70:71], v[150:151], v[70:71]
	s_waitcnt lgkmcnt(0)
	v_pk_mul_f32 v[74:75], v[100:101], v[68:69]
	v_pk_mul_f32 v[68:69], v[150:151], v[66:67]
	v_cvt_pk_bf16_f32 v66, v70, v71
	v_or_b32_e32 v70, 0x4000, v98
	v_ashrrev_i32_e32 v71, 31, v70
	v_lshlrev_b64 v[70:71], 7, v[70:71]
	v_lshl_add_u64 v[70:71], s[20:21], 0, v[70:71]
	v_lshl_add_u64 v[70:71], v[148:149], 1, v[70:71]
	v_pk_mul_f32 v[72:73], v[100:101], v[72:73]
	s_nop 0
	v_cvt_pk_bf16_f32 v67, v72, v73
	v_cvt_pk_bf16_f32 v68, v68, v69
	v_cvt_pk_bf16_f32 v69, v74, v75
	global_store_dwordx4 v[70:71], v[66:69], off nt sc1
	s_and_b64 vcc, exec, s[6:7]
	s_cbranch_vccnz .LBB0_307
	s_add_i32 s22, 0, 0x20000
	v_lshl_add_u32 v74, v64, 6, s22
	ds_read_b128 v[70:73], v74 offset:8192
	ds_read_b128 v[66:69], v74 offset:8208
	ds_read_b128 v[78:81], v74 offset:8224
	ds_read_b128 v[74:77], v74 offset:8240
	s_and_b64 vcc, exec, s[6:7]
	s_cbranch_vccz .LBB0_308
	s_branch .LBB0_311

.LBB0_311:
	s_waitcnt lgkmcnt(0)
	v_add_u32_e32 v82, 0x80, v154
	v_and_b32_e32 v83, 0x1fff, v82
	v_lshrrev_b32_e32 v82, 9, v82
	v_and_b32_e32 v82, 0x7fff0, v82
	v_or_b32_e32 v82, s39, v82
	v_lshl_or_b32 v82, v82, 13, v83
	v_mov_b32_e32 v84, v150
	v_mov_b32_e32 v85, v150
	v_pk_mul_f32 v[60:61], v[150:151], v[60:61]
	v_ashrrev_i32_e32 v83, 31, v82
	v_pk_mul_f32 v[86:87], v[84:85], v[58:59]
	v_pk_mul_f32 v[58:59], v[150:151], v[56:57]
	v_cvt_pk_bf16_f32 v56, v60, v61
	v_lshlrev_b64 v[60:61], 7, v[82:83]
	v_lshl_add_u64 v[60:61], s[20:21], 0, v[60:61]
	v_lshl_add_u64 v[60:61], v[148:149], 1, v[60:61]
	s_and_b64 vcc, exec, s[6:7]
	v_pk_mul_f32 v[62:63], v[84:85], v[62:63]
	s_nop 0
	v_cvt_pk_bf16_f32 v57, v62, v63
	v_cvt_pk_bf16_f32 v58, v58, v59
	v_cvt_pk_bf16_f32 v59, v86, v87
	global_store_dwordx4 v[60:61], v[56:59], off nt sc1
	s_cbranch_vccnz .LBB0_315
	ds_swizzle_b32 v60, v52 offset:swizzle(SWAP,16)
	ds_swizzle_b32 v56, v48 offset:swizzle(SWAP,16)
	ds_swizzle_b32 v61, v53 offset:swizzle(SWAP,16)
	ds_swizzle_b32 v57, v49 offset:swizzle(SWAP,16)
	ds_swizzle_b32 v62, v54 offset:swizzle(SWAP,16)
	ds_swizzle_b32 v58, v50 offset:swizzle(SWAP,16)
	ds_swizzle_b32 v63, v55 offset:swizzle(SWAP,16)
	ds_swizzle_b32 v59, v51 offset:swizzle(SWAP,16)
	s_and_saveexec_b64 s[22:23], s[8:9]
	s_cbranch_execz .LBB0_314
	s_waitcnt lgkmcnt(0)
	v_pk_mul_f32 v[62:63], v[80:81], v[62:63]
	v_pk_mul_f32 v[60:61], v[78:79], v[60:61]
	v_mov_b32_e32 v78, v146
	v_mov_b32_e32 v79, v146
	v_pk_mul_f32 v[58:59], v[76:77], v[58:59]
	v_pk_mul_f32 v[56:57], v[74:75], v[56:57]
	v_pk_mul_f32 v[62:63], v[78:79], v[62:63]
	v_pk_mul_f32 v[60:61], v[146:147], v[60:61]
	v_pk_mul_f32 v[58:59], v[78:79], v[58:59]
	v_pk_mul_f32 v[56:57], v[146:147], v[56:57]
	v_pk_fma_f32 v[54:55], v[54:55], v[72:73], v[62:63]
	v_pk_fma_f32 v[52:53], v[52:53], v[70:71], v[60:61]
	v_pk_fma_f32 v[50:51], v[50:51], v[68:69], v[58:59]
	v_pk_fma_f32 v[48:49], v[48:49], v[66:67], v[56:57]

.LBB0_315:
	v_pk_mul_f32 v[52:53], v[150:151], v[52:53]
	s_waitcnt lgkmcnt(0)
	v_pk_mul_f32 v[56:57], v[84:85], v[50:51]
	v_pk_mul_f32 v[50:51], v[150:151], v[48:49]
	v_cvt_pk_bf16_f32 v48, v52, v53
	v_or_b32_e32 v52, 0x4000, v82
	v_ashrrev_i32_e32 v53, 31, v52
	v_lshlrev_b64 v[52:53], 7, v[52:53]
	v_lshl_add_u64 v[52:53], s[20:21], 0, v[52:53]
	v_lshl_add_u64 v[52:53], v[148:149], 1, v[52:53]
	v_pk_mul_f32 v[54:55], v[84:85], v[54:55]
	s_nop 0
	v_cvt_pk_bf16_f32 v49, v54, v55
	v_cvt_pk_bf16_f32 v50, v50, v51
	v_cvt_pk_bf16_f32 v51, v56, v57
	global_store_dwordx4 v[52:53], v[48:51], off nt sc1
	s_and_b64 vcc, exec, s[6:7]
	s_cbranch_vccnz .LBB0_317
	s_add_i32 s22, 0, 0x20000
	v_lshl_add_u32 v56, v64, 6, s22
	ds_read_b128 v[52:55], v56 offset:9216
	ds_read_b128 v[48:51], v56 offset:9232
	ds_read_b128 v[60:63], v56 offset:9248
	ds_read_b128 v[56:59], v56 offset:9264
	s_and_b64 vcc, exec, s[6:7]
	s_cbranch_vccz .LBB0_318
	s_branch .LBB0_321

.LBB0_321:
	s_waitcnt lgkmcnt(0)
	v_add_u32_e32 v66, 0x90, v154
	v_and_b32_e32 v67, 0x1fff, v66
	v_lshrrev_b32_e32 v66, 9, v66
	v_and_b32_e32 v66, 0x7fff0, v66
	v_or_b32_e32 v66, s39, v66
	v_lshl_or_b32 v66, v66, 13, v67
	v_mov_b32_e32 v68, v150
	v_mov_b32_e32 v69, v150
	v_pk_mul_f32 v[44:45], v[150:151], v[44:45]
	v_ashrrev_i32_e32 v67, 31, v66
	v_pk_mul_f32 v[70:71], v[68:69], v[42:43]
	v_pk_mul_f32 v[42:43], v[150:151], v[40:41]
	v_cvt_pk_bf16_f32 v40, v44, v45
	v_lshlrev_b64 v[44:45], 7, v[66:67]
	v_lshl_add_u64 v[44:45], s[20:21], 0, v[44:45]
	v_lshl_add_u64 v[44:45], v[148:149], 1, v[44:45]
	s_and_b64 vcc, exec, s[6:7]
	v_pk_mul_f32 v[46:47], v[68:69], v[46:47]
	s_nop 0
	v_cvt_pk_bf16_f32 v41, v46, v47
	v_cvt_pk_bf16_f32 v42, v42, v43
	v_cvt_pk_bf16_f32 v43, v70, v71
	global_store_dwordx4 v[44:45], v[40:43], off nt sc1
	s_cbranch_vccnz .LBB0_325
	ds_swizzle_b32 v44, v36 offset:swizzle(SWAP,16)
	ds_swizzle_b32 v40, v32 offset:swizzle(SWAP,16)
	ds_swizzle_b32 v45, v37 offset:swizzle(SWAP,16)
	ds_swizzle_b32 v41, v33 offset:swizzle(SWAP,16)
	ds_swizzle_b32 v46, v38 offset:swizzle(SWAP,16)
	ds_swizzle_b32 v42, v34 offset:swizzle(SWAP,16)
	ds_swizzle_b32 v47, v39 offset:swizzle(SWAP,16)
	ds_swizzle_b32 v43, v35 offset:swizzle(SWAP,16)
	s_and_saveexec_b64 s[22:23], s[8:9]
	s_cbranch_execz .LBB0_324
	s_waitcnt lgkmcnt(0)
	v_pk_mul_f32 v[46:47], v[62:63], v[46:47]
	v_pk_mul_f32 v[44:45], v[60:61], v[44:45]
	v_mov_b32_e32 v60, v146
	v_mov_b32_e32 v61, v146
	v_pk_mul_f32 v[42:43], v[58:59], v[42:43]
	v_pk_mul_f32 v[40:41], v[56:57], v[40:41]
	v_pk_mul_f32 v[46:47], v[60:61], v[46:47]
	v_pk_mul_f32 v[44:45], v[146:147], v[44:45]
	v_pk_mul_f32 v[42:43], v[60:61], v[42:43]
	v_pk_mul_f32 v[40:41], v[146:147], v[40:41]
	v_pk_fma_f32 v[38:39], v[38:39], v[54:55], v[46:47]
	v_pk_fma_f32 v[36:37], v[36:37], v[52:53], v[44:45]
	v_pk_fma_f32 v[34:35], v[34:35], v[50:51], v[42:43]
	v_pk_fma_f32 v[32:33], v[32:33], v[48:49], v[40:41]

.LBB0_325:
	v_pk_mul_f32 v[36:37], v[150:151], v[36:37]
	s_waitcnt lgkmcnt(0)
	v_pk_mul_f32 v[40:41], v[68:69], v[34:35]
	v_pk_mul_f32 v[34:35], v[150:151], v[32:33]
	v_cvt_pk_bf16_f32 v32, v36, v37
	v_or_b32_e32 v36, 0x4000, v66
	v_ashrrev_i32_e32 v37, 31, v36
	v_lshlrev_b64 v[36:37], 7, v[36:37]
	v_lshl_add_u64 v[36:37], s[20:21], 0, v[36:37]
	v_lshl_add_u64 v[36:37], v[148:149], 1, v[36:37]
	v_pk_mul_f32 v[38:39], v[68:69], v[38:39]
	s_nop 0
	v_cvt_pk_bf16_f32 v33, v38, v39
	v_cvt_pk_bf16_f32 v34, v34, v35
	v_cvt_pk_bf16_f32 v35, v40, v41
	global_store_dwordx4 v[36:37], v[32:35], off nt sc1
	s_and_b64 vcc, exec, s[6:7]
	s_cbranch_vccnz .LBB0_327
	s_add_i32 s22, 0, 0x20000
	v_lshl_add_u32 v40, v64, 6, s22
	ds_read_b128 v[36:39], v40 offset:10240
	ds_read_b128 v[32:35], v40 offset:10256
	ds_read_b128 v[44:47], v40 offset:10272
	ds_read_b128 v[40:43], v40 offset:10288
	s_and_b64 vcc, exec, s[6:7]
	s_cbranch_vccz .LBB0_328
	s_branch .LBB0_331

.LBB0_331:
	s_waitcnt lgkmcnt(0)
	v_add_u32_e32 v48, 0xa0, v154
	v_and_b32_e32 v49, 0x1fff, v48
	v_lshrrev_b32_e32 v48, 9, v48
	v_and_b32_e32 v48, 0x7fff0, v48
	v_or_b32_e32 v48, s39, v48
	v_lshl_or_b32 v48, v48, 13, v49
	v_mov_b32_e32 v50, v150
	v_mov_b32_e32 v51, v150
	v_pk_mul_f32 v[28:29], v[150:151], v[28:29]
	v_ashrrev_i32_e32 v49, 31, v48
	v_pk_mul_f32 v[52:53], v[50:51], v[26:27]
	v_pk_mul_f32 v[26:27], v[150:151], v[24:25]
	v_cvt_pk_bf16_f32 v24, v28, v29
	v_lshlrev_b64 v[28:29], 7, v[48:49]
	v_lshl_add_u64 v[28:29], s[20:21], 0, v[28:29]
	v_lshl_add_u64 v[28:29], v[148:149], 1, v[28:29]
	s_and_b64 vcc, exec, s[6:7]
	v_pk_mul_f32 v[30:31], v[50:51], v[30:31]
	s_nop 0
	v_cvt_pk_bf16_f32 v25, v30, v31
	v_cvt_pk_bf16_f32 v26, v26, v27
	v_cvt_pk_bf16_f32 v27, v52, v53
	global_store_dwordx4 v[28:29], v[24:27], off nt sc1
	s_cbranch_vccnz .LBB0_335
	ds_swizzle_b32 v28, v20 offset:swizzle(SWAP,16)
	ds_swizzle_b32 v24, v16 offset:swizzle(SWAP,16)
	ds_swizzle_b32 v29, v21 offset:swizzle(SWAP,16)
	ds_swizzle_b32 v25, v17 offset:swizzle(SWAP,16)
	ds_swizzle_b32 v30, v22 offset:swizzle(SWAP,16)
	ds_swizzle_b32 v26, v18 offset:swizzle(SWAP,16)
	ds_swizzle_b32 v31, v23 offset:swizzle(SWAP,16)
	ds_swizzle_b32 v27, v19 offset:swizzle(SWAP,16)
	s_and_saveexec_b64 s[22:23], s[8:9]
	s_cbranch_execz .LBB0_334
	s_waitcnt lgkmcnt(0)
	v_pk_mul_f32 v[30:31], v[46:47], v[30:31]
	v_pk_mul_f32 v[28:29], v[44:45], v[28:29]
	v_mov_b32_e32 v44, v146
	v_mov_b32_e32 v45, v146
	v_pk_mul_f32 v[26:27], v[42:43], v[26:27]
	v_pk_mul_f32 v[24:25], v[40:41], v[24:25]
	v_pk_mul_f32 v[30:31], v[44:45], v[30:31]
	v_pk_mul_f32 v[28:29], v[146:147], v[28:29]
	v_pk_mul_f32 v[26:27], v[44:45], v[26:27]
	v_pk_mul_f32 v[24:25], v[146:147], v[24:25]
	v_pk_fma_f32 v[22:23], v[22:23], v[38:39], v[30:31]
	v_pk_fma_f32 v[20:21], v[20:21], v[36:37], v[28:29]
	v_pk_fma_f32 v[18:19], v[18:19], v[34:35], v[26:27]
	v_pk_fma_f32 v[16:17], v[16:17], v[32:33], v[24:25]

.LBB0_335:
	v_pk_mul_f32 v[20:21], v[150:151], v[20:21]
	s_waitcnt lgkmcnt(0)
	v_pk_mul_f32 v[24:25], v[50:51], v[18:19]
	v_pk_mul_f32 v[18:19], v[150:151], v[16:17]
	v_cvt_pk_bf16_f32 v16, v20, v21
	v_or_b32_e32 v20, 0x4000, v48
	v_ashrrev_i32_e32 v21, 31, v20
	v_lshlrev_b64 v[20:21], 7, v[20:21]
	v_lshl_add_u64 v[20:21], s[20:21], 0, v[20:21]
	v_lshl_add_u64 v[20:21], v[148:149], 1, v[20:21]
	v_pk_mul_f32 v[22:23], v[50:51], v[22:23]
	s_nop 0
	v_cvt_pk_bf16_f32 v17, v22, v23
	v_cvt_pk_bf16_f32 v18, v18, v19
	v_cvt_pk_bf16_f32 v19, v24, v25
	global_store_dwordx4 v[20:21], v[16:19], off nt sc1
	s_and_b64 vcc, exec, s[6:7]
	s_cbranch_vccnz .LBB0_337
	s_add_i32 s22, 0, 0x20000
	v_lshl_add_u32 v24, v64, 6, s22
	ds_read_b128 v[20:23], v24 offset:11264
	ds_read_b128 v[16:19], v24 offset:11280
	ds_read_b128 v[28:31], v24 offset:11296
	ds_read_b128 v[24:27], v24 offset:11312
	s_and_b64 vcc, exec, s[6:7]
	s_cbranch_vccz .LBB0_338
	s_branch .LBB0_341

.LBB0_341:
	s_waitcnt lgkmcnt(0)
	v_add_u32_e32 v32, 0xb0, v154
	v_and_b32_e32 v33, 0x1fff, v32
	v_lshrrev_b32_e32 v32, 9, v32
	v_and_b32_e32 v32, 0x7fff0, v32
	v_or_b32_e32 v32, s39, v32
	v_lshl_or_b32 v32, v32, 13, v33
	v_mov_b32_e32 v34, v150
	v_mov_b32_e32 v35, v150
	v_pk_mul_f32 v[12:13], v[150:151], v[12:13]
	v_ashrrev_i32_e32 v33, 31, v32
	v_pk_mul_f32 v[36:37], v[34:35], v[10:11]
	v_pk_mul_f32 v[10:11], v[150:151], v[8:9]
	v_cvt_pk_bf16_f32 v8, v12, v13
	v_lshlrev_b64 v[12:13], 7, v[32:33]
	v_lshl_add_u64 v[12:13], s[20:21], 0, v[12:13]
	v_lshl_add_u64 v[12:13], v[148:149], 1, v[12:13]
	s_and_b64 vcc, exec, s[6:7]
	v_pk_mul_f32 v[14:15], v[34:35], v[14:15]
	s_nop 0
	v_cvt_pk_bf16_f32 v9, v14, v15
	v_cvt_pk_bf16_f32 v10, v10, v11
	v_cvt_pk_bf16_f32 v11, v36, v37
	global_store_dwordx4 v[12:13], v[8:11], off nt sc1
	s_cbranch_vccnz .LBB0_345
	ds_swizzle_b32 v12, v4 offset:swizzle(SWAP,16)
	ds_swizzle_b32 v8, v0 offset:swizzle(SWAP,16)
	ds_swizzle_b32 v13, v5 offset:swizzle(SWAP,16)
	ds_swizzle_b32 v9, v1 offset:swizzle(SWAP,16)
	ds_swizzle_b32 v14, v6 offset:swizzle(SWAP,16)
	ds_swizzle_b32 v10, v2 offset:swizzle(SWAP,16)
	ds_swizzle_b32 v15, v7 offset:swizzle(SWAP,16)
	ds_swizzle_b32 v11, v3 offset:swizzle(SWAP,16)
	s_and_saveexec_b64 s[6:7], s[8:9]
	s_cbranch_execz .LBB0_344
	s_waitcnt lgkmcnt(0)
	v_pk_mul_f32 v[14:15], v[30:31], v[14:15]
	v_pk_mul_f32 v[12:13], v[28:29], v[12:13]
	v_mov_b32_e32 v28, v146
	v_mov_b32_e32 v29, v146
	v_pk_mul_f32 v[10:11], v[26:27], v[10:11]
	v_pk_mul_f32 v[8:9], v[24:25], v[8:9]
	v_pk_mul_f32 v[14:15], v[28:29], v[14:15]
	v_pk_mul_f32 v[12:13], v[146:147], v[12:13]
	v_pk_mul_f32 v[10:11], v[28:29], v[10:11]
	v_pk_mul_f32 v[8:9], v[146:147], v[8:9]
	v_pk_fma_f32 v[6:7], v[6:7], v[22:23], v[14:15]
	v_pk_fma_f32 v[4:5], v[4:5], v[20:21], v[12:13]
	v_pk_fma_f32 v[2:3], v[2:3], v[18:19], v[10:11]
	v_pk_fma_f32 v[0:1], v[0:1], v[16:17], v[8:9]

.LBB0_345:
	v_pk_mul_f32 v[4:5], v[150:151], v[4:5]
	s_waitcnt lgkmcnt(0)
	v_pk_mul_f32 v[8:9], v[34:35], v[2:3]
	v_pk_mul_f32 v[2:3], v[150:151], v[0:1]
	v_cvt_pk_bf16_f32 v0, v4, v5
	v_or_b32_e32 v4, 0x4000, v32
	v_ashrrev_i32_e32 v5, 31, v4
	v_lshlrev_b64 v[4:5], 7, v[4:5]
	v_lshl_add_u64 v[4:5], s[20:21], 0, v[4:5]
	v_lshl_add_u64 v[4:5], v[148:149], 1, v[4:5]
	v_pk_mul_f32 v[6:7], v[34:35], v[6:7]
	s_nop 0
	v_cvt_pk_bf16_f32 v1, v6, v7
	v_cvt_pk_bf16_f32 v2, v2, v3
	v_cvt_pk_bf16_f32 v3, v8, v9
	global_store_dwordx4 v[4:5], v[0:3], off nt sc1
	s_cmp_eq_u32 s38, 11
	s_mov_b64 s[6:7], -1
	s_cbranch_scc1 .LBB0_259
	s_andn2_b64 vcc, exec, s[12:13]
	s_cbranch_vccnz .LBB0_258
	s_barrier
	s_branch .LBB0_258

.LBB0_361:
	v_mul_f32_e32 v151, 0xbfb8aa3b, v107
	v_exp_f32_e32 v151, v151
	v_mul_f32_e32 v152, 0xbfb8aa3b, v116
	v_mul_f32_e32 v153, 0xbfb8aa3b, v108
	v_exp_f32_e32 v152, v152
	v_add_f32_e32 v151, 1.0, v151
	v_rcp_f32_e32 v151, v151
	v_exp_f32_e32 v153, v153
	v_mul_f32_e32 v130, 0xbfb8aa3b, v114
	v_mul_f32_e32 v131, 0xbfb8aa3b, v106
	v_mul_f32_e32 v150, 0xbfb8aa3b, v115
	v_mul_f32_e32 v154, v123, v151
	v_add_f32_e32 v151, 1.0, v152
	v_add_f32_e32 v152, 1.0, v153
	v_mul_f32_e32 v153, 0xbfb8aa3b, v117
	v_exp_f32_e32 v130, v130
	v_exp_f32_e32 v131, v131
	v_exp_f32_e32 v150, v150
	v_exp_f32_e32 v153, v153
	v_mul_f32_e32 v155, 0xbfb8aa3b, v109
	v_exp_f32_e32 v155, v155
	v_add_f32_e32 v130, 1.0, v130
	v_add_f32_e32 v131, 1.0, v131
	v_add_f32_e32 v150, 1.0, v150
	v_add_f32_e32 v153, 1.0, v153
	v_rcp_f32_e32 v130, v130
	v_rcp_f32_e32 v131, v131
	v_rcp_f32_e32 v150, v150
	v_rcp_f32_e32 v151, v151
	v_rcp_f32_e32 v152, v152
	v_rcp_f32_e32 v153, v153
	v_add_f32_e32 v155, 1.0, v155
	s_lshl_b32 s14, s31, 7
	v_rcp_f32_e32 v155, v155
	s_add_i32 s14, s29, s14
	v_add_u32_e32 v132, s14, v149
	v_mul_f32_e32 v130, v126, v130
	v_mul_f32_e32 v131, v122, v131
	v_mul_f32_e32 v150, v127, v150
	v_mul_f32_e32 v151, v128, v151
	v_mul_f32_e32 v156, v124, v152
	v_mul_f32_e32 v152, v129, v153
	v_ashrrev_i32_e32 v133, 31, v132
	v_cvt_pk_bf16_f32 v150, v130, v150
	v_cvt_pk_bf16_f32 v151, v151, v152
	v_cvt_pk_bf16_f32 v152, v131, v154
	v_mov_b64_e32 v[130:131], s[64:65]
	v_mul_f32_e32 v153, v125, v155
	v_mad_i64_i32 v[154:155], s[14:15], v148, s1, v[130:131]
	v_lshlrev_b64 v[132:133], 1, v[132:133]
	v_lshl_add_u64 v[154:155], v[154:155], 0, v[132:133]
	v_cvt_pk_bf16_f32 v153, v156, v153
	global_store_dwordx4 v[154:155], v[150:153], off nt sc1
	v_mul_f32_e32 v156, 0xbfb8aa3b, v98
	v_exp_f32_e32 v156, v156
	v_mul_f32_e32 v151, 0xbfb8aa3b, v90
	v_mul_f32_e32 v152, 0xbfb8aa3b, v99
	v_exp_f32_e32 v151, v151
	v_exp_f32_e32 v152, v152
	v_mul_f32_e32 v153, 0xbfb8aa3b, v91
	v_exp_f32_e32 v153, v153
	v_add_f32_e32 v151, 1.0, v151
	v_add_f32_e32 v152, 1.0, v152
	v_rcp_f32_e32 v151, v151
	v_rcp_f32_e32 v152, v152
	v_add_f32_e32 v150, 1.0, v156
	v_mul_f32_e32 v155, 0xbfb8aa3b, v92
	v_mul_f32_e32 v154, v110, v151
	v_mul_f32_e32 v151, v119, v152
	v_add_f32_e32 v152, 1.0, v153
	v_mul_f32_e32 v153, 0xbfb8aa3b, v100
	v_mul_f32_e32 v156, 0xbfb8aa3b, v101
	v_exp_f32_e32 v153, v153
	v_exp_f32_e32 v155, v155
	v_exp_f32_e32 v156, v156
	v_mul_f32_e32 v157, 0xbfb8aa3b, v93
	v_exp_f32_e32 v157, v157
	v_rcp_f32_e32 v150, v150
	v_rcp_f32_e32 v152, v152
	v_add_f32_e32 v153, 1.0, v153
	v_add_f32_e32 v155, 1.0, v155
	v_add_f32_e32 v156, 1.0, v156
	v_rcp_f32_e32 v153, v153
	v_rcp_f32_e32 v155, v155
	v_rcp_f32_e32 v156, v156
	v_add_f32_e32 v157, 1.0, v157
	v_rcp_f32_e32 v157, v157
	v_mul_f32_e32 v150, v118, v150
	v_mul_f32_e32 v152, v111, v152
	v_mul_f32_e32 v153, v120, v153
	v_mul_f32_e32 v155, v112, v155
	v_mul_f32_e32 v156, v121, v156
	v_cvt_pk_bf16_f32 v150, v150, v151
	v_cvt_pk_bf16_f32 v151, v153, v156
	v_cvt_pk_bf16_f32 v152, v154, v152
	v_mul_f32_e32 v154, 0xbfb8aa3b, v82
	v_mul_f32_e32 v157, v113, v157
	v_cvt_pk_bf16_f32 v153, v155, v157
	v_exp_f32_e32 v156, v154
	v_mad_i64_i32 v[154:155], s[14:15], v147, s1, v[130:131]
	v_lshl_add_u64 v[154:155], v[154:155], 0, v[132:133]
	global_store_dwordx4 v[154:155], v[150:153], off nt sc1
	v_mul_f32_e32 v155, 0xbfb8aa3b, v76
	v_exp_f32_e32 v155, v155
	v_mul_f32_e32 v151, 0xbfb8aa3b, v74
	v_mul_f32_e32 v152, 0xbfb8aa3b, v83
	v_exp_f32_e32 v151, v151
	v_exp_f32_e32 v152, v152
	v_mul_f32_e32 v153, 0xbfb8aa3b, v75
	v_exp_f32_e32 v153, v153
	v_add_f32_e32 v151, 1.0, v151
	v_add_f32_e32 v152, 1.0, v152
	v_rcp_f32_e32 v151, v151
	v_rcp_f32_e32 v152, v152
	v_add_f32_e32 v150, 1.0, v156
	v_mul_f32_e32 v156, 0xbfb8aa3b, v85
	v_mul_f32_e32 v154, v94, v151
	v_mul_f32_e32 v151, v103, v152
	v_add_f32_e32 v152, 1.0, v153
	v_mul_f32_e32 v153, 0xbfb8aa3b, v84
	v_exp_f32_e32 v153, v153
	v_exp_f32_e32 v156, v156
	v_mul_f32_e32 v157, 0xbfb8aa3b, v77
	v_exp_f32_e32 v157, v157
	v_rcp_f32_e32 v150, v150
	v_rcp_f32_e32 v152, v152
	v_add_f32_e32 v153, 1.0, v153
	v_add_f32_e32 v155, 1.0, v155
	v_add_f32_e32 v156, 1.0, v156
	v_rcp_f32_e32 v153, v153
	v_rcp_f32_e32 v155, v155
	v_rcp_f32_e32 v156, v156
	v_add_f32_e32 v157, 1.0, v157
	v_rcp_f32_e32 v157, v157
	v_mul_f32_e32 v150, v102, v150
	v_mul_f32_e32 v152, v95, v152
	v_mul_f32_e32 v153, v104, v153
	v_mul_f32_e32 v155, v96, v155
	v_mul_f32_e32 v156, v105, v156
	v_cvt_pk_bf16_f32 v150, v150, v151
	v_cvt_pk_bf16_f32 v151, v153, v156
	v_cvt_pk_bf16_f32 v152, v154, v152
	v_mul_f32_e32 v154, 0xbfb8aa3b, v70
	v_mul_f32_e32 v157, v97, v157
	v_cvt_pk_bf16_f32 v153, v155, v157
	v_exp_f32_e32 v156, v154
	v_mad_i64_i32 v[154:155], s[14:15], v146, s1, v[130:131]
	v_lshl_add_u64 v[154:155], v[154:155], 0, v[132:133]
	global_store_dwordx4 v[154:155], v[150:153], off nt sc1
	v_mul_f32_e32 v155, 0xbfb8aa3b, v68
	v_exp_f32_e32 v155, v155
	v_mul_f32_e32 v151, 0xbfb8aa3b, v66
	v_mul_f32_e32 v152, 0xbfb8aa3b, v71
	v_exp_f32_e32 v151, v151
	v_exp_f32_e32 v152, v152
	v_mul_f32_e32 v153, 0xbfb8aa3b, v67
	v_exp_f32_e32 v153, v153
	v_add_f32_e32 v151, 1.0, v151
	v_add_f32_e32 v152, 1.0, v152
	v_rcp_f32_e32 v151, v151
	v_rcp_f32_e32 v152, v152
	v_add_f32_e32 v150, 1.0, v156
	v_mul_f32_e32 v156, 0xbfb8aa3b, v73
	v_mul_f32_e32 v154, v78, v151
	v_mul_f32_e32 v151, v87, v152
	v_add_f32_e32 v152, 1.0, v153
	v_mul_f32_e32 v153, 0xbfb8aa3b, v72
	v_exp_f32_e32 v153, v153
	v_exp_f32_e32 v156, v156
	v_mul_f32_e32 v157, 0xbfb8aa3b, v69
	v_exp_f32_e32 v157, v157
	v_rcp_f32_e32 v150, v150
	v_rcp_f32_e32 v152, v152
	v_add_f32_e32 v153, 1.0, v153
	v_add_f32_e32 v155, 1.0, v155
	v_add_f32_e32 v156, 1.0, v156
	v_rcp_f32_e32 v153, v153
	v_rcp_f32_e32 v155, v155
	v_rcp_f32_e32 v156, v156
	v_add_f32_e32 v157, 1.0, v157
	v_rcp_f32_e32 v157, v157
	v_mul_f32_e32 v150, v86, v150
	v_mul_f32_e32 v152, v79, v152
	v_mul_f32_e32 v153, v88, v153
	v_mul_f32_e32 v155, v80, v155
	v_mul_f32_e32 v156, v89, v156
	v_cvt_pk_bf16_f32 v150, v150, v151
	v_cvt_pk_bf16_f32 v151, v153, v156
	v_cvt_pk_bf16_f32 v152, v154, v152
	v_mul_f32_e32 v154, 0xbfb8aa3b, v48
	v_mul_f32_e32 v157, v81, v157
	v_cvt_pk_bf16_f32 v153, v155, v157
	v_exp_f32_e32 v156, v154
	v_mad_i64_i32 v[154:155], s[14:15], v145, s1, v[130:131]
	v_lshl_add_u64 v[154:155], v[154:155], 0, v[132:133]
	global_store_dwordx4 v[154:155], v[150:153], off nt sc1
	v_mul_f32_e32 v155, 0xbfb8aa3b, v42
	v_exp_f32_e32 v155, v155
	v_mul_f32_e32 v151, 0xbfb8aa3b, v40
	v_mul_f32_e32 v152, 0xbfb8aa3b, v49
	v_exp_f32_e32 v151, v151
	v_exp_f32_e32 v152, v152
	v_mul_f32_e32 v153, 0xbfb8aa3b, v41
	v_exp_f32_e32 v153, v153
	v_add_f32_e32 v151, 1.0, v151
	v_add_f32_e32 v152, 1.0, v152
	v_rcp_f32_e32 v151, v151
	v_rcp_f32_e32 v152, v152
	v_add_f32_e32 v150, 1.0, v156
	v_mul_f32_e32 v156, 0xbfb8aa3b, v51
	v_mul_f32_e32 v154, v56, v151
	v_mul_f32_e32 v151, v61, v152
	v_add_f32_e32 v152, 1.0, v153
	v_mul_f32_e32 v153, 0xbfb8aa3b, v50
	v_exp_f32_e32 v153, v153
	v_exp_f32_e32 v156, v156
	v_mul_f32_e32 v157, 0xbfb8aa3b, v43
	v_exp_f32_e32 v157, v157
	v_rcp_f32_e32 v150, v150
	v_rcp_f32_e32 v152, v152
	v_add_f32_e32 v153, 1.0, v153
	v_add_f32_e32 v155, 1.0, v155
	v_add_f32_e32 v156, 1.0, v156
	v_rcp_f32_e32 v153, v153
	v_rcp_f32_e32 v155, v155
	v_rcp_f32_e32 v156, v156
	v_add_f32_e32 v157, 1.0, v157
	v_rcp_f32_e32 v157, v157
	v_mul_f32_e32 v150, v60, v150
	v_mul_f32_e32 v152, v57, v152
	v_mul_f32_e32 v153, v62, v153
	v_mul_f32_e32 v155, v58, v155
	v_mul_f32_e32 v156, v63, v156
	v_cvt_pk_bf16_f32 v150, v150, v151
	v_cvt_pk_bf16_f32 v151, v153, v156
	v_cvt_pk_bf16_f32 v152, v154, v152
	v_mul_f32_e32 v154, 0xbfb8aa3b, v32
	v_mul_f32_e32 v157, v59, v157
	v_cvt_pk_bf16_f32 v153, v155, v157
	v_exp_f32_e32 v156, v154
	v_mad_i64_i32 v[154:155], s[14:15], v144, s1, v[130:131]
	v_lshl_add_u64 v[154:155], v[154:155], 0, v[132:133]
	global_store_dwordx4 v[154:155], v[150:153], off nt sc1
	v_mul_f32_e32 v155, 0xbfb8aa3b, v26
	v_exp_f32_e32 v155, v155
	v_mul_f32_e32 v151, 0xbfb8aa3b, v24
	v_mul_f32_e32 v152, 0xbfb8aa3b, v33
	v_exp_f32_e32 v151, v151
	v_exp_f32_e32 v152, v152
	v_mul_f32_e32 v153, 0xbfb8aa3b, v25
	v_exp_f32_e32 v153, v153
	v_add_f32_e32 v151, 1.0, v151
	v_add_f32_e32 v152, 1.0, v152
	v_rcp_f32_e32 v151, v151
	v_rcp_f32_e32 v152, v152
	v_add_f32_e32 v150, 1.0, v156
	v_mul_f32_e32 v156, 0xbfb8aa3b, v35
	v_mul_f32_e32 v154, v44, v151
	v_mul_f32_e32 v151, v53, v152
	v_add_f32_e32 v152, 1.0, v153
	v_mul_f32_e32 v153, 0xbfb8aa3b, v34
	v_exp_f32_e32 v153, v153
	v_exp_f32_e32 v156, v156
	v_mul_f32_e32 v157, 0xbfb8aa3b, v27
	v_exp_f32_e32 v157, v157
	v_rcp_f32_e32 v150, v150
	v_rcp_f32_e32 v152, v152
	v_add_f32_e32 v153, 1.0, v153
	v_add_f32_e32 v155, 1.0, v155
	v_add_f32_e32 v156, 1.0, v156
	v_rcp_f32_e32 v153, v153
	v_rcp_f32_e32 v155, v155
	v_rcp_f32_e32 v156, v156
	v_add_f32_e32 v157, 1.0, v157
	v_rcp_f32_e32 v157, v157
	v_mul_f32_e32 v150, v52, v150
	v_mul_f32_e32 v152, v45, v152
	v_mul_f32_e32 v153, v54, v153
	v_mul_f32_e32 v155, v46, v155
	v_mul_f32_e32 v156, v55, v156
	v_cvt_pk_bf16_f32 v150, v150, v151
	v_cvt_pk_bf16_f32 v151, v153, v156
	v_cvt_pk_bf16_f32 v152, v154, v152
	v_mul_f32_e32 v154, 0xbfb8aa3b, v16
	v_mul_f32_e32 v157, v47, v157
	v_cvt_pk_bf16_f32 v153, v155, v157
	v_exp_f32_e32 v156, v154
	v_mad_i64_i32 v[154:155], s[14:15], v143, s1, v[130:131]
	v_lshl_add_u64 v[154:155], v[154:155], 0, v[132:133]
	global_store_dwordx4 v[154:155], v[150:153], off nt sc1
	v_mul_f32_e32 v155, 0xbfb8aa3b, v10
	v_exp_f32_e32 v155, v155
	v_mul_f32_e32 v151, 0xbfb8aa3b, v8
	v_mul_f32_e32 v152, 0xbfb8aa3b, v17
	v_exp_f32_e32 v151, v151
	v_exp_f32_e32 v152, v152
	v_mul_f32_e32 v153, 0xbfb8aa3b, v9
	v_exp_f32_e32 v153, v153
	v_add_f32_e32 v151, 1.0, v151
	v_add_f32_e32 v152, 1.0, v152
	v_rcp_f32_e32 v151, v151
	v_rcp_f32_e32 v152, v152
	v_add_f32_e32 v150, 1.0, v156
	v_mul_f32_e32 v156, 0xbfb8aa3b, v19
	v_mul_f32_e32 v154, v28, v151
	v_mul_f32_e32 v151, v37, v152
	v_add_f32_e32 v152, 1.0, v153
	v_mul_f32_e32 v153, 0xbfb8aa3b, v18
	v_exp_f32_e32 v153, v153
	v_exp_f32_e32 v156, v156
	v_mul_f32_e32 v157, 0xbfb8aa3b, v11
	v_exp_f32_e32 v157, v157
	v_rcp_f32_e32 v150, v150
	v_rcp_f32_e32 v152, v152
	v_add_f32_e32 v153, 1.0, v153
	v_add_f32_e32 v155, 1.0, v155
	v_add_f32_e32 v156, 1.0, v156
	v_rcp_f32_e32 v153, v153
	v_rcp_f32_e32 v155, v155
	v_rcp_f32_e32 v156, v156
	v_add_f32_e32 v157, 1.0, v157
	v_rcp_f32_e32 v157, v157
	v_mul_f32_e32 v150, v36, v150
	v_mul_f32_e32 v152, v29, v152
	v_mul_f32_e32 v153, v38, v153
	v_mul_f32_e32 v155, v30, v155
	v_mul_f32_e32 v156, v39, v156
	v_cvt_pk_bf16_f32 v150, v150, v151
	v_cvt_pk_bf16_f32 v151, v153, v156
	v_cvt_pk_bf16_f32 v152, v154, v152
	v_mul_f32_e32 v154, 0xbfb8aa3b, v4
	v_mul_f32_e32 v157, v31, v157
	v_cvt_pk_bf16_f32 v153, v155, v157
	v_exp_f32_e32 v156, v154
	v_mad_i64_i32 v[154:155], s[14:15], v142, s1, v[130:131]
	v_lshl_add_u64 v[154:155], v[154:155], 0, v[132:133]
	global_store_dwordx4 v[154:155], v[150:153], off nt sc1
	v_mul_f32_e32 v155, 0xbfb8aa3b, v2
	v_mul_f32_e32 v157, 0xbfb8aa3b, v3
	v_mul_f32_e32 v151, 0xbfb8aa3b, v0
	v_mul_f32_e32 v152, 0xbfb8aa3b, v5
	v_exp_f32_e32 v151, v151
	v_exp_f32_e32 v152, v152
	v_mul_f32_e32 v153, 0xbfb8aa3b, v1
	v_exp_f32_e32 v153, v153
	v_add_f32_e32 v151, 1.0, v151
	v_add_f32_e32 v152, 1.0, v152
	v_rcp_f32_e32 v151, v151
	v_rcp_f32_e32 v152, v152
	v_add_f32_e32 v150, 1.0, v156
	v_mul_f32_e32 v156, 0xbfb8aa3b, v7
	v_mul_f32_e32 v154, v12, v151
	v_mul_f32_e32 v151, v21, v152
	v_add_f32_e32 v152, 1.0, v153
	v_mul_f32_e32 v153, 0xbfb8aa3b, v6
	v_exp_f32_e32 v153, v153
	v_exp_f32_e32 v155, v155
	v_exp_f32_e32 v156, v156
	v_exp_f32_e32 v157, v157
	v_add_f32_e32 v153, 1.0, v153
	v_rcp_f32_e32 v150, v150
	v_rcp_f32_e32 v152, v152
	v_rcp_f32_e32 v153, v153
	v_add_f32_e32 v155, 1.0, v155
	v_add_f32_e32 v156, 1.0, v156
	v_add_f32_e32 v157, 1.0, v157
	v_rcp_f32_e32 v155, v155
	v_rcp_f32_e32 v156, v156
	v_rcp_f32_e32 v157, v157
	v_mad_i64_i32 v[130:131], s[14:15], v64, s1, v[130:131]
	v_mul_f32_e32 v150, v20, v150
	v_mul_f32_e32 v152, v13, v152
	v_mul_f32_e32 v153, v22, v153
	v_lshl_add_u64 v[130:131], v[130:131], 0, v[132:133]
	v_mul_f32_e32 v155, v14, v155
	v_mul_f32_e32 v156, v23, v156
	v_mul_f32_e32 v157, v15, v157
	v_cvt_pk_bf16_f32 v150, v150, v151
	v_cvt_pk_bf16_f32 v151, v153, v156
	v_cvt_pk_bf16_f32 v152, v154, v152
	v_cvt_pk_bf16_f32 v153, v155, v157
	global_store_dwordx4 v[130:131], v[150:153], off nt sc1
	s_cbranch_execnz .LBB0_360
.LBB0_362:
	s_lshl_b32 s14, s31, 8
	s_or_b32 s14, s14, s26
	v_add_u32_e32 v130, s14, v149
	v_ashrrev_i32_e32 v131, 31, v130
	v_mov_b64_e32 v[132:133], s[64:65]
	v_mad_i64_i32 v[148:149], s[14:15], v148, s1, v[132:133]
	v_lshlrev_b64 v[130:131], 1, v[130:131]
	v_lshl_add_u64 v[148:149], v[148:149], 0, v[130:131]
	v_cvt_pk_bf16_f32 v126, v126, v127
	v_cvt_pk_bf16_f32 v127, v128, v129
	v_cvt_pk_bf16_f32 v128, v122, v123
	v_cvt_pk_bf16_f32 v129, v124, v125
	global_store_dwordx4 v[148:149], v[126:129], off nt sc1
	v_cvt_pk_bf16_f32 v114, v114, v115
	v_cvt_pk_bf16_f32 v115, v116, v117
	v_cvt_pk_bf16_f32 v116, v106, v107
	v_mad_i64_i32 v[106:107], s[14:15], v147, s1, v[132:133]
	v_cvt_pk_bf16_f32 v117, v108, v109
	global_store_dwordx4 v[148:149], v[114:117], off offset:256 nt sc1
	s_nop 1
	v_lshl_add_u64 v[114:115], v[106:107], 0, v[130:131]
	v_cvt_pk_bf16_f32 v106, v118, v119
	v_cvt_pk_bf16_f32 v107, v120, v121
	v_cvt_pk_bf16_f32 v108, v110, v111
	v_cvt_pk_bf16_f32 v109, v112, v113
	global_store_dwordx4 v[114:115], v[106:109], off nt sc1
	v_cvt_pk_bf16_f32 v98, v98, v99
	v_cvt_pk_bf16_f32 v99, v100, v101
	v_cvt_pk_bf16_f32 v100, v90, v91
	v_mad_i64_i32 v[90:91], s[14:15], v146, s1, v[132:133]
	v_cvt_pk_bf16_f32 v101, v92, v93
	global_store_dwordx4 v[114:115], v[98:101], off offset:256 nt sc1
	s_nop 1
	v_lshl_add_u64 v[98:99], v[90:91], 0, v[130:131]
	v_cvt_pk_bf16_f32 v90, v102, v103
	v_cvt_pk_bf16_f32 v91, v104, v105
	v_cvt_pk_bf16_f32 v92, v94, v95
	v_cvt_pk_bf16_f32 v93, v96, v97
	global_store_dwordx4 v[98:99], v[90:93], off nt sc1
	v_cvt_pk_bf16_f32 v82, v82, v83
	v_cvt_pk_bf16_f32 v83, v84, v85
	v_cvt_pk_bf16_f32 v84, v74, v75
	v_mad_i64_i32 v[74:75], s[14:15], v145, s1, v[132:133]
	v_cvt_pk_bf16_f32 v85, v76, v77
	global_store_dwordx4 v[98:99], v[82:85], off offset:256 nt sc1
	s_nop 1
	v_lshl_add_u64 v[82:83], v[74:75], 0, v[130:131]
	v_cvt_pk_bf16_f32 v74, v86, v87
	v_cvt_pk_bf16_f32 v75, v88, v89
	v_cvt_pk_bf16_f32 v76, v78, v79
	v_cvt_pk_bf16_f32 v77, v80, v81
	global_store_dwordx4 v[82:83], v[74:77], off nt sc1
	v_cvt_pk_bf16_f32 v70, v70, v71
	v_cvt_pk_bf16_f32 v71, v72, v73
	v_cvt_pk_bf16_f32 v72, v66, v67
	v_mad_i64_i32 v[66:67], s[14:15], v144, s1, v[132:133]
	v_lshl_add_u64 v[66:67], v[66:67], 0, v[130:131]
	v_cvt_pk_bf16_f32 v73, v68, v69
	global_store_dwordx4 v[82:83], v[70:73], off offset:256 nt sc1
	v_cvt_pk_bf16_f32 v60, v60, v61
	v_cvt_pk_bf16_f32 v61, v62, v63
	v_cvt_pk_bf16_f32 v62, v56, v57
	v_cvt_pk_bf16_f32 v63, v58, v59
	global_store_dwordx4 v[66:67], v[60:63], off nt sc1
	v_cvt_pk_bf16_f32 v48, v48, v49
	v_cvt_pk_bf16_f32 v49, v50, v51
	v_cvt_pk_bf16_f32 v50, v40, v41
	v_mad_i64_i32 v[40:41], s[14:15], v143, s1, v[132:133]
	v_cvt_pk_bf16_f32 v51, v42, v43
	global_store_dwordx4 v[66:67], v[48:51], off offset:256 nt sc1
	s_nop 1
	v_lshl_add_u64 v[48:49], v[40:41], 0, v[130:131]
	v_cvt_pk_bf16_f32 v40, v52, v53
	v_cvt_pk_bf16_f32 v41, v54, v55
	v_cvt_pk_bf16_f32 v42, v44, v45
	v_cvt_pk_bf16_f32 v43, v46, v47
	global_store_dwordx4 v[48:49], v[40:43], off nt sc1
	v_cvt_pk_bf16_f32 v32, v32, v33
	v_cvt_pk_bf16_f32 v33, v34, v35
	v_cvt_pk_bf16_f32 v34, v24, v25
	v_mad_i64_i32 v[24:25], s[14:15], v142, s1, v[132:133]
	v_cvt_pk_bf16_f32 v35, v26, v27
	global_store_dwordx4 v[48:49], v[32:35], off offset:256 nt sc1
	s_nop 1
	v_lshl_add_u64 v[32:33], v[24:25], 0, v[130:131]
	v_cvt_pk_bf16_f32 v24, v36, v37
	v_cvt_pk_bf16_f32 v25, v38, v39
	v_cvt_pk_bf16_f32 v26, v28, v29
	v_cvt_pk_bf16_f32 v27, v30, v31
	global_store_dwordx4 v[32:33], v[24:27], off nt sc1
	v_cvt_pk_bf16_f32 v16, v16, v17
	v_cvt_pk_bf16_f32 v17, v18, v19
	v_cvt_pk_bf16_f32 v18, v8, v9
	v_mad_i64_i32 v[8:9], s[14:15], v64, s1, v[132:133]
	v_cvt_pk_bf16_f32 v19, v10, v11
	global_store_dwordx4 v[32:33], v[16:19], off offset:256 nt sc1
	s_nop 1
	v_lshl_add_u64 v[16:17], v[8:9], 0, v[130:131]
	v_cvt_pk_bf16_f32 v8, v20, v21
	v_cvt_pk_bf16_f32 v9, v22, v23
	v_cvt_pk_bf16_f32 v10, v12, v13
	v_cvt_pk_bf16_f32 v11, v14, v15
	global_store_dwordx4 v[16:17], v[8:11], off nt sc1
	v_cvt_pk_bf16_f32 v4, v4, v5
	v_cvt_pk_bf16_f32 v5, v6, v7
	v_cvt_pk_bf16_f32 v6, v0, v1
	v_cvt_pk_bf16_f32 v7, v2, v3
	global_store_dwordx4 v[16:17], v[4:7], off offset:256 nt sc1
	s_cmp_eq_u32 s31, 10
	s_mov_b64 s[14:15], -1
	s_cbranch_scc1 .LBB0_353

.LBB0_414:
	v_add3_u32 v64, s23, v173, v171
	ds_read_b64_tr_b16 v[90:91], v64 offset:36864
	s_nop 1
	ds_read_b64_tr_b16 v[86:87], v64 offset:36896
	ds_read_b64_tr_b16 v[100:101], v64 offset:36928
	ds_read_b64_tr_b16 v[108:109], v64 offset:36960
	ds_read_b64_tr_b16 v[92:93], v64 offset:39168
	ds_read_b64_tr_b16 v[88:89], v64 offset:39200
	ds_read_b64_tr_b16 v[102:103], v64 offset:39232
	ds_read_b64_tr_b16 v[110:111], v64 offset:39264
	ds_read_b64_tr_b16 v[104:105], v64 offset:41472
	ds_read_b64_tr_b16 v[112:113], v64 offset:41504
	ds_read_b64_tr_b16 v[118:119], v64 offset:41536
	ds_read_b64_tr_b16 v[126:127], v64 offset:41568
	ds_read_b64_tr_b16 v[106:107], v64 offset:43776
	ds_read_b64_tr_b16 v[114:115], v64 offset:43808
	ds_read_b64_tr_b16 v[120:121], v64 offset:43840
	ds_read_b64_tr_b16 v[128:129], v64 offset:43872
	ds_read_b64_tr_b16 v[122:123], v64 offset:46080
	ds_read_b64_tr_b16 v[130:131], v64 offset:46112
	ds_read_b64_tr_b16 v[138:139], v64 offset:46144
	ds_read_b64_tr_b16 v[146:147], v64 offset:46176
	ds_read_b64_tr_b16 v[124:125], v64 offset:48384
	ds_read_b64_tr_b16 v[132:133], v64 offset:48416
	ds_read_b64_tr_b16 v[140:141], v64 offset:48448
	ds_read_b64_tr_b16 v[148:149], v64 offset:48480
	ds_read_b64_tr_b16 v[142:143], v64 offset:50688
	ds_read_b64_tr_b16 v[152:153], v64 offset:50720
	ds_read_b64_tr_b16 v[156:157], v64 offset:50752
	ds_read_b64_tr_b16 v[134:135], v64 offset:50784
	ds_read_b64_tr_b16 v[144:145], v64 offset:52992
	ds_read_b64_tr_b16 v[154:155], v64 offset:53024
	ds_read_b64_tr_b16 v[158:159], v64 offset:53056
	ds_read_b64_tr_b16 v[136:137], v64 offset:53088
	ds_read_b64_tr_b16 v[150:151], v64 offset:55296
	ds_read_b64_tr_b16 v[116:117], v64 offset:55328
	ds_read_b64_tr_b16 v[98:99], v64 offset:55360
	ds_read_b64_tr_b16 v[94:95], v64 offset:55392
	v_max3_f32 v64, v82, s84, v83
	v_max3_f32 v64, v64, v84, v85
	v_max3_f32 v64, v64, v78, v79
	v_max3_f32 v64, v64, v80, v81
	v_max3_f32 v64, v64, v74, v75
	v_max3_f32 v64, v64, v76, v77
	v_max3_f32 v64, v64, v70, v71
	v_max3_f32 v64, v64, v72, v73
	v_max3_f32 v64, v64, v66, v67
	v_max3_f32 v64, v64, v68, v69
	v_max3_f32 v64, v64, v60, v61
	v_max3_f32 v64, v64, v62, v63
	v_max3_f32 v64, v64, v56, v57
	v_max3_f32 v64, v64, v58, v59
	v_max3_f32 v64, v64, v52, v53
	v_max3_f32 v64, v64, v54, v55
	v_max3_f32 v64, v64, v48, v49
	v_max3_f32 v64, v64, v50, v51
	v_mov_b32_e32 v96, v64
	s_nop 1
	v_permlane16_swap_b32_e32 v64, v96
	v_max_f32_e32 v96, v96, v96
	v_max_f32_e32 v64, v64, v64
	v_max_f32_e32 v64, v64, v96
	v_mov_b32_e32 v96, v64
	s_nop 1
	v_permlane32_swap_b32_e32 v64, v96
	v_max_f32_e32 v96, v96, v96
	v_max_f32_e32 v64, v64, v64
	v_max_f32_e32 v170, v64, v96
	v_pk_add_f32 v[82:83], v[82:83], v[170:171] op_sel_hi:[1,0] neg_lo:[0,1] neg_hi:[0,1]
	v_pk_add_f32 v[84:85], v[84:85], v[170:171] op_sel_hi:[1,0] neg_lo:[0,1] neg_hi:[0,1]
	v_exp_f32_e32 v82, v82
	v_exp_f32_e32 v83, v83
	v_exp_f32_e32 v84, v84
	v_exp_f32_e32 v85, v85
	v_pk_add_f32 v[78:79], v[78:79], v[170:171] op_sel_hi:[1,0] neg_lo:[0,1] neg_hi:[0,1]
	v_pk_add_f32 v[80:81], v[80:81], v[170:171] op_sel_hi:[1,0] neg_lo:[0,1] neg_hi:[0,1]
	v_exp_f32_e32 v78, v78
	v_exp_f32_e32 v79, v79
	v_exp_f32_e32 v80, v80
	v_exp_f32_e32 v81, v81
	v_pk_add_f32 v[74:75], v[74:75], v[170:171] op_sel_hi:[1,0] neg_lo:[0,1] neg_hi:[0,1]
	v_pk_add_f32 v[96:97], v[82:83], 0 op_sel_hi:[1,0]
	v_pk_add_f32 v[76:77], v[76:77], v[170:171] op_sel_hi:[1,0] neg_lo:[0,1] neg_hi:[0,1]
	v_exp_f32_e32 v192, v74
	v_exp_f32_e32 v193, v75
	v_pk_add_f32 v[96:97], v[84:85], v[96:97]
	v_exp_f32_e32 v194, v76
	v_exp_f32_e32 v195, v77
	v_pk_add_f32 v[70:71], v[70:71], v[170:171] op_sel_hi:[1,0] neg_lo:[0,1] neg_hi:[0,1]
	v_pk_add_f32 v[74:75], v[78:79], v[96:97]
	v_pk_add_f32 v[72:73], v[72:73], v[170:171] op_sel_hi:[1,0] neg_lo:[0,1] neg_hi:[0,1]
	v_exp_f32_e32 v96, v70
	v_exp_f32_e32 v97, v71
	v_pk_add_f32 v[74:75], v[80:81], v[74:75]
	v_exp_f32_e32 v196, v72
	v_exp_f32_e32 v197, v73
	v_pk_add_f32 v[66:67], v[66:67], v[170:171] op_sel_hi:[1,0] neg_lo:[0,1] neg_hi:[0,1]
	v_pk_add_f32 v[74:75], v[192:193], v[74:75]
	v_pk_add_f32 v[68:69], v[68:69], v[170:171] op_sel_hi:[1,0] neg_lo:[0,1] neg_hi:[0,1]
	v_exp_f32_e32 v198, v66
	v_exp_f32_e32 v199, v67
	v_pk_add_f32 v[74:75], v[194:195], v[74:75]
	v_exp_f32_e32 v200, v68
	v_exp_f32_e32 v201, v69
	v_pk_add_f32 v[66:67], v[96:97], v[74:75]
	v_cvt_pk_bf16_f32 v68, v78, v79
	v_pk_add_f32 v[66:67], v[196:197], v[66:67]
	v_cvt_pk_bf16_f32 v69, v80, v81
	v_pk_add_f32 v[66:67], v[198:199], v[66:67]
	v_pk_add_f32 v[74:75], v[60:61], v[170:171] op_sel_hi:[1,0] neg_lo:[0,1] neg_hi:[0,1]
	v_pk_add_f32 v[202:203], v[200:201], v[66:67]
	v_cvt_pk_bf16_f32 v66, v82, v83
	v_cvt_pk_bf16_f32 v67, v84, v85
	v_pk_add_f32 v[76:77], v[62:63], v[170:171] op_sel_hi:[1,0] neg_lo:[0,1] neg_hi:[0,1]
	v_exp_f32_e32 v78, v74
	s_waitcnt lgkmcnt(14)
	v_mfma_f32_16x16x32_bf16 v[70:73], v[90:93], v[66:69], 0
	v_exp_f32_e32 v79, v75
	v_exp_f32_e32 v80, v76
	v_exp_f32_e32 v81, v77
	v_mfma_f32_16x16x32_bf16 v[60:63], v[86:89], v[66:69], 0
	v_add_f32_e64 v84, v56, -v170
	v_add_f32_e64 v85, v57, -v170
	v_pk_add_f32 v[86:87], v[58:59], v[170:171] op_sel_hi:[1,0] neg_lo:[0,1] neg_hi:[0,1]
	v_exp_f32_e32 v84, v84
	v_mfma_f32_16x16x32_bf16 v[74:77], v[100:103], v[66:69], 0
	v_exp_f32_e32 v85, v85
	v_exp_f32_e32 v86, v86
	v_exp_f32_e32 v87, v87
	v_mfma_f32_16x16x32_bf16 v[56:59], v[108:111], v[66:69], 0
	v_cvt_pk_bf16_f32 v66, v192, v193
	v_cvt_pk_bf16_f32 v67, v194, v195
	v_cvt_pk_bf16_f32 v68, v96, v97
	v_cvt_pk_bf16_f32 v69, v196, v197
	v_pk_add_f32 v[88:89], v[52:53], v[170:171] op_sel_hi:[1,0] neg_lo:[0,1] neg_hi:[0,1]
	v_pk_add_f32 v[82:83], v[78:79], v[202:203]
	v_mfma_f32_16x16x32_bf16 v[70:73], v[104:107], v[66:69], v[70:73]
	v_add_f32_e64 v90, v54, -v170
	v_add_f32_e64 v91, v55, -v170
	v_pk_add_f32 v[82:83], v[80:81], v[82:83]
	v_pk_add_f32 v[48:49], v[48:49], v[170:171] op_sel_hi:[1,0] neg_lo:[0,1] neg_hi:[0,1]
	v_mfma_f32_16x16x32_bf16 v[60:63], v[112:115], v[66:69], v[60:63]
	v_add_f32_e64 v82, v84, v82
	v_add_f32_e64 v83, v85, v83
	s_waitcnt lgkmcnt(1)
	v_mov_b32_e32 v100, v98
	v_pk_add_f32 v[82:83], v[86:87], v[82:83]
	v_mfma_f32_16x16x32_bf16 v[74:77], v[118:121], v[66:69], v[74:77]
	v_mov_b32_e32 v118, v116
	v_mov_b32_e32 v119, v117
	v_mov_b32_e32 v101, v99
	v_mfma_f32_16x16x32_bf16 v[52:55], v[126:129], v[66:69], v[56:59]
	s_waitcnt lgkmcnt(0)
	v_mov_b32_e32 v96, v94
	v_mov_b32_e32 v97, v95
	v_mov_b32_e32 v64, v65
	v_cvt_pk_bf16_f32 v58, v78, v79
	v_exp_f32_e32 v78, v88
	v_exp_f32_e32 v79, v89
	v_cvt_pk_bf16_f32 v56, v198, v199
	v_cvt_pk_bf16_f32 v57, v200, v201
	v_cvt_pk_bf16_f32 v59, v80, v81
	v_exp_f32_e32 v80, v90
	v_exp_f32_e32 v81, v91
	v_mfma_f32_16x16x32_bf16 v[66:69], v[122:125], v[56:59], v[70:73]
	v_add_f32_e64 v82, v78, v82
	v_add_f32_e64 v83, v79, v83
	s_cmp_eq_u32 s30, 1
	s_mov_b32 s23, 0xe800000
	v_mfma_f32_16x16x32_bf16 v[60:63], v[130:133], v[56:59], v[60:63]
	s_cselect_b32 s23, s23, 0x2e800000
	s_cmp_lg_u32 s30, 0
	s_cselect_b32 s23, s23, 0x12800000
	v_mfma_f32_16x16x32_bf16 v[70:73], v[138:141], v[56:59], v[74:77]
	s_add_u32 s36, s42, s23
	s_addc_u32 s37, s43, 0
	s_lshl_b32 s66, s22, 6
	v_pk_add_f32 v[74:75], v[50:51], v[170:171] op_sel_hi:[1,0] neg_lo:[0,1] neg_hi:[0,1]
	v_exp_f32_e32 v76, v48
	v_exp_f32_e32 v77, v49
	v_exp_f32_e32 v74, v74
	v_exp_f32_e32 v75, v75
	v_mfma_f32_16x16x32_bf16 v[48:51], v[146:149], v[56:59], v[52:55]
	s_nop 2
	v_cvt_pk_bf16_f32 v52, v84, v85
	v_cvt_pk_bf16_f32 v53, v86, v87
	v_cvt_pk_bf16_f32 v54, v78, v79
	v_cvt_pk_bf16_f32 v55, v80, v81
	v_pk_add_f32 v[78:79], v[80:81], v[82:83]
	s_nop 0
	v_mfma_f32_16x16x32_bf16 v[56:59], v[142:145], v[52:55], v[66:69]
	v_mfma_f32_16x16x32_bf16 v[66:69], v[152:155], v[52:55], v[60:63]
	v_mov_b32_e32 v152, v150
	v_mov_b32_e32 v153, v151
	s_nop 0
	v_pk_add_f32 v[60:61], v[76:77], v[78:79]
	v_mfma_f32_16x16x32_bf16 v[70:73], v[156:159], v[52:55], v[70:73]
	v_add_f32_e64 v60, v74, v60
	v_add_f32_e64 v61, v75, v61
	v_cvt_pk_bf16_f32 v62, v76, v77
	v_pk_add_f32 v[60:61], v[60:61], v[60:61] op_sel:[0,1] op_sel_hi:[1,0]
	v_mfma_f32_16x16x32_bf16 v[48:51], v[134:137], v[52:55], v[48:51]
	v_mov_b32_e32 v61, v60
	s_nop 1
	v_permlane16_swap_b32_e32 v60, v61
	v_cvt_pk_bf16_f32 v63, v74, v75
	v_add_f32_e32 v74, v60, v61
	s_nop 0
	v_mfma_f32_16x16x32_bf16 v[52:55], v[150:153], v[62:65], v[56:59]
	v_mfma_f32_16x16x32_bf16 v[56:59], v[116:119], v[62:65], v[66:69]
	v_mfma_f32_16x16x32_bf16 v[66:69], v[98:101], v[62:65], v[70:73]
	s_nop 2
	v_mov_b32_e32 v70, v74
	s_nop 1
	v_permlane32_swap_b32_e32 v74, v70
	v_mfma_f32_16x16x32_bf16 v[60:63], v[94:97], v[62:65], v[48:51]
	s_nop 2
	v_add_f32_e32 v48, v74, v70
	v_rcp_f32_e32 v49, v48
	s_nop 0
	v_mul_f32_e32 v49, 0x42800000, v49
	v_mul_f32_e32 v50, v49, v52
	v_mul_f32_e32 v51, v49, v53
	v_med3_f32 v53, v50, s55, v228
	v_med3_f32 v51, v51, s55, v228
	v_mov_b32_e32 v50, v65
	v_cvt_pk_fp8_f32 v50, v53, v51
	v_mul_f32_e32 v52, v49, v54
	v_mul_f32_e32 v51, v49, v55
	v_med3_f32 v52, v52, s55, v228
	v_med3_f32 v51, v51, s55, v228
	v_cvt_pk_fp8_f32 v50, v52, v51 op_sel:[0,0,1]
	v_mul_f32_e32 v51, v49, v56
	v_mul_f32_e32 v52, v49, v57
	v_med3_f32 v54, v51, s55, v228
	v_med3_f32 v52, v52, s55, v228
	v_mov_b32_e32 v51, v65
	v_cvt_pk_fp8_f32 v51, v54, v52
	v_mul_f32_e32 v53, v49, v58
	v_mul_f32_e32 v52, v49, v59
	v_med3_f32 v53, v53, s55, v228
	v_med3_f32 v52, v52, s55, v228
	v_cvt_pk_fp8_f32 v51, v53, v52 op_sel:[0,0,1]
	v_mul_f32_e32 v52, v49, v66
	v_mul_f32_e32 v53, v49, v67
	v_med3_f32 v55, v52, s55, v228
	v_med3_f32 v53, v53, s55, v228
	v_mov_b32_e32 v52, v65
	v_cvt_pk_fp8_f32 v52, v55, v53
	v_mul_f32_e32 v54, v49, v68
	v_mul_f32_e32 v53, v49, v69
	v_med3_f32 v54, v54, s55, v228
	v_med3_f32 v53, v53, s55, v228
	v_cvt_pk_fp8_f32 v52, v54, v53 op_sel:[0,0,1]
	v_mul_f32_e32 v53, v49, v60
	v_mul_f32_e32 v54, v49, v61
	v_med3_f32 v56, v53, s55, v228
	v_med3_f32 v54, v54, s55, v228
	v_mov_b32_e32 v53, v65
	v_cvt_pk_fp8_f32 v53, v56, v54
	v_mul_f32_e32 v55, v49, v62
	v_mul_f32_e32 v49, v49, v63
	v_med3_f32 v54, v55, s55, v228
	v_med3_f32 v49, v49, s55, v228
	v_cvt_pk_fp8_f32 v53, v54, v49 op_sel:[0,0,1]
	v_lshlrev_b64 v[54:55], 10, v[166:167]
	v_lshl_add_u64 v[54:55], s[36:37], 0, v[54:55]
	v_lshl_add_u64 v[54:55], v[54:55], 0, s[66:67]
	v_lshl_add_u64 v[54:55], v[54:55], 0, v[160:161]
	global_store_dwordx4 v[54:55], v[50:53], off sc1
	s_and_saveexec_b64 s[36:37], vcc
	s_cbranch_execz .LBB0_416
	v_log_f32_e32 v48, v48
	s_ashr_i32 s31, s30, 31
	s_lshl_b64 s[30:31], s[30:31], 22
	v_readlane_b32 s23, v254, 30
	s_add_u32 s30, s23, s30
	v_readlane_b32 s23, v254, 31
	v_add_f32_e32 v48, v170, v48
	s_addc_u32 s31, s23, s31
	v_mul_f32_e32 v50, 0x3f317218, v48
	v_lshlrev_b64 v[48:49], 6, v[166:167]
	v_lshl_add_u64 v[48:49], s[30:31], 0, v[48:49]
	s_mov_b32 s23, s67
	v_lshl_add_u64 v[48:49], s[22:23], 2, v[48:49]
	global_store_dword v[48:49], v50, off

.LBB0_420:
	v_readlane_b32 s6, v255, 3
	s_mov_b32 s63, s71
	s_nop 0
	v_add3_u32 v10, s6, v173, v171
	v_add3_u32 v12, s6, v171, v173
	ds_read_b64_tr_b16 v[44:45], v10
	ds_read_b64_tr_b16 v[8:9], v10 offset:32
	ds_read_b64_tr_b16 v[50:51], v10 offset:64
	ds_read_b64_tr_b16 v[58:59], v10 offset:96
	ds_read_b64_tr_b16 v[46:47], v12 offset:2304
	ds_read_b64_tr_b16 v[10:11], v12 offset:2336
	ds_read_b64_tr_b16 v[52:53], v12 offset:2368
	ds_read_b64_tr_b16 v[60:61], v12 offset:2400
	ds_read_b64_tr_b16 v[54:55], v12 offset:4608
	ds_read_b64_tr_b16 v[66:67], v12 offset:4640
	ds_read_b64_tr_b16 v[70:71], v12 offset:4672
	ds_read_b64_tr_b16 v[78:79], v12 offset:4704
	ds_read_b64_tr_b16 v[56:57], v12 offset:6912
	ds_read_b64_tr_b16 v[68:69], v12 offset:6944
	ds_read_b64_tr_b16 v[72:73], v12 offset:6976
	ds_read_b64_tr_b16 v[80:81], v12 offset:7008
	ds_read_b64_tr_b16 v[74:75], v12 offset:9216
	ds_read_b64_tr_b16 v[82:83], v12 offset:9248
	ds_read_b64_tr_b16 v[90:91], v12 offset:9280
	ds_read_b64_tr_b16 v[98:99], v12 offset:9312
	ds_read_b64_tr_b16 v[76:77], v12 offset:11520
	ds_read_b64_tr_b16 v[84:85], v12 offset:11552
	ds_read_b64_tr_b16 v[92:93], v12 offset:11584
	ds_read_b64_tr_b16 v[100:101], v12 offset:11616
	ds_read_b64_tr_b16 v[94:95], v12 offset:13824
	ds_read_b64_tr_b16 v[104:105], v12 offset:13856
	ds_read_b64_tr_b16 v[108:109], v12 offset:13888
	ds_read_b64_tr_b16 v[86:87], v12 offset:13920
	ds_read_b64_tr_b16 v[96:97], v12 offset:16128
	ds_read_b64_tr_b16 v[106:107], v12 offset:16160
	ds_read_b64_tr_b16 v[110:111], v12 offset:16192
	ds_read_b64_tr_b16 v[88:89], v12 offset:16224
	ds_read_b64_tr_b16 v[102:103], v12 offset:18432
	ds_read_b64_tr_b16 v[14:15], v12 offset:18464
	ds_read_b64_tr_b16 v[48:49], v12 offset:18496
	ds_read_b64_tr_b16 v[12:13], v12 offset:18528
	v_max3_f32 v62, v40, s84, v41
	v_max3_f32 v62, v62, v42, v43
	v_max3_f32 v62, v62, v36, v37
	v_max3_f32 v62, v62, v38, v39
	v_max3_f32 v62, v62, v32, v33
	v_max3_f32 v62, v62, v34, v35
	v_max3_f32 v62, v62, v28, v29
	v_max3_f32 v62, v62, v30, v31
	v_max3_f32 v62, v62, v24, v25
	v_max3_f32 v62, v62, v26, v27
	v_max3_f32 v62, v62, v20, v21
	v_max3_f32 v62, v62, v22, v23
	v_max3_f32 v62, v62, v16, v17
	v_max3_f32 v62, v62, v18, v19
	v_max3_f32 v62, v62, v4, v5
	v_max3_f32 v62, v62, v6, v7
	v_max3_f32 v62, v62, v0, v1
	v_max3_f32 v62, v62, v2, v3
	v_mov_b32_e32 v63, v62
	s_nop 1
	v_permlane16_swap_b32_e32 v62, v63
	v_max_f32_e32 v63, v63, v63
	v_max_f32_e32 v62, v62, v62
	v_max_f32_e32 v62, v62, v63
	v_mov_b32_e32 v63, v62
	s_nop 1
	v_permlane32_swap_b32_e32 v62, v63
	v_max_f32_e32 v63, v63, v63
	v_max_f32_e32 v62, v62, v62
	v_max_f32_e32 v112, v62, v63
	v_pk_add_f32 v[40:41], v[40:41], v[112:113] op_sel_hi:[1,0] neg_lo:[0,1] neg_hi:[0,1]
	v_pk_add_f32 v[42:43], v[42:43], v[112:113] op_sel_hi:[1,0] neg_lo:[0,1] neg_hi:[0,1]
	v_exp_f32_e32 v40, v40
	v_exp_f32_e32 v41, v41
	v_exp_f32_e32 v42, v42
	v_exp_f32_e32 v43, v43
	v_pk_add_f32 v[36:37], v[36:37], v[112:113] op_sel_hi:[1,0] neg_lo:[0,1] neg_hi:[0,1]
	v_pk_add_f32 v[38:39], v[38:39], v[112:113] op_sel_hi:[1,0] neg_lo:[0,1] neg_hi:[0,1]
	v_exp_f32_e32 v36, v36
	v_exp_f32_e32 v37, v37
	v_exp_f32_e32 v38, v38
	v_exp_f32_e32 v39, v39
	v_pk_add_f32 v[32:33], v[32:33], v[112:113] op_sel_hi:[1,0] neg_lo:[0,1] neg_hi:[0,1]
	v_pk_add_f32 v[62:63], v[40:41], 0 op_sel_hi:[1,0]
	v_pk_add_f32 v[34:35], v[34:35], v[112:113] op_sel_hi:[1,0] neg_lo:[0,1] neg_hi:[0,1]
	v_exp_f32_e32 v32, v32
	v_exp_f32_e32 v33, v33
	v_pk_add_f32 v[62:63], v[42:43], v[62:63]
	v_exp_f32_e32 v34, v34
	v_exp_f32_e32 v35, v35
	v_pk_add_f32 v[28:29], v[28:29], v[112:113] op_sel_hi:[1,0] neg_lo:[0,1] neg_hi:[0,1]
	v_pk_add_f32 v[62:63], v[36:37], v[62:63]
	v_pk_add_f32 v[30:31], v[30:31], v[112:113] op_sel_hi:[1,0] neg_lo:[0,1] neg_hi:[0,1]
	v_exp_f32_e32 v114, v28
	v_exp_f32_e32 v115, v29
	v_pk_add_f32 v[62:63], v[38:39], v[62:63]
	v_exp_f32_e32 v116, v30
	v_exp_f32_e32 v117, v31
	v_pk_add_f32 v[24:25], v[24:25], v[112:113] op_sel_hi:[1,0] neg_lo:[0,1] neg_hi:[0,1]
	v_pk_add_f32 v[62:63], v[32:33], v[62:63]
	v_pk_add_f32 v[26:27], v[26:27], v[112:113] op_sel_hi:[1,0] neg_lo:[0,1] neg_hi:[0,1]
	v_exp_f32_e32 v118, v24
	v_exp_f32_e32 v119, v25
	v_pk_add_f32 v[62:63], v[34:35], v[62:63]
	v_exp_f32_e32 v120, v26
	v_exp_f32_e32 v121, v27
	v_pk_add_f32 v[24:25], v[114:115], v[62:63]
	v_cvt_pk_bf16_f32 v26, v36, v37
	v_pk_add_f32 v[24:25], v[116:117], v[24:25]
	v_cvt_pk_bf16_f32 v27, v38, v39
	v_pk_add_f32 v[24:25], v[118:119], v[24:25]
	v_pk_add_f32 v[20:21], v[20:21], v[112:113] op_sel_hi:[1,0] neg_lo:[0,1] neg_hi:[0,1]
	v_pk_add_f32 v[62:63], v[120:121], v[24:25]
	v_cvt_pk_bf16_f32 v24, v40, v41
	v_cvt_pk_bf16_f32 v25, v42, v43
	v_pk_add_f32 v[22:23], v[22:23], v[112:113] op_sel_hi:[1,0] neg_lo:[0,1] neg_hi:[0,1]
	v_exp_f32_e32 v36, v20
	s_waitcnt lgkmcnt(14)
	v_mfma_f32_16x16x32_bf16 v[28:31], v[44:47], v[24:27], 0
	v_exp_f32_e32 v37, v21
	v_exp_f32_e32 v38, v22
	v_exp_f32_e32 v39, v23
	v_mfma_f32_16x16x32_bf16 v[8:11], v[8:11], v[24:27], 0
	v_add_f32_e64 v42, v16, -v112
	v_add_f32_e64 v43, v17, -v112
	v_pk_add_f32 v[44:45], v[18:19], v[112:113] op_sel_hi:[1,0] neg_lo:[0,1] neg_hi:[0,1]
	v_pk_add_f32 v[40:41], v[36:37], v[62:63]
	v_mfma_f32_16x16x32_bf16 v[20:23], v[50:53], v[24:27], 0
	v_add_f32_e64 v40, v38, v40
	v_add_f32_e64 v41, v39, v41
	v_pk_add_f32 v[0:1], v[0:1], v[112:113] op_sel_hi:[1,0] neg_lo:[0,1] neg_hi:[0,1]
	v_mov_b32_e32 v64, v65
	v_mfma_f32_16x16x32_bf16 v[16:19], v[58:61], v[24:27], 0
	v_cvt_pk_bf16_f32 v24, v32, v33
	v_cvt_pk_bf16_f32 v25, v34, v35
	v_cvt_pk_bf16_f32 v26, v114, v115
	v_cvt_pk_bf16_f32 v27, v116, v117
	v_exp_f32_e32 v32, v42
	v_exp_f32_e32 v33, v43
	v_mfma_f32_16x16x32_bf16 v[28:31], v[54:57], v[24:27], v[28:31]
	v_exp_f32_e32 v34, v44
	v_exp_f32_e32 v35, v45
	v_pk_add_f32 v[42:43], v[4:5], v[112:113] op_sel_hi:[1,0] neg_lo:[0,1] neg_hi:[0,1]
	v_mfma_f32_16x16x32_bf16 v[8:11], v[66:69], v[24:27], v[8:11]
	v_add_f32_e64 v44, v6, -v112
	v_add_f32_e64 v45, v7, -v112
	v_pk_add_f32 v[40:41], v[32:33], v[40:41]
	s_waitcnt lgkmcnt(1)
	v_mov_b32_e32 v50, v48
	v_mfma_f32_16x16x32_bf16 v[4:7], v[78:81], v[24:27], v[16:19]
	v_add_f32_e64 v40, v34, v40
	v_add_f32_e64 v41, v35, v41
	v_mov_b32_e32 v51, v49
	s_and_b64 s[6:7], s[26:27], exec
	v_cvt_pk_bf16_f32 v16, v118, v119
	v_cvt_pk_bf16_f32 v17, v120, v121
	v_cvt_pk_bf16_f32 v18, v36, v37
	v_cvt_pk_bf16_f32 v19, v38, v39
	v_mfma_f32_16x16x32_bf16 v[20:23], v[70:73], v[24:27], v[20:23]
	v_add_f32_e64 v38, v2, -v112
	v_add_f32_e64 v39, v3, -v112
	s_mov_b32 s6, 0xe800000
	s_cselect_b32 s8, s6, 0x2e800000
	v_mfma_f32_16x16x32_bf16 v[24:27], v[74:77], v[16:19], v[28:31]
	s_and_b64 s[6:7], s[28:29], exec
	s_cselect_b32 s6, 0x12800000, s8
	s_add_u32 s6, s42, s6
	v_exp_f32_e32 v28, v42
	v_exp_f32_e32 v29, v43
	v_exp_f32_e32 v30, v44
	v_exp_f32_e32 v31, v45
	v_mfma_f32_16x16x32_bf16 v[8:11], v[82:85], v[16:19], v[8:11]
	v_add_f32_e64 v36, v28, v40
	v_add_f32_e64 v37, v29, v41
	v_exp_f32_e32 v40, v0
	v_exp_f32_e32 v41, v1
	v_mfma_f32_16x16x32_bf16 v[0:3], v[98:101], v[16:19], v[4:7]
	s_addc_u32 s7, s43, 0
	s_lshl_b32 s66, s22, 6
	v_cvt_pk_bf16_f32 v62, v40, v41
	v_cvt_pk_bf16_f32 v4, v32, v33
	v_cvt_pk_bf16_f32 v5, v34, v35
	v_cvt_pk_bf16_f32 v6, v28, v29
	v_cvt_pk_bf16_f32 v7, v30, v31
	v_mfma_f32_16x16x32_bf16 v[20:23], v[90:93], v[16:19], v[20:23]
	s_nop 0
	v_mfma_f32_16x16x32_bf16 v[16:19], v[94:97], v[4:7], v[24:27]
	s_nop 2
	v_exp_f32_e32 v24, v38
	v_exp_f32_e32 v25, v39
	v_mfma_f32_16x16x32_bf16 v[8:11], v[104:107], v[4:7], v[8:11]
	v_mov_b32_e32 v104, v102
	v_mov_b32_e32 v105, v103
	v_cvt_pk_bf16_f32 v63, v24, v25
	v_mfma_f32_16x16x32_bf16 v[20:23], v[108:111], v[4:7], v[20:23]
	v_add_f32_e64 v26, v30, v36
	v_add_f32_e64 v27, v31, v37
	v_pk_add_f32 v[26:27], v[40:41], v[26:27]
	v_mfma_f32_16x16x32_bf16 v[0:3], v[86:89], v[4:7], v[0:3]
	v_add_f32_e64 v26, v24, v26
	v_add_f32_e64 v27, v25, v27
	v_pk_add_f32 v[26:27], v[26:27], v[26:27] op_sel:[0,1] op_sel_hi:[1,0]
	v_mfma_f32_16x16x32_bf16 v[4:7], v[102:105], v[62:65], v[16:19]
	v_mov_b32_e32 v27, v26
	s_nop 1
	v_permlane16_swap_b32_e32 v26, v27
	v_mov_b32_e32 v16, v14
	v_mov_b32_e32 v17, v15
	v_add_f32_e32 v24, v26, v27
	s_nop 0
	v_mfma_f32_16x16x32_bf16 v[8:11], v[14:17], v[62:65], v[8:11]
	s_waitcnt lgkmcnt(0)
	v_mov_b32_e32 v14, v12
	v_mov_b32_e32 v15, v13
	v_mfma_f32_16x16x32_bf16 v[16:19], v[48:51], v[62:65], v[20:23]
	s_nop 2
	v_mov_b32_e32 v20, v24
	s_nop 1
	v_permlane32_swap_b32_e32 v24, v20
	v_mfma_f32_16x16x32_bf16 v[12:15], v[12:15], v[62:65], v[0:3]
	s_nop 2
	v_add_f32_e32 v0, v24, v20
	v_rcp_f32_e32 v1, v0
	s_nop 0
	v_mul_f32_e32 v1, 0x42800000, v1
	v_mul_f32_e32 v2, v1, v4
	v_mul_f32_e32 v3, v1, v5
	v_med3_f32 v5, v2, s55, v228
	v_med3_f32 v3, v3, s55, v228
	v_mov_b32_e32 v2, v65
	v_cvt_pk_fp8_f32 v2, v5, v3
	v_mul_f32_e32 v4, v1, v6
	v_mul_f32_e32 v3, v1, v7
	v_med3_f32 v4, v4, s55, v228
	v_med3_f32 v3, v3, s55, v228
	v_cvt_pk_fp8_f32 v2, v4, v3 op_sel:[0,0,1]
	v_mul_f32_e32 v3, v1, v8
	v_mul_f32_e32 v4, v1, v9
	v_med3_f32 v6, v3, s55, v228
	v_med3_f32 v4, v4, s55, v228
	v_mov_b32_e32 v3, v65
	v_cvt_pk_fp8_f32 v3, v6, v4
	v_mul_f32_e32 v5, v1, v10
	v_mul_f32_e32 v4, v1, v11
	v_med3_f32 v5, v5, s55, v228
	v_med3_f32 v4, v4, s55, v228
	v_cvt_pk_fp8_f32 v3, v5, v4 op_sel:[0,0,1]
	v_mul_f32_e32 v4, v1, v16
	v_mul_f32_e32 v5, v1, v17
	v_med3_f32 v7, v4, s55, v228
	v_med3_f32 v5, v5, s55, v228
	v_mov_b32_e32 v4, v65
	v_cvt_pk_fp8_f32 v4, v7, v5
	v_mul_f32_e32 v6, v1, v18
	v_mul_f32_e32 v5, v1, v19
	v_med3_f32 v6, v6, s55, v228
	v_med3_f32 v5, v5, s55, v228
	v_cvt_pk_fp8_f32 v4, v6, v5 op_sel:[0,0,1]
	v_mul_f32_e32 v5, v1, v12
	v_mul_f32_e32 v6, v1, v13
	v_med3_f32 v8, v5, s55, v228
	v_med3_f32 v6, v6, s55, v228
	v_mov_b32_e32 v5, v65
	v_cvt_pk_fp8_f32 v5, v8, v6
	v_mul_f32_e32 v7, v1, v14
	v_mul_f32_e32 v1, v1, v15
	v_med3_f32 v6, v7, s55, v228
	v_med3_f32 v1, v1, s55, v228
	v_cvt_pk_fp8_f32 v5, v6, v1 op_sel:[0,0,1]
	v_lshlrev_b64 v[6:7], 10, v[164:165]
	v_lshl_add_u64 v[6:7], s[6:7], 0, v[6:7]
	v_lshl_add_u64 v[6:7], v[6:7], 0, s[66:67]
	v_lshl_add_u64 v[6:7], v[6:7], 0, v[160:161]
	global_store_dwordx4 v[6:7], v[2:5], off sc1
	s_and_saveexec_b64 s[6:7], vcc
	s_cbranch_execz .LBB0_422
	v_log_f32_e32 v0, v0
	s_ashr_i32 s25, s24, 31
	s_lshl_b64 s[8:9], s[24:25], 22
	v_readlane_b32 s10, v254, 30
	s_add_u32 s8, s10, s8
	v_readlane_b32 s10, v254, 31
	s_addc_u32 s9, s10, s9
	v_add_f32_e32 v0, v112, v0
	v_mul_f32_e32 v2, 0x3f317218, v0
	v_lshl_add_u64 v[0:1], s[8:9], 0, v[162:163]
	s_lshl_b32 s66, s22, 2
	v_lshl_add_u64 v[0:1], v[0:1], 0, s[66:67]
	global_store_dword v[0:1], v2, off

.LBB0_472:
	s_and_b32 s24, s30, 3
	s_lshl_b32 s25, s24, 8
	v_mov_b32_e32 v16, s25
	s_barrier
	global_load_dwordx4 v[20:23], v16, s[22:23]
	s_nop 0
	global_load_dwordx4 v[16:19], v16, s[22:23] offset:16
	s_waitcnt vmcnt(4)
	v_lshlrev_b32_e32 v50, 16, v4
	v_and_b32_e32 v51, 0xffff0000, v4
	v_lshlrev_b32_e32 v52, 16, v5
	v_readlane_b32 s26, v254, 34
	s_or_b32 s24, s24, s26
	v_and_b32_e32 v53, 0xffff0000, v5
	v_lshlrev_b32_e32 v34, 16, v0
	v_and_b32_e32 v35, 0xffff0000, v0
	v_lshlrev_b32_e32 v49, 16, v6
	v_and_b32_e32 v48, 0xffff0000, v6
	v_lshlrev_b32_e32 v47, 16, v7
	v_and_b32_e32 v46, 0xffff0000, v7
	s_lshr_b32 s25, s30, 2
	s_add_i32 s25, s25, s3
	s_lshl_b32 s24, s24, 7
	s_add_i32 s24, s25, s24
	s_ashr_i32 s25, s24, 31
	s_lshl_b64 s[24:25], s[24:25], 6
	s_waitcnt vmcnt(3)
	ds_write_b128 v42, v[8:11] offset:39168
	s_waitcnt vmcnt(2)
	ds_write_b128 v43, v[12:15] offset:39168
	s_waitcnt vmcnt(1)
	v_add_f32_e32 v20, v20, v50
	v_add_f32_e32 v21, v21, v51
	v_min_f32_e32 v50, 0, v20
	v_mul_f32_e64 v20, |v20|, s0
	v_min_f32_e32 v51, 0, v21
	v_mul_f32_e64 v21, |v21|, s0
	v_exp_f32_e32 v20, v20
	v_exp_f32_e32 v21, v21
	v_add_f32_e32 v22, v22, v52
	v_min_f32_e32 v52, 0, v22
	v_add_f32_e32 v20, 1.0, v20
	v_add_f32_e32 v21, 1.0, v21
	v_log_f32_e32 v20, v20
	v_log_f32_e32 v21, v21
	v_mul_f32_e64 v22, |v22|, s0
	v_exp_f32_e32 v22, v22
	v_fmac_f32_e32 v50, 0xbf317218, v20
	v_fmac_f32_e32 v51, 0xbf317218, v21
	v_mul_f32_e32 v20, 0x3d800000, v50
	v_mul_f32_e32 v21, 0x3d800000, v51
	v_add_f32_e32 v22, 1.0, v22
	v_mov_b32_dpp v20, v20 row_shr:1 row_mask:0xf bank_mask:0xf bound_ctrl:1
	v_mov_b32_dpp v21, v21 row_shr:1 row_mask:0xf bank_mask:0xf bound_ctrl:1
	v_log_f32_e32 v22, v22
	v_fmac_f32_e32 v20, 0x3d800000, v50
	v_fmac_f32_e32 v21, 0x3d800000, v51
	v_add_f32_e32 v23, v23, v53
	v_add_f32_dpp v20, v20, v20 row_shr:2 row_mask:0xf bank_mask:0xf bound_ctrl:1
	v_add_f32_dpp v21, v21, v21 row_shr:2 row_mask:0xf bank_mask:0xf bound_ctrl:1
	v_fmac_f32_e32 v52, 0xbf317218, v22
	v_add_f32_dpp v20, v20, v20 row_shr:4 row_mask:0xf bank_mask:0xf bound_ctrl:1
	v_add_f32_dpp v21, v21, v21 row_shr:4 row_mask:0xf bank_mask:0xf bound_ctrl:1
	v_mul_f32_e32 v22, 0x3d800000, v52
	v_add_f32_dpp v20, v20, v20 row_shr:8 row_mask:0xf bank_mask:0xf bound_ctrl:1
	v_add_f32_dpp v21, v21, v21 row_shr:8 row_mask:0xf bank_mask:0xf bound_ctrl:1
	v_readlane_b32 s26, v20, 15
	v_readlane_b32 s34, v21, 15
	v_readlane_b32 s27, v20, 31
	v_readlane_b32 s35, v21, 31
	v_mov_b32_e32 v50, s26
	v_mov_b32_e32 v54, s34
	v_mov_b32_dpp v22, v22 row_shr:1 row_mask:0xf bank_mask:0xf bound_ctrl:1
	v_readlane_b32 s31, v20, 47
	v_readlane_b32 s36, v21, 47
	v_mov_b32_e32 v51, s27
	v_mov_b32_e32 v55, s35
	v_cndmask_b32_e64 v50, v50, 0, vcc
	v_cndmask_b32_e64 v54, v54, 0, vcc
	v_fmac_f32_e32 v22, 0x3d800000, v52
	v_mov_b32_e32 v52, s31
	v_mov_b32_e32 v56, s36
	v_cndmask_b32_e64 v51, 0, v51, s[6:7]
	v_cndmask_b32_e64 v55, 0, v55, s[6:7]
	v_add_f32_e32 v20, v50, v20
	v_add_f32_e32 v21, v21, v54
	v_cndmask_b32_e64 v52, 0, v52, s[8:9]
	v_cndmask_b32_e64 v56, 0, v56, s[8:9]
	v_add_f32_e32 v20, v51, v20
	v_add_f32_e32 v21, v21, v55
	v_add_f32_e32 v20, v52, v20
	v_add_f32_e32 v21, v21, v56
	v_readlane_b32 s34, v20, 63
	v_readlane_b32 s31, v21, 63
	v_mul_f32_e64 v53, |v23|, s0
	v_sub_f32_e32 v20, s34, v20
	v_sub_f32_e32 v21, s31, v21
	v_mul_f32_e32 v20, 0x3fb8aa3b, v20
	v_mul_f32_e32 v21, 0x3fb8aa3b, v21
	v_exp_f32_e32 v53, v53
	v_exp_f32_e32 v20, v20
	v_exp_f32_e32 v21, v21
	v_min_f32_e32 v23, 0, v23
	v_add_f32_dpp v22, v22, v22 row_shr:2 row_mask:0xf bank_mask:0xf bound_ctrl:1
	s_waitcnt vmcnt(0)
	v_add_f32_e32 v16, v16, v49
	v_pk_mul_f32 v[20:21], v[20:21], v[34:35]
	v_add_f32_e32 v34, 1.0, v53
	v_log_f32_e32 v34, v34
	v_add_f32_dpp v22, v22, v22 row_shr:4 row_mask:0xf bank_mask:0xf bound_ctrl:1
	v_add_f32_e32 v17, v17, v48
	v_add_f32_e32 v18, v18, v47
	v_fmac_f32_e32 v23, 0xbf317218, v34
	v_mul_f32_e32 v34, 0x3d800000, v23
	v_add_f32_dpp v22, v22, v22 row_shr:8 row_mask:0xf bank_mask:0xf bound_ctrl:1
	v_add_f32_e32 v19, v19, v46
	v_mov_b32_dpp v34, v34 row_shr:1 row_mask:0xf bank_mask:0xf bound_ctrl:1
	v_fmac_f32_e32 v34, 0x3d800000, v23
	v_readlane_b32 s37, v22, 15
	v_readlane_b32 s38, v22, 31
	v_add_f32_dpp v23, v34, v34 row_shr:2 row_mask:0xf bank_mask:0xf bound_ctrl:1
	v_mov_b32_e32 v57, s37
	v_readlane_b32 s39, v22, 47
	v_add_f32_dpp v23, v23, v23 row_shr:4 row_mask:0xf bank_mask:0xf bound_ctrl:1
	v_mov_b32_e32 v58, s38
	v_cndmask_b32_e64 v57, v57, 0, vcc
	v_add_f32_dpp v23, v23, v23 row_shr:8 row_mask:0xf bank_mask:0xf bound_ctrl:1
	v_mov_b32_e32 v59, s39
	v_readlane_b32 s26, v23, 15
	v_readlane_b32 s27, v23, 31
	v_readlane_b32 s36, v23, 47
	v_mov_b32_e32 v34, s26
	v_cndmask_b32_e64 v34, v34, 0, vcc
	v_add_f32_e32 v23, v23, v34
	v_mov_b32_e32 v34, s27
	v_cndmask_b32_e64 v34, 0, v34, s[6:7]
	v_add_f32_e32 v23, v23, v34
	v_mov_b32_e32 v34, s36
	v_cndmask_b32_e64 v34, 0, v34, s[8:9]
	v_add_f32_e32 v23, v23, v34
	v_mul_f32_e64 v34, |v16|, s0
	v_cndmask_b32_e64 v58, 0, v58, s[6:7]
	v_add_f32_e32 v22, v22, v57
	v_exp_f32_e32 v35, v34
	v_cndmask_b32_e64 v59, 0, v59, s[8:9]
	v_add_f32_e32 v22, v22, v58
	v_add_f32_e32 v22, v22, v59
	v_readlane_b32 s36, v23, 63
	v_readlane_b32 s35, v22, 63
	v_add_f32_e32 v35, 1.0, v35
	v_sub_f32_e32 v23, s36, v23
	v_sub_f32_e32 v22, s35, v22
	v_mul_f32_e32 v22, 0x3fb8aa3b, v22
	v_mul_f32_e32 v23, 0x3fb8aa3b, v23
	v_log_f32_e32 v49, v35
	v_exp_f32_e32 v22, v22
	v_exp_f32_e32 v23, v23
	v_min_f32_e32 v16, 0, v16
	v_lshlrev_b32_e32 v34, 16, v1
	v_and_b32_e32 v35, 0xffff0000, v1
	v_fmac_f32_e32 v16, 0xbf317218, v49
	v_pk_mul_f32 v[22:23], v[22:23], v[34:35]
	v_mul_f32_e32 v34, 0x3d800000, v16
	v_mul_f32_e64 v35, |v17|, s0
	v_exp_f32_e32 v35, v35
	v_mov_b32_dpp v34, v34 row_shr:1 row_mask:0xf bank_mask:0xf bound_ctrl:1
	v_fmac_f32_e32 v34, 0x3d800000, v16
	v_min_f32_e32 v17, 0, v17
	v_mul_f32_e64 v46, |v19|, s0
	v_add_f32_dpp v16, v34, v34 row_shr:2 row_mask:0xf bank_mask:0xf bound_ctrl:1
	v_exp_f32_e32 v46, v46
	v_min_f32_e32 v19, 0, v19
	v_add_f32_dpp v16, v16, v16 row_shr:4 row_mask:0xf bank_mask:0xf bound_ctrl:1
	v_add_f32_e32 v46, 1.0, v46
	s_nop 0
	v_add_f32_dpp v16, v16, v16 row_shr:8 row_mask:0xf bank_mask:0xf bound_ctrl:1
	v_log_f32_e32 v46, v46
	v_readlane_b32 s26, v16, 15
	v_readlane_b32 s27, v16, 31
	v_readlane_b32 s37, v16, 47
	v_mov_b32_e32 v34, s26
	v_cndmask_b32_e64 v34, v34, 0, vcc
	v_add_f32_e32 v16, v16, v34
	v_mov_b32_e32 v34, s27
	v_cndmask_b32_e64 v34, 0, v34, s[6:7]
	v_add_f32_e32 v16, v16, v34
	v_mov_b32_e32 v34, s37
	v_cndmask_b32_e64 v34, 0, v34, s[8:9]
	v_add_f32_e32 v16, v16, v34
	v_add_f32_e32 v34, 1.0, v35
	v_log_f32_e32 v34, v34
	v_fmac_f32_e32 v19, 0xbf317218, v46
	v_mul_f32_e32 v46, 0x3d800000, v19
	v_readlane_b32 s37, v16, 63
	v_fmac_f32_e32 v17, 0xbf317218, v34
	v_mul_f32_e32 v34, 0x3d800000, v17
	v_mov_b32_dpp v46, v46 row_shr:1 row_mask:0xf bank_mask:0xf bound_ctrl:1
	v_fmac_f32_e32 v46, 0x3d800000, v19
	v_mov_b32_dpp v34, v34 row_shr:1 row_mask:0xf bank_mask:0xf bound_ctrl:1
	v_fmac_f32_e32 v34, 0x3d800000, v17
	v_add_f32_dpp v19, v46, v46 row_shr:2 row_mask:0xf bank_mask:0xf bound_ctrl:1
	v_sub_f32_e32 v16, s37, v16
	v_add_f32_dpp v17, v34, v34 row_shr:2 row_mask:0xf bank_mask:0xf bound_ctrl:1
	v_add_f32_dpp v19, v19, v19 row_shr:4 row_mask:0xf bank_mask:0xf bound_ctrl:1
	v_mul_f32_e32 v16, 0x3fb8aa3b, v16
	v_add_f32_dpp v17, v17, v17 row_shr:4 row_mask:0xf bank_mask:0xf bound_ctrl:1
	v_add_f32_dpp v19, v19, v19 row_shr:8 row_mask:0xf bank_mask:0xf bound_ctrl:1
	v_exp_f32_e32 v16, v16
	v_add_f32_dpp v17, v17, v17 row_shr:8 row_mask:0xf bank_mask:0xf bound_ctrl:1
	v_readlane_b32 s49, v19, 47
	v_readlane_b32 s26, v17, 15
	v_readlane_b32 s27, v17, 31
	v_readlane_b32 s38, v17, 47
	v_mov_b32_e32 v34, s26
	v_cndmask_b32_e64 v34, v34, 0, vcc
	v_add_f32_e32 v17, v17, v34
	v_mov_b32_e32 v34, s27
	v_cndmask_b32_e64 v34, 0, v34, s[6:7]
	v_add_f32_e32 v17, v17, v34
	v_mov_b32_e32 v34, s38
	v_cndmask_b32_e64 v34, 0, v34, s[8:9]
	v_add_f32_e32 v17, v17, v34
	v_mul_f32_e64 v34, |v18|, s0
	v_exp_f32_e32 v34, v34
	v_min_f32_e32 v18, 0, v18
	v_readlane_b32 s38, v17, 63
	v_and_b32_e32 v35, 0xffff0000, v2
	v_add_f32_e32 v34, 1.0, v34
	v_log_f32_e32 v47, v34
	v_sub_f32_e32 v17, s38, v17
	v_mul_f32_e32 v17, 0x3fb8aa3b, v17
	v_exp_f32_e32 v17, v17
	v_fmac_f32_e32 v18, 0xbf317218, v47
	v_mul_f32_e32 v47, 0x3d800000, v18
	v_lshlrev_b32_e32 v34, 16, v2
	v_pk_mul_f32 v[34:35], v[16:17], v[34:35]
	v_mov_b32_dpp v47, v47 row_shr:1 row_mask:0xf bank_mask:0xf bound_ctrl:1
	v_fmac_f32_e32 v47, 0x3d800000, v18
	v_lshlrev_b32_e32 v16, 16, v3
	v_and_b32_e32 v17, 0xffff0000, v3
	v_add_f32_dpp v18, v47, v47 row_shr:2 row_mask:0xf bank_mask:0xf bound_ctrl:1
	s_nop 1
	v_add_f32_dpp v18, v18, v18 row_shr:4 row_mask:0xf bank_mask:0xf bound_ctrl:1
	s_nop 1
	v_add_f32_dpp v18, v18, v18 row_shr:8 row_mask:0xf bank_mask:0xf bound_ctrl:1
	s_nop 0
	v_readlane_b32 s26, v18, 15
	v_readlane_b32 s27, v18, 31
	v_readlane_b32 s39, v18, 47
	v_mov_b32_e32 v47, s26
	v_readlane_b32 s26, v19, 15
	v_cndmask_b32_e64 v47, v47, 0, vcc
	v_add_f32_e32 v18, v18, v47
	v_mov_b32_e32 v46, s26
	v_mov_b32_e32 v47, s27
	v_readlane_b32 s27, v19, 31
	v_cndmask_b32_e64 v46, v46, 0, vcc
	v_add_f32_e32 v19, v19, v46
	v_mov_b32_e32 v46, s27
	v_cndmask_b32_e64 v47, 0, v47, s[6:7]
	v_cndmask_b32_e64 v46, 0, v46, s[6:7]
	v_add_f32_e32 v18, v18, v47
	v_mov_b32_e32 v47, s39
	v_add_f32_e32 v19, v19, v46
	v_mov_b32_e32 v46, s49
	v_cndmask_b32_e64 v47, 0, v47, s[8:9]
	v_cndmask_b32_e64 v46, 0, v46, s[8:9]
	v_add_f32_e32 v18, v18, v47
	v_add_f32_e32 v19, v19, v46
	v_readlane_b32 s39, v18, 63
	v_readlane_b32 s49, v19, 63
	s_nop 0
	v_sub_f32_e32 v18, s39, v18
	v_sub_f32_e32 v19, s49, v19
	v_mul_f32_e32 v18, 0x3fb8aa3b, v18
	v_mul_f32_e32 v19, 0x3fb8aa3b, v19
	v_exp_f32_e32 v18, v18
	v_exp_f32_e32 v19, v19
	s_nop 0
	v_pk_mul_f32 v[46:47], v[18:19], v[16:17]
	v_cvt_pk_bf16_f32 v16, v20, v21
	v_cvt_pk_bf16_f32 v17, v22, v23
	v_cvt_pk_bf16_f32 v18, v34, v35
	v_cvt_pk_bf16_f32 v19, v46, v47
	ds_write_b128 v44, v[16:19] offset:28928
	s_and_saveexec_b64 s[26:27], s[10:11]
	s_cbranch_execz .LBB0_474
	v_mov_b32_e32 v23, 0x3fb8aa3b
	v_mul_f32_e32 v16, s34, v23
	v_mul_f32_e32 v17, s31, v23
	v_mul_f32_e32 v18, s35, v23
	v_mul_f32_e32 v19, s36, v23
	v_exp_f32_e32 v16, v16
	v_exp_f32_e32 v17, v17
	v_exp_f32_e32 v18, v18
	v_exp_f32_e32 v19, v19
	v_mul_f32_e32 v20, s37, v23
	v_mul_f32_e32 v21, s38, v23
	v_mul_f32_e32 v22, s39, v23
	v_mul_f32_e32 v23, s49, v23
	v_exp_f32_e32 v20, v20
	v_exp_f32_e32 v21, v21
	v_exp_f32_e32 v22, v22
	v_exp_f32_e32 v23, v23
	s_lshl_b64 s[34:35], s[24:25], 2
	s_add_u32 s34, s28, s34
	s_addc_u32 s35, s29, s35
	global_store_dwordx4 v65, v[16:19], s[34:35] sc1
	global_store_dwordx4 v65, v[20:23], s[34:35] offset:16 sc1

.LBB0_571:
	s_or_b64 exec, exec, s[28:29]
	s_waitcnt lgkmcnt(0)
	s_barrier
	ds_read_b128 v[52:55], v100
	ds_read_b128 v[56:59], v100 offset:256
	s_lshl_b32 s28, s49, 7
	s_lshl_b32 s66, s28, 1
	s_add_i32 s59, s59, 1
	s_cmp_lg_u32 s59, 16
	s_waitcnt lgkmcnt(0)
	v_add_f32_e32 v52, v52, v56
	v_fmamk_f32 v52, v52, 0x3c000000, v229
	v_rsq_f32_e32 v52, v52
	s_nop 0
	v_mul_f32_e32 v56, v36, v52
	global_load_dword v36, v[84:85], off
	s_waitcnt vmcnt(0)
	v_mul_f32_e32 v56, v36, v56
	v_bfe_u32 v60, v56, 16, 1
	v_add3_u32 v56, v56, v60, s60
	v_add_u32_e32 v60, v108, v101
	ds_write_b16_d16_hi v60, v56 offset:57600
	v_mul_f32_e32 v56, v40, v52
	global_load_dword v40, v[86:87], off
	s_waitcnt vmcnt(0)
	v_mul_f32_e32 v56, v40, v56
	v_bfe_u32 v60, v56, 16, 1
	v_add3_u32 v56, v56, v60, s60
	v_add_u32_e32 v60, v108, v102
	ds_write_b16_d16_hi v60, v56 offset:57600
	v_mul_f32_e32 v56, v44, v52
	global_load_dword v44, v[88:89], off
	v_mul_f32_e32 v52, v48, v52
	global_load_dword v48, v[90:91], off
	s_waitcnt vmcnt(1)
	v_mul_f32_e32 v56, v44, v56
	v_bfe_u32 v60, v56, 16, 1
	v_add3_u32 v56, v56, v60, s60
	v_add_u32_e32 v60, v108, v103
	s_waitcnt vmcnt(0)
	v_mul_f32_e32 v52, v52, v48
	ds_write_b16_d16_hi v60, v56 offset:57600
	v_bfe_u32 v56, v52, 16, 1
	v_add3_u32 v52, v52, v56, s60
	v_add_u32_e32 v56, v108, v104
	ds_write_b16_d16_hi v56, v52 offset:57600
	v_add_f32_e32 v52, v53, v57
	v_fmamk_f32 v52, v52, 0x3c000000, v229
	v_rsq_f32_e32 v52, v52
	s_nop 0
	v_mul_f32_e32 v37, v37, v52
	v_mul_f32_e32 v37, v36, v37
	v_bfe_u32 v53, v37, 16, 1
	v_add3_u32 v37, v37, v53, s60
	v_add_u32_e32 v53, v109, v101
	ds_write_b16_d16_hi v53, v37 offset:57600
	v_mul_f32_e32 v37, v41, v52
	v_mul_f32_e32 v37, v40, v37
	v_bfe_u32 v41, v37, 16, 1
	v_add3_u32 v37, v37, v41, s60
	v_add_u32_e32 v41, v109, v102
	ds_write_b16_d16_hi v41, v37 offset:57600
	v_mul_f32_e32 v37, v45, v52
	v_mul_f32_e32 v37, v44, v37
	v_bfe_u32 v41, v37, 16, 1
	v_add3_u32 v37, v37, v41, s60
	v_add_u32_e32 v41, v109, v103
	ds_write_b16_d16_hi v41, v37 offset:57600
	v_mul_f32_e32 v37, v49, v52
	v_mul_f32_e32 v37, v48, v37
	v_bfe_u32 v41, v37, 16, 1
	v_add3_u32 v37, v37, v41, s60
	v_add_u32_e32 v41, v109, v104
	ds_write_b16_d16_hi v41, v37 offset:57600
	v_add_f32_e32 v37, v54, v58
	v_fmamk_f32 v37, v37, 0x3c000000, v229
	v_rsq_f32_e32 v37, v37
	v_and_b32_e32 v45, 0xffff0000, v32
	v_mul_f32_e32 v38, v38, v37
	v_mul_f32_e32 v38, v36, v38
	v_bfe_u32 v41, v38, 16, 1
	v_add3_u32 v38, v38, v41, s60
	v_add_u32_e32 v41, v110, v101
	ds_write_b16_d16_hi v41, v38 offset:57600
	v_mul_f32_e32 v38, v42, v37
	v_mul_f32_e32 v38, v40, v38
	v_bfe_u32 v41, v38, 16, 1
	v_add3_u32 v38, v38, v41, s60
	v_add_u32_e32 v41, v110, v102
	ds_write_b16_d16_hi v41, v38 offset:57600
	v_mul_f32_e32 v38, v46, v37
	v_mul_f32_e32 v38, v44, v38
	v_bfe_u32 v41, v38, 16, 1
	v_mul_f32_e32 v37, v50, v37
	v_add3_u32 v38, v38, v41, s60
	v_add_u32_e32 v41, v110, v103
	v_mul_f32_e32 v37, v48, v37
	ds_write_b16_d16_hi v41, v38 offset:57600
	v_bfe_u32 v38, v37, 16, 1
	v_add3_u32 v37, v37, v38, s60
	v_add_u32_e32 v38, v110, v104
	ds_write_b16_d16_hi v38, v37 offset:57600
	v_add_f32_e32 v37, v55, v59
	v_fmamk_f32 v37, v37, 0x3c000000, v229
	v_rsq_f32_e32 v37, v37
	s_nop 0
	v_mul_f32_e32 v38, v39, v37
	v_mul_f32_e32 v36, v36, v38
	v_bfe_u32 v38, v36, 16, 1
	v_add3_u32 v36, v36, v38, s60
	v_add_u32_e32 v38, v111, v101
	ds_write_b16_d16_hi v38, v36 offset:57600
	v_mul_f32_e32 v36, v43, v37
	v_mul_f32_e32 v36, v40, v36
	v_bfe_u32 v38, v36, 16, 1
	v_add3_u32 v36, v36, v38, s60
	v_add_u32_e32 v38, v111, v102
	ds_write_b16_d16_hi v38, v36 offset:57600
	v_mul_f32_e32 v36, v47, v37
	v_mul_f32_e32 v36, v44, v36
	v_lshlrev_b32_e32 v44, 16, v32
	v_mul_f32_e32 v32, 0xbfb8aa3b, v44
	v_exp_f32_e32 v32, v32
	v_bfe_u32 v38, v36, 16, 1
	v_add3_u32 v36, v36, v38, s60
	v_add_u32_e32 v38, v111, v103
	v_add_f32_e32 v32, 1.0, v32
	v_rcp_f32_e32 v46, v32
	v_mul_f32_e32 v32, 0xbfb8aa3b, v45
	ds_write_b16_d16_hi v38, v36 offset:57600
	v_mul_f32_e32 v36, v51, v37
	v_exp_f32_e32 v32, v32
	v_mul_f32_e32 v36, v48, v36
	v_bfe_u32 v37, v36, 16, 1
	v_add3_u32 v36, v36, v37, s60
	v_add_u32_e32 v37, v111, v104
	ds_write_b16_d16_hi v37, v36 offset:57600
	s_waitcnt lgkmcnt(0)
	s_barrier
	ds_read_b128 v[38:41], v116 offset:57600
	v_add_f32_e32 v32, 1.0, v32
	v_rcp_f32_e32 v47, v32
	v_lshlrev_b32_e32 v32, 16, v33
	v_and_b32_e32 v33, 0xffff0000, v33
	s_waitcnt lgkmcnt(0)
	v_lshlrev_b32_e32 v42, 16, v38
	v_and_b32_e32 v43, 0xffff0000, v38
	v_pk_mul_f32 v[44:45], v[46:47], v[44:45]
	v_lshlrev_b32_e32 v38, 16, v39
	v_pk_mul_f32 v[42:43], v[44:45], v[42:43]
	v_mul_f32_e32 v44, 0xbfb8aa3b, v32
	v_mul_f32_e32 v45, 0xbfb8aa3b, v33
	v_exp_f32_e32 v44, v44
	v_exp_f32_e32 v45, v45
	v_and_b32_e32 v39, 0xffff0000, v39
	v_lshl_add_u64 v[36:37], v[80:81], 0, s[66:67]
	v_add_f32_e32 v44, 1.0, v44
	v_add_f32_e32 v45, 1.0, v45
	v_rcp_f32_e32 v44, v44
	v_rcp_f32_e32 v45, v45
	s_nop 0
	v_pk_mul_f32 v[32:33], v[44:45], v[32:33]
	v_lshlrev_b32_e32 v44, 16, v34
	v_and_b32_e32 v45, 0xffff0000, v34
	v_mul_f32_e32 v34, 0xbfb8aa3b, v44
	v_exp_f32_e32 v34, v34
	v_pk_mul_f32 v[38:39], v[32:33], v[38:39]
	v_lshlrev_b32_e32 v32, 16, v40
	v_and_b32_e32 v33, 0xffff0000, v40
	v_add_f32_e32 v34, 1.0, v34
	v_rcp_f32_e32 v46, v34
	v_mul_f32_e32 v34, 0xbfb8aa3b, v45
	v_exp_f32_e32 v34, v34
	s_nop 0
	v_add_f32_e32 v34, 1.0, v34
	v_rcp_f32_e32 v47, v34
	v_lshlrev_b32_e32 v34, 16, v35
	v_and_b32_e32 v35, 0xffff0000, v35
	v_mul_f32_e32 v40, 0xbfb8aa3b, v34
	v_pk_mul_f32 v[44:45], v[46:47], v[44:45]
	v_exp_f32_e32 v40, v40
	v_pk_mul_f32 v[44:45], v[44:45], v[32:33]
	v_lshlrev_b32_e32 v32, 16, v41
	v_and_b32_e32 v33, 0xffff0000, v41
	v_mul_f32_e32 v41, 0xbfb8aa3b, v35
	v_exp_f32_e32 v41, v41
	v_add_f32_e32 v40, 1.0, v40
	v_rcp_f32_e32 v40, v40
	v_add_f32_e32 v41, 1.0, v41
	v_rcp_f32_e32 v41, v41
	s_nop 0
	v_pk_mul_f32 v[34:35], v[40:41], v[34:35]
	s_nop 0
	v_pk_mul_f32 v[40:41], v[34:35], v[32:33]
	v_cvt_pk_bf16_f32 v32, v42, v43
	v_cvt_pk_bf16_f32 v35, v40, v41
	v_lshlrev_b32_e32 v40, 16, v28
	v_and_b32_e32 v41, 0xffff0000, v28
	v_mul_f32_e32 v28, 0xbfb8aa3b, v40
	v_exp_f32_e32 v28, v28
	v_cvt_pk_bf16_f32 v33, v38, v39
	v_lshlrev_b64 v[38:39], 11, v[94:95]
	v_cvt_pk_bf16_f32 v34, v44, v45
	v_add_f32_e32 v28, 1.0, v28
	v_rcp_f32_e32 v42, v28
	v_mul_f32_e32 v28, 0xbfb8aa3b, v41
	v_exp_f32_e32 v28, v28
	v_lshl_add_u64 v[38:39], v[36:37], 0, v[38:39]
	global_store_dwordx4 v[38:39], v[32:35], off sc1
	ds_read_b128 v[32:35], v117 offset:57600
	v_add_f32_e32 v28, 1.0, v28
	v_rcp_f32_e32 v43, v28
	v_lshlrev_b32_e32 v28, 16, v29
	v_and_b32_e32 v29, 0xffff0000, v29
	s_waitcnt lgkmcnt(0)
	v_lshlrev_b32_e32 v38, 16, v32
	v_and_b32_e32 v39, 0xffff0000, v32
	v_pk_mul_f32 v[40:41], v[42:43], v[40:41]
	v_lshlrev_b32_e32 v32, 16, v33
	v_pk_mul_f32 v[38:39], v[40:41], v[38:39]
	v_mul_f32_e32 v40, 0xbfb8aa3b, v28
	v_mul_f32_e32 v41, 0xbfb8aa3b, v29
	v_exp_f32_e32 v40, v40
	v_exp_f32_e32 v41, v41
	v_and_b32_e32 v33, 0xffff0000, v33
	v_add_f32_e32 v40, 1.0, v40
	v_add_f32_e32 v41, 1.0, v41
	v_rcp_f32_e32 v40, v40
	v_rcp_f32_e32 v41, v41
	s_nop 0
	v_pk_mul_f32 v[28:29], v[40:41], v[28:29]
	v_lshlrev_b32_e32 v40, 16, v30
	v_and_b32_e32 v41, 0xffff0000, v30
	v_mul_f32_e32 v30, 0xbfb8aa3b, v40
	v_exp_f32_e32 v30, v30
	v_pk_mul_f32 v[32:33], v[28:29], v[32:33]
	v_lshlrev_b32_e32 v28, 16, v34
	v_and_b32_e32 v29, 0xffff0000, v34
	v_add_f32_e32 v30, 1.0, v30
	v_rcp_f32_e32 v42, v30
	v_mul_f32_e32 v30, 0xbfb8aa3b, v41
	v_exp_f32_e32 v30, v30
	s_nop 0
	v_add_f32_e32 v30, 1.0, v30
	v_rcp_f32_e32 v43, v30
	v_lshlrev_b32_e32 v30, 16, v31
	v_and_b32_e32 v31, 0xffff0000, v31
	v_mul_f32_e32 v34, 0xbfb8aa3b, v30
	v_pk_mul_f32 v[40:41], v[42:43], v[40:41]
	v_exp_f32_e32 v34, v34
	v_pk_mul_f32 v[40:41], v[40:41], v[28:29]
	v_lshlrev_b32_e32 v28, 16, v35
	v_and_b32_e32 v29, 0xffff0000, v35
	v_mul_f32_e32 v35, 0xbfb8aa3b, v31
	v_exp_f32_e32 v35, v35
	v_add_f32_e32 v34, 1.0, v34
	v_rcp_f32_e32 v34, v34
	v_add_f32_e32 v35, 1.0, v35
	v_rcp_f32_e32 v35, v35
	s_nop 0
	v_pk_mul_f32 v[30:31], v[34:35], v[30:31]
	s_nop 0
	v_pk_mul_f32 v[34:35], v[30:31], v[28:29]
	v_cvt_pk_bf16_f32 v29, v32, v33
	v_lshlrev_b64 v[32:33], 11, v[92:93]
	v_cvt_pk_bf16_f32 v28, v38, v39
	v_cvt_pk_bf16_f32 v30, v40, v41
	v_cvt_pk_bf16_f32 v31, v34, v35
	v_lshl_add_u64 v[32:33], v[36:37], 0, v[32:33]
	global_store_dwordx4 v[32:33], v[28:31], off sc1
	s_cbranch_scc0 .LBB0_596

.LBB0_675:
	v_mov_b32_e32 v64, v136
	v_mov_b32_e32 v130, v137
	s_mov_b32 s14, s2
	s_lshl_b32 s14, s14, 8
	s_lshl_b32 s15, s34, 8
	s_add_i32 s14, s14, s27
	s_or_b32 s15, s15, s28
	v_add_u32_e32 v140, s14, v64
	v_lshl_add_u32 v130, v130, 3, s15
	v_ashrrev_i32_e32 v141, 31, v140
	v_readlane_b32 s14, v254, 24
	v_lshlrev_b64 v[140:141], 11, v[140:141]
	v_readlane_b32 s15, v254, 25
	v_ashrrev_i32_e32 v131, 31, v130
	v_pk_mul_f32 v[128:129], v[128:129], s[58:59] op_sel_hi:[1,0]
	v_lshl_add_u64 v[140:141], s[14:15], 0, v[140:141]
	v_lshl_add_u64 v[130:131], v[130:131], 1, v[140:141]
	v_pk_mul_f32 v[126:127], v[126:127], s[58:59] op_sel_hi:[1,0]
	v_pk_mul_f32 v[140:141], v[124:125], s[58:59] op_sel_hi:[1,0]
	v_pk_mul_f32 v[124:125], v[122:123], s[58:59] op_sel_hi:[1,0]
	v_cvt_pk_bf16_f32 v122, v126, v127
	v_cvt_pk_bf16_f32 v123, v128, v129
	v_pk_mul_f32 v[120:121], v[120:121], s[58:59] op_sel_hi:[1,0]
	v_cvt_pk_bf16_f32 v124, v124, v125
	v_cvt_pk_bf16_f32 v125, v140, v141
	global_store_dwordx4 v[130:131], v[122:125], off sc1
	v_pk_mul_f32 v[118:119], v[118:119], s[58:59] op_sel_hi:[1,0]
	s_mov_b64 s[14:15], 0x8000
	v_pk_mul_f32 v[122:123], v[112:113], s[58:59] op_sel_hi:[1,0]
	v_pk_mul_f32 v[112:113], v[110:111], s[58:59] op_sel_hi:[1,0]
	v_cvt_pk_bf16_f32 v110, v118, v119
	v_cvt_pk_bf16_f32 v111, v120, v121
	v_pk_mul_f32 v[114:115], v[114:115], s[58:59] op_sel_hi:[1,0]
	v_cvt_pk_bf16_f32 v112, v112, v113
	v_cvt_pk_bf16_f32 v113, v122, v123
	global_store_dwordx4 v[130:131], v[110:113], off offset:256 sc1
	v_pk_mul_f32 v[104:105], v[104:105], s[58:59] op_sel_hi:[1,0]
	v_pk_mul_f32 v[102:103], v[102:103], s[58:59] op_sel_hi:[1,0]
	v_lshl_add_u64 v[110:111], v[130:131], 0, s[14:15]
	v_pk_mul_f32 v[112:113], v[116:117], s[58:59] op_sel_hi:[1,0]
	s_mov_b32 s14, 0x8000
	v_pk_mul_f32 v[116:117], v[108:109], s[58:59] op_sel_hi:[1,0]
	v_pk_mul_f32 v[108:109], v[106:107], s[58:59] op_sel_hi:[1,0]
	v_cvt_pk_bf16_f32 v106, v114, v115
	v_cvt_pk_bf16_f32 v107, v112, v113
	v_add_co_u32_e32 v112, vcc, s14, v130
	v_cvt_pk_bf16_f32 v108, v108, v109
	v_cvt_pk_bf16_f32 v109, v116, v117
	s_mov_b64 s[14:15], 0x10000
	s_nop 0
	v_addc_co_u32_e32 v113, vcc, 0, v131, vcc
	global_store_dwordx4 v[112:113], v[106:109], off sc1
	v_pk_mul_f32 v[98:99], v[98:99], s[58:59] op_sel_hi:[1,0]
	v_pk_mul_f32 v[88:89], v[88:89], s[58:59] op_sel_hi:[1,0]
	v_pk_mul_f32 v[106:107], v[96:97], s[58:59] op_sel_hi:[1,0]
	v_pk_mul_f32 v[96:97], v[94:95], s[58:59] op_sel_hi:[1,0]
	v_cvt_pk_bf16_f32 v94, v102, v103
	v_cvt_pk_bf16_f32 v95, v104, v105
	v_pk_mul_f32 v[86:87], v[86:87], s[58:59] op_sel_hi:[1,0]
	v_cvt_pk_bf16_f32 v96, v96, v97
	v_cvt_pk_bf16_f32 v97, v106, v107
	global_store_dwordx4 v[110:111], v[94:97], off offset:256 sc1
	v_pk_mul_f32 v[82:83], v[82:83], s[58:59] op_sel_hi:[1,0]
	v_pk_mul_f32 v[72:73], v[72:73], s[58:59] op_sel_hi:[1,0]
	v_lshl_add_u64 v[94:95], v[130:131], 0, s[14:15]
	v_pk_mul_f32 v[96:97], v[100:101], s[58:59] op_sel_hi:[1,0]
	s_mov_b32 s14, 0x10000
	v_pk_mul_f32 v[100:101], v[92:93], s[58:59] op_sel_hi:[1,0]
	v_pk_mul_f32 v[92:93], v[90:91], s[58:59] op_sel_hi:[1,0]
	v_cvt_pk_bf16_f32 v90, v98, v99
	v_cvt_pk_bf16_f32 v91, v96, v97
	v_add_co_u32_e32 v96, vcc, s14, v130
	v_cvt_pk_bf16_f32 v92, v92, v93
	v_cvt_pk_bf16_f32 v93, v100, v101
	s_mov_b64 s[14:15], 0x18000
	s_nop 0
	v_addc_co_u32_e32 v97, vcc, 0, v131, vcc
	global_store_dwordx4 v[96:97], v[90:93], off sc1
	v_pk_mul_f32 v[70:71], v[70:71], s[58:59] op_sel_hi:[1,0]
	v_pk_mul_f32 v[60:61], v[60:61], s[58:59] op_sel_hi:[1,0]
	v_pk_mul_f32 v[90:91], v[80:81], s[58:59] op_sel_hi:[1,0]
	v_pk_mul_f32 v[80:81], v[78:79], s[58:59] op_sel_hi:[1,0]
	v_cvt_pk_bf16_f32 v78, v86, v87
	v_cvt_pk_bf16_f32 v79, v88, v89
	v_pk_mul_f32 v[62:63], v[62:63], s[58:59] op_sel_hi:[1,0]
	v_cvt_pk_bf16_f32 v80, v80, v81
	v_cvt_pk_bf16_f32 v81, v90, v91
	global_store_dwordx4 v[94:95], v[78:81], off offset:256 sc1
	v_pk_mul_f32 v[54:55], v[54:55], s[58:59] op_sel_hi:[1,0]
	v_pk_mul_f32 v[52:53], v[52:53], s[58:59] op_sel_hi:[1,0]
	v_lshl_add_u64 v[78:79], v[130:131], 0, s[14:15]
	v_pk_mul_f32 v[80:81], v[84:85], s[58:59] op_sel_hi:[1,0]
	s_mov_b32 s14, 0x18000
	v_pk_mul_f32 v[84:85], v[76:77], s[58:59] op_sel_hi:[1,0]
	v_pk_mul_f32 v[76:77], v[74:75], s[58:59] op_sel_hi:[1,0]
	v_cvt_pk_bf16_f32 v74, v82, v83
	v_cvt_pk_bf16_f32 v75, v80, v81
	v_add_co_u32_e32 v80, vcc, s14, v130
	v_cvt_pk_bf16_f32 v76, v76, v77
	v_cvt_pk_bf16_f32 v77, v84, v85
	s_mov_b32 s14, 0x40000
	s_nop 0
	v_addc_co_u32_e32 v81, vcc, 0, v131, vcc
	global_store_dwordx4 v[80:81], v[74:77], off sc1
	v_pk_mul_f32 v[48:49], v[48:49], s[58:59] op_sel_hi:[1,0]
	v_pk_mul_f32 v[38:39], v[38:39], s[58:59] op_sel_hi:[1,0]
	v_pk_mul_f32 v[74:75], v[68:69], s[58:59] op_sel_hi:[1,0]
	v_pk_mul_f32 v[68:69], v[66:67], s[58:59] op_sel_hi:[1,0]
	v_cvt_pk_bf16_f32 v66, v70, v71
	v_cvt_pk_bf16_f32 v67, v72, v73
	v_pk_mul_f32 v[36:37], v[36:37], s[58:59] op_sel_hi:[1,0]
	v_cvt_pk_bf16_f32 v68, v68, v69
	v_cvt_pk_bf16_f32 v69, v74, v75
	global_store_dwordx4 v[78:79], v[66:69], off offset:256 sc1
	v_pk_mul_f32 v[32:33], v[32:33], s[58:59] op_sel_hi:[1,0]
	v_pk_mul_f32 v[22:23], v[22:23], s[58:59] op_sel_hi:[1,0]
	v_pk_mul_f32 v[68:69], v[58:59], s[58:59] op_sel_hi:[1,0]
	v_pk_mul_f32 v[58:59], v[56:57], s[58:59] op_sel_hi:[1,0]
	v_cvt_pk_bf16_f32 v56, v60, v61
	v_add_co_u32_e32 v60, vcc, s14, v130
	v_cvt_pk_bf16_f32 v57, v62, v63
	v_cvt_pk_bf16_f32 v58, v58, v59
	v_cvt_pk_bf16_f32 v59, v68, v69
	v_lshl_add_u64 v[66:67], v[130:131], 0, s[90:91]
	s_nop 0
	v_addc_co_u32_e32 v61, vcc, 0, v131, vcc
	global_store_dwordx4 v[60:61], v[56:59], off sc1
	s_mov_b64 s[14:15], 0x48000
	v_pk_mul_f32 v[20:21], v[20:21], s[58:59] op_sel_hi:[1,0]
	v_pk_mul_f32 v[56:57], v[46:47], s[58:59] op_sel_hi:[1,0]
	v_pk_mul_f32 v[46:47], v[44:45], s[58:59] op_sel_hi:[1,0]
	v_cvt_pk_bf16_f32 v44, v52, v53
	v_cvt_pk_bf16_f32 v45, v54, v55
	v_pk_mul_f32 v[16:17], v[16:17], s[58:59] op_sel_hi:[1,0]
	v_cvt_pk_bf16_f32 v46, v46, v47
	v_cvt_pk_bf16_f32 v47, v56, v57
	global_store_dwordx4 v[66:67], v[44:47], off offset:256 sc1
	s_cmp_eq_u32 s34, 3
	v_pk_mul_f32 v[6:7], v[6:7], s[58:59] op_sel_hi:[1,0]
	v_lshl_add_u64 v[44:45], v[130:131], 0, s[14:15]
	v_pk_mul_f32 v[46:47], v[50:51], s[58:59] op_sel_hi:[1,0]
	s_mov_b32 s14, 0x48000
	v_pk_mul_f32 v[50:51], v[42:43], s[58:59] op_sel_hi:[1,0]
	v_pk_mul_f32 v[42:43], v[40:41], s[58:59] op_sel_hi:[1,0]
	v_cvt_pk_bf16_f32 v40, v48, v49
	v_cvt_pk_bf16_f32 v41, v46, v47
	v_add_co_u32_e32 v46, vcc, s14, v130
	v_cvt_pk_bf16_f32 v42, v42, v43
	v_cvt_pk_bf16_f32 v43, v50, v51
	s_mov_b64 s[14:15], 0x50000
	s_nop 0
	v_addc_co_u32_e32 v47, vcc, 0, v131, vcc
	global_store_dwordx4 v[46:47], v[40:43], off sc1
	v_pk_mul_f32 v[4:5], v[4:5], s[58:59] op_sel_hi:[1,0]
	s_nop 0
	v_pk_mul_f32 v[40:41], v[30:31], s[58:59] op_sel_hi:[1,0]
	v_pk_mul_f32 v[30:31], v[28:29], s[58:59] op_sel_hi:[1,0]
	v_cvt_pk_bf16_f32 v28, v36, v37
	v_cvt_pk_bf16_f32 v29, v38, v39
	s_nop 0
	v_cvt_pk_bf16_f32 v30, v30, v31
	v_cvt_pk_bf16_f32 v31, v40, v41
	global_store_dwordx4 v[44:45], v[28:31], off offset:256 sc1
	s_nop 1
	v_lshl_add_u64 v[28:29], v[130:131], 0, s[14:15]
	v_pk_mul_f32 v[30:31], v[34:35], s[58:59] op_sel_hi:[1,0]
	s_mov_b32 s14, 0x50000
	v_pk_mul_f32 v[34:35], v[26:27], s[58:59] op_sel_hi:[1,0]
	v_pk_mul_f32 v[26:27], v[24:25], s[58:59] op_sel_hi:[1,0]
	v_cvt_pk_bf16_f32 v24, v32, v33
	v_cvt_pk_bf16_f32 v25, v30, v31
	v_add_co_u32_e32 v30, vcc, s14, v130
	v_cvt_pk_bf16_f32 v26, v26, v27
	v_cvt_pk_bf16_f32 v27, v34, v35
	s_mov_b64 s[14:15], 0x58000
	s_nop 0
	v_addc_co_u32_e32 v31, vcc, 0, v131, vcc
	global_store_dwordx4 v[30:31], v[24:27], off sc1
	s_nop 1
	v_pk_mul_f32 v[24:25], v[14:15], s[58:59] op_sel_hi:[1,0]
	v_pk_mul_f32 v[14:15], v[12:13], s[58:59] op_sel_hi:[1,0]
	v_cvt_pk_bf16_f32 v12, v20, v21
	v_cvt_pk_bf16_f32 v13, v22, v23
	s_nop 0
	v_cvt_pk_bf16_f32 v14, v14, v15
	v_cvt_pk_bf16_f32 v15, v24, v25
	global_store_dwordx4 v[28:29], v[12:15], off offset:256 sc1
	s_nop 1
	v_lshl_add_u64 v[12:13], v[130:131], 0, s[14:15]
	v_pk_mul_f32 v[14:15], v[18:19], s[58:59] op_sel_hi:[1,0]
	s_mov_b32 s14, 0x58000
	v_pk_mul_f32 v[18:19], v[10:11], s[58:59] op_sel_hi:[1,0]
	v_pk_mul_f32 v[10:11], v[8:9], s[58:59] op_sel_hi:[1,0]
	v_cvt_pk_bf16_f32 v8, v16, v17
	v_cvt_pk_bf16_f32 v9, v14, v15
	v_add_co_u32_e32 v14, vcc, s14, v130
	v_cvt_pk_bf16_f32 v10, v10, v11
	v_cvt_pk_bf16_f32 v11, v18, v19
	s_mov_b64 s[14:15], -1
	s_nop 0
	v_addc_co_u32_e32 v15, vcc, 0, v131, vcc
	global_store_dwordx4 v[14:15], v[8:11], off sc1
	s_nop 1
	v_pk_mul_f32 v[8:9], v[2:3], s[58:59] op_sel_hi:[1,0]
	v_pk_mul_f32 v[2:3], v[0:1], s[58:59] op_sel_hi:[1,0]
	v_cvt_pk_bf16_f32 v0, v4, v5
	v_cvt_pk_bf16_f32 v1, v6, v7
	s_nop 0
	v_cvt_pk_bf16_f32 v2, v2, v3
	v_cvt_pk_bf16_f32 v3, v8, v9
	global_store_dwordx4 v[12:13], v[0:3], off offset:256 sc1
	s_cbranch_scc1 .LBB0_670
	s_andn2_b64 vcc, exec, s[8:9]
	s_cbranch_vccnz .LBB0_669
	s_barrier
	s_branch .LBB0_669

.LBB0_689:
	v_mov_b32_e32 v64, v136
	v_mov_b32_e32 v130, v137
	s_mov_b32 s14, s2
	s_lshl_b32 s14, s14, 8
	s_lshl_b32 s15, s30, 8
	s_add_i32 s14, s14, s25
	s_or_b32 s15, s15, s26
	v_add_u32_e32 v140, s14, v64
	v_lshl_add_u32 v130, v130, 3, s15
	v_ashrrev_i32_e32 v141, 31, v140
	v_readlane_b32 s14, v254, 24
	v_lshlrev_b64 v[140:141], 11, v[140:141]
	v_readlane_b32 s15, v254, 25
	v_ashrrev_i32_e32 v131, 31, v130
	v_cvt_pk_bf16_f32 v126, v126, v127
	v_cvt_pk_bf16_f32 v127, v128, v129
	v_cvt_pk_bf16_f32 v128, v122, v123
	v_cvt_pk_bf16_f32 v129, v124, v125
	s_nop 0
	v_lshl_add_u64 v[140:141], s[14:15], 0, v[140:141]
	v_lshl_add_u64 v[130:131], v[130:131], 1, v[140:141]
	global_store_dwordx4 v[130:131], v[126:129], off sc1
	v_cvt_pk_bf16_f32 v114, v114, v115
	v_cvt_pk_bf16_f32 v115, v116, v117
	s_mov_b64 s[14:15], 0x8000
	v_cvt_pk_bf16_f32 v116, v106, v107
	v_cvt_pk_bf16_f32 v117, v108, v109
	global_store_dwordx4 v[130:131], v[114:117], off offset:256 sc1
	v_cvt_pk_bf16_f32 v106, v118, v119
	v_cvt_pk_bf16_f32 v107, v120, v121
	v_cvt_pk_bf16_f32 v108, v110, v111
	v_cvt_pk_bf16_f32 v109, v112, v113
	s_cmp_eq_u32 s30, 3
	s_nop 0
	v_lshl_add_u64 v[114:115], v[130:131], 0, s[14:15]
	s_mov_b32 s14, 0x8000
	v_add_co_u32_e32 v110, vcc, s14, v130
	s_mov_b64 s[14:15], 0x10000
	s_nop 0
	v_addc_co_u32_e32 v111, vcc, 0, v131, vcc
	global_store_dwordx4 v[110:111], v[106:109], off sc1
	v_cvt_pk_bf16_f32 v98, v98, v99
	v_cvt_pk_bf16_f32 v99, v100, v101
	v_cvt_pk_bf16_f32 v100, v90, v91
	v_cvt_pk_bf16_f32 v101, v92, v93
	global_store_dwordx4 v[114:115], v[98:101], off offset:256 sc1
	v_cvt_pk_bf16_f32 v90, v102, v103
	v_cvt_pk_bf16_f32 v91, v104, v105
	v_cvt_pk_bf16_f32 v92, v94, v95
	v_cvt_pk_bf16_f32 v93, v96, v97
	s_nop 1
	v_lshl_add_u64 v[98:99], v[130:131], 0, s[14:15]
	s_mov_b32 s14, 0x10000
	v_add_co_u32_e32 v94, vcc, s14, v130
	s_mov_b64 s[14:15], 0x18000
	s_nop 0
	v_addc_co_u32_e32 v95, vcc, 0, v131, vcc
	global_store_dwordx4 v[94:95], v[90:93], off sc1
	v_cvt_pk_bf16_f32 v82, v82, v83
	v_cvt_pk_bf16_f32 v83, v84, v85
	v_cvt_pk_bf16_f32 v84, v74, v75
	v_cvt_pk_bf16_f32 v85, v76, v77
	global_store_dwordx4 v[98:99], v[82:85], off offset:256 sc1
	v_cvt_pk_bf16_f32 v74, v86, v87
	v_cvt_pk_bf16_f32 v75, v88, v89
	v_cvt_pk_bf16_f32 v76, v78, v79
	v_cvt_pk_bf16_f32 v77, v80, v81
	s_nop 1
	v_lshl_add_u64 v[82:83], v[130:131], 0, s[14:15]
	s_mov_b32 s14, 0x18000
	v_add_co_u32_e32 v78, vcc, s14, v130
	s_mov_b32 s14, 0x40000
	s_nop 0
	v_addc_co_u32_e32 v79, vcc, 0, v131, vcc
	global_store_dwordx4 v[78:79], v[74:77], off sc1
	v_cvt_pk_bf16_f32 v70, v70, v71
	v_cvt_pk_bf16_f32 v71, v72, v73
	v_cvt_pk_bf16_f32 v72, v66, v67
	v_cvt_pk_bf16_f32 v73, v68, v69
	global_store_dwordx4 v[82:83], v[70:73], off offset:256 sc1
	v_cvt_pk_bf16_f32 v60, v60, v61
	v_cvt_pk_bf16_f32 v61, v62, v63
	v_cvt_pk_bf16_f32 v62, v56, v57
	v_add_co_u32_e32 v56, vcc, s14, v130
	v_lshl_add_u64 v[66:67], v[130:131], 0, s[90:91]
	s_nop 0
	v_addc_co_u32_e32 v57, vcc, 0, v131, vcc
	v_cvt_pk_bf16_f32 v63, v58, v59
	global_store_dwordx4 v[56:57], v[60:63], off sc1
	v_cvt_pk_bf16_f32 v48, v48, v49
	v_cvt_pk_bf16_f32 v49, v50, v51
	s_mov_b64 s[14:15], 0x48000
	v_cvt_pk_bf16_f32 v50, v40, v41
	v_cvt_pk_bf16_f32 v51, v42, v43
	global_store_dwordx4 v[66:67], v[48:51], off offset:256 sc1
	v_cvt_pk_bf16_f32 v40, v52, v53
	v_cvt_pk_bf16_f32 v41, v54, v55
	v_cvt_pk_bf16_f32 v42, v44, v45
	v_cvt_pk_bf16_f32 v43, v46, v47
	s_nop 1
	v_lshl_add_u64 v[48:49], v[130:131], 0, s[14:15]
	s_mov_b32 s14, 0x48000
	v_add_co_u32_e32 v44, vcc, s14, v130
	s_mov_b64 s[14:15], 0x50000
	s_nop 0
	v_addc_co_u32_e32 v45, vcc, 0, v131, vcc
	global_store_dwordx4 v[44:45], v[40:43], off sc1
	v_cvt_pk_bf16_f32 v32, v32, v33
	v_cvt_pk_bf16_f32 v33, v34, v35
	v_cvt_pk_bf16_f32 v34, v24, v25
	v_cvt_pk_bf16_f32 v35, v26, v27
	global_store_dwordx4 v[48:49], v[32:35], off offset:256 sc1
	v_cvt_pk_bf16_f32 v24, v36, v37
	v_cvt_pk_bf16_f32 v25, v38, v39
	v_cvt_pk_bf16_f32 v26, v28, v29
	v_cvt_pk_bf16_f32 v27, v30, v31
	s_nop 1
	v_lshl_add_u64 v[32:33], v[130:131], 0, s[14:15]
	s_mov_b32 s14, 0x50000
	v_add_co_u32_e32 v28, vcc, s14, v130
	s_mov_b64 s[14:15], 0x58000
	s_nop 0
	v_addc_co_u32_e32 v29, vcc, 0, v131, vcc
	global_store_dwordx4 v[28:29], v[24:27], off sc1
	v_cvt_pk_bf16_f32 v16, v16, v17
	v_cvt_pk_bf16_f32 v17, v18, v19
	v_cvt_pk_bf16_f32 v18, v8, v9
	v_cvt_pk_bf16_f32 v19, v10, v11
	global_store_dwordx4 v[32:33], v[16:19], off offset:256 sc1
	v_cvt_pk_bf16_f32 v8, v20, v21
	v_cvt_pk_bf16_f32 v9, v22, v23
	v_cvt_pk_bf16_f32 v10, v12, v13
	v_cvt_pk_bf16_f32 v11, v14, v15
	s_nop 1
	v_lshl_add_u64 v[16:17], v[130:131], 0, s[14:15]
	s_mov_b32 s14, 0x58000
	v_add_co_u32_e32 v12, vcc, s14, v130
	s_mov_b64 s[14:15], -1
	s_nop 0
	v_addc_co_u32_e32 v13, vcc, 0, v131, vcc
	global_store_dwordx4 v[12:13], v[8:11], off sc1
	v_cvt_pk_bf16_f32 v4, v4, v5
	v_cvt_pk_bf16_f32 v5, v6, v7
	v_cvt_pk_bf16_f32 v6, v0, v1
	v_cvt_pk_bf16_f32 v7, v2, v3
	global_store_dwordx4 v[16:17], v[4:7], off offset:256 sc1
	s_cbranch_scc1 .LBB0_684
	s_andn2_b64 vcc, exec, s[8:9]
	s_cbranch_vccnz .LBB0_683
	s_barrier
	s_branch .LBB0_683

.LBB0_909:
	s_lshl_b32 s21, s71, 8
	v_mov_b32_e32 v64, v134
	v_mov_b32_e32 v139, v135
	s_and_b32 s21, s21, 0x300
	s_or_b32 s21, s21, s51
	v_mul_f32_e32 v122, 0.5, v122
	v_lshl_add_u32 v138, v64, 4, s21
	v_mul_f32_e32 v64, 0.5, v126
	v_med3_f32 v126, v122, s55, v228
	v_mul_f32_e32 v122, 0.5, v127
	v_med3_f32 v127, v122, s55, v228
	v_mul_f32_e32 v122, 0.5, v123
	v_med3_f32 v141, v122, s55, v228
	v_mul_f32_e32 v122, 0.5, v128
	v_med3_f32 v128, v122, s55, v228
	v_mul_f32_e32 v122, 0.5, v124
	v_mov_b32_e32 v123, v65
	v_med3_f32 v124, v122, s55, v228
	v_mul_f32_e32 v122, 0.5, v129
	v_cvt_pk_fp8_f32 v123, v126, v141
	v_med3_f32 v64, v64, s55, v228
	v_med3_f32 v129, v122, s55, v228
	v_mov_b32_e32 v122, v65
	v_cvt_pk_fp8_f32 v122, v64, v127
	v_mul_f32_e32 v64, 0.5, v125
	v_mul_f32_e32 v114, 0.5, v114
	v_mul_f32_e32 v115, 0.5, v115
	v_med3_f32 v64, v64, s55, v228
	v_med3_f32 v114, v114, s55, v228
	v_med3_f32 v115, v115, s55, v228
	v_mov_b32_e32 v125, v65
	v_cvt_pk_fp8_f32 v123, v124, v64 op_sel:[0,0,1]
	v_mul_f32_e32 v64, 0.5, v118
	v_mul_f32_e32 v118, 0.5, v119
	v_cvt_pk_fp8_f32 v125, v114, v115
	v_med3_f32 v64, v64, s55, v228
	v_med3_f32 v118, v118, s55, v228
	v_mov_b32_e32 v124, v65
	v_mul_f32_e32 v116, 0.5, v116
	v_cvt_pk_fp8_f32 v124, v64, v118
	v_mul_f32_e32 v64, 0.5, v117
	v_med3_f32 v116, v116, s55, v228
	v_med3_f32 v64, v64, s55, v228
	v_mul_f32_e32 v106, 0.5, v106
	v_cvt_pk_fp8_f32 v125, v116, v64 op_sel:[0,0,1]
	v_mul_f32_e32 v64, 0.5, v110
	v_med3_f32 v110, v106, s55, v228
	v_mul_f32_e32 v106, 0.5, v111
	v_med3_f32 v111, v106, s55, v228
	v_mul_f32_e32 v106, 0.5, v107
	v_med3_f32 v116, v106, s55, v228
	v_mul_f32_e32 v106, 0.5, v112
	v_med3_f32 v112, v106, s55, v228
	v_mul_f32_e32 v106, 0.5, v108
	v_mov_b32_e32 v107, v65
	v_med3_f32 v108, v106, s55, v228
	v_mul_f32_e32 v106, 0.5, v113
	v_cvt_pk_fp8_f32 v107, v110, v116
	v_med3_f32 v64, v64, s55, v228
	v_med3_f32 v113, v106, s55, v228
	v_mov_b32_e32 v106, v65
	v_cvt_pk_fp8_f32 v106, v64, v111
	v_mul_f32_e32 v64, 0.5, v109
	v_med3_f32 v64, v64, s55, v228
	v_cvt_pk_fp8_f32 v107, v108, v64 op_sel:[0,0,1]
	v_mul_f32_e32 v64, 0.5, v102
	v_mul_f32_e32 v98, 0.5, v98
	v_mul_f32_e32 v102, 0.5, v103
	v_mul_f32_e32 v99, 0.5, v99
	s_lshl_b32 s20, s29, 8
	v_med3_f32 v64, v64, s55, v228
	v_med3_f32 v98, v98, s55, v228
	v_med3_f32 v102, v102, s55, v228
	v_med3_f32 v99, v99, s55, v228
	v_mov_b32_e32 v108, v65
	v_mov_b32_e32 v109, v65
	s_add_i32 s20, s20, s37
	v_cvt_pk_fp8_f32 v108, v64, v102
	v_cvt_pk_fp8_f32 v109, v98, v99
	v_add_u32_e32 v140, s20, v139
	v_ashrrev_i32_e32 v141, 31, v140
	v_readlane_b32 s20, v254, 42
	v_mul_f32_e32 v103, 0.5, v104
	v_mul_f32_e32 v100, 0.5, v100
	v_mul_f32_e32 v104, 0.5, v105
	v_mul_f32_e32 v64, 0.5, v101
	v_lshlrev_b64 v[114:115], 10, v[140:141]
	v_readlane_b32 s21, v254, 43
	v_med3_f32 v103, v103, s55, v228
	v_med3_f32 v100, v100, s55, v228
	v_med3_f32 v104, v104, s55, v228
	v_med3_f32 v64, v64, s55, v228
	v_ashrrev_i32_e32 v139, 31, v138
	v_lshl_add_u64 v[114:115], s[20:21], 0, v[114:115]
	v_cvt_pk_fp8_f32 v106, v112, v113 op_sel:[0,0,1]
	v_cvt_pk_fp8_f32 v108, v103, v104 op_sel:[0,0,1]
	v_cvt_pk_fp8_f32 v109, v100, v64 op_sel:[0,0,1]
	v_lshl_add_u64 v[114:115], v[114:115], 0, v[138:139]
	s_movk_i32 s20, 0x4000
	v_mul_f32_e32 v90, 0.5, v90
	v_add_co_u32_e32 v98, vcc, s20, v114
	v_mul_f32_e32 v64, 0.5, v94
	v_med3_f32 v94, v90, s55, v228
	v_mul_f32_e32 v90, 0.5, v95
	v_addc_co_u32_e32 v99, vcc, 0, v115, vcc
	v_med3_f32 v95, v90, s55, v228
	v_mul_f32_e32 v90, 0.5, v91
	global_store_dwordx4 v[98:99], v[106:109], off nt sc1
	v_med3_f32 v98, v90, s55, v228
	v_mul_f32_e32 v90, 0.5, v96
	v_med3_f32 v96, v90, s55, v228
	v_mul_f32_e32 v90, 0.5, v92
	v_mov_b32_e32 v91, v65
	v_med3_f32 v92, v90, s55, v228
	v_mul_f32_e32 v90, 0.5, v97
	v_cvt_pk_fp8_f32 v91, v94, v98
	v_med3_f32 v64, v64, s55, v228
	v_med3_f32 v97, v90, s55, v228
	v_mov_b32_e32 v90, v65
	v_cvt_pk_fp8_f32 v90, v64, v95
	v_mul_f32_e32 v64, 0.5, v93
	v_med3_f32 v64, v64, s55, v228
	v_cvt_pk_fp8_f32 v91, v92, v64 op_sel:[0,0,1]
	v_mul_f32_e32 v64, 0.5, v86
	v_mul_f32_e32 v82, 0.5, v82
	v_mul_f32_e32 v86, 0.5, v87
	v_mul_f32_e32 v83, 0.5, v83
	v_med3_f32 v64, v64, s55, v228
	v_med3_f32 v82, v82, s55, v228
	v_med3_f32 v86, v86, s55, v228
	v_med3_f32 v83, v83, s55, v228
	v_mov_b32_e32 v92, v65
	v_mov_b32_e32 v93, v65
	v_cvt_pk_fp8_f32 v92, v64, v86
	v_cvt_pk_fp8_f32 v93, v82, v83
	v_mul_f32_e32 v87, 0.5, v88
	v_mul_f32_e32 v84, 0.5, v84
	v_mul_f32_e32 v88, 0.5, v89
	v_mul_f32_e32 v64, 0.5, v85
	v_med3_f32 v87, v87, s55, v228
	v_med3_f32 v84, v84, s55, v228
	v_med3_f32 v88, v88, s55, v228
	v_med3_f32 v64, v64, s55, v228
	v_cvt_pk_fp8_f32 v90, v96, v97 op_sel:[0,0,1]
	v_cvt_pk_fp8_f32 v92, v87, v88 op_sel:[0,0,1]
	v_cvt_pk_fp8_f32 v93, v84, v64 op_sel:[0,0,1]
	s_mov_b32 s20, 0x8000
	v_mul_f32_e32 v74, 0.5, v74
	v_add_co_u32_e32 v82, vcc, s20, v114
	v_mul_f32_e32 v64, 0.5, v78
	v_med3_f32 v78, v74, s55, v228
	v_mul_f32_e32 v74, 0.5, v79
	v_addc_co_u32_e32 v83, vcc, 0, v115, vcc
	v_med3_f32 v79, v74, s55, v228
	v_mul_f32_e32 v74, 0.5, v75
	global_store_dwordx4 v[82:83], v[90:93], off nt sc1
	v_med3_f32 v82, v74, s55, v228
	v_mul_f32_e32 v74, 0.5, v80
	v_med3_f32 v80, v74, s55, v228
	v_mul_f32_e32 v74, 0.5, v76
	v_mov_b32_e32 v75, v65
	v_med3_f32 v76, v74, s55, v228
	v_mul_f32_e32 v74, 0.5, v81
	v_cvt_pk_fp8_f32 v75, v78, v82
	v_med3_f32 v64, v64, s55, v228
	v_med3_f32 v81, v74, s55, v228
	v_mov_b32_e32 v74, v65
	v_cvt_pk_fp8_f32 v74, v64, v79
	v_mul_f32_e32 v64, 0.5, v77
	v_med3_f32 v64, v64, s55, v228
	v_cvt_pk_fp8_f32 v75, v76, v64 op_sel:[0,0,1]
	v_mul_f32_e32 v64, 0.5, v70
	v_mul_f32_e32 v66, 0.5, v66
	v_mul_f32_e32 v70, 0.5, v71
	v_mul_f32_e32 v67, 0.5, v67
	v_med3_f32 v64, v64, s55, v228
	v_med3_f32 v66, v66, s55, v228
	v_med3_f32 v70, v70, s55, v228
	v_med3_f32 v67, v67, s55, v228
	v_mov_b32_e32 v76, v65
	v_mov_b32_e32 v77, v65
	v_cvt_pk_fp8_f32 v76, v64, v70
	v_cvt_pk_fp8_f32 v77, v66, v67
	v_mul_f32_e32 v71, 0.5, v72
	v_mul_f32_e32 v68, 0.5, v68
	v_mul_f32_e32 v72, 0.5, v73
	v_mul_f32_e32 v64, 0.5, v69
	v_med3_f32 v71, v71, s55, v228
	v_med3_f32 v68, v68, s55, v228
	v_med3_f32 v72, v72, s55, v228
	v_med3_f32 v64, v64, s55, v228
	v_cvt_pk_fp8_f32 v74, v80, v81 op_sel:[0,0,1]
	v_cvt_pk_fp8_f32 v76, v71, v72 op_sel:[0,0,1]
	v_cvt_pk_fp8_f32 v77, v68, v64 op_sel:[0,0,1]
	s_mov_b32 s20, 0xc000
	v_mul_f32_e32 v56, 0.5, v56
	v_add_co_u32_e32 v66, vcc, s20, v114
	v_med3_f32 v64, v56, s55, v228
	v_mul_f32_e32 v56, 0.5, v61
	v_addc_co_u32_e32 v67, vcc, 0, v115, vcc
	v_med3_f32 v61, v56, s55, v228
	v_mul_f32_e32 v56, 0.5, v57
	global_store_dwordx4 v[66:67], v[74:77], off nt sc1
	v_med3_f32 v66, v56, s55, v228
	v_mov_b32_e32 v57, v65
	v_cvt_pk_fp8_f32 v57, v64, v66
	v_mul_f32_e32 v56, 0.5, v62
	v_med3_f32 v62, v56, s55, v228
	v_mul_f32_e32 v56, 0.5, v58
	v_mul_f32_e32 v59, 0.5, v59
	v_mul_f32_e32 v60, 0.5, v60
	v_med3_f32 v58, v56, s55, v228
	v_mul_f32_e32 v56, 0.5, v63
	v_med3_f32 v59, v59, s55, v228
	v_mul_f32_e32 v52, 0.5, v52
	v_mul_f32_e32 v48, 0.5, v48
	v_mul_f32_e32 v53, 0.5, v53
	v_mul_f32_e32 v49, 0.5, v49
	v_med3_f32 v60, v60, s55, v228
	v_med3_f32 v63, v56, s55, v228
	v_mov_b32_e32 v56, v65
	v_cvt_pk_fp8_f32 v57, v58, v59 op_sel:[0,0,1]
	v_med3_f32 v52, v52, s55, v228
	v_med3_f32 v48, v48, s55, v228
	v_med3_f32 v53, v53, s55, v228
	v_med3_f32 v49, v49, s55, v228
	v_mov_b32_e32 v58, v65
	v_mov_b32_e32 v59, v65
	v_cvt_pk_fp8_f32 v56, v60, v61
	v_cvt_pk_fp8_f32 v58, v52, v53
	v_cvt_pk_fp8_f32 v59, v48, v49
	v_mul_f32_e32 v54, 0.5, v54
	v_mul_f32_e32 v50, 0.5, v50
	v_mul_f32_e32 v55, 0.5, v55
	v_mul_f32_e32 v48, 0.5, v51
	v_med3_f32 v54, v54, s55, v228
	v_med3_f32 v50, v50, s55, v228
	v_med3_f32 v55, v55, s55, v228
	v_med3_f32 v48, v48, s55, v228
	v_cvt_pk_fp8_f32 v56, v62, v63 op_sel:[0,0,1]
	v_cvt_pk_fp8_f32 v58, v54, v55 op_sel:[0,0,1]
	v_cvt_pk_fp8_f32 v59, v50, v48 op_sel:[0,0,1]
	s_mov_b32 s20, 0x20000
	v_add_co_u32_e32 v48, vcc, s20, v114
	v_mul_f32_e32 v40, 0.5, v40
	s_nop 0
	v_addc_co_u32_e32 v49, vcc, 0, v115, vcc
	global_store_dwordx4 v[48:49], v[56:59], off nt sc1
	v_med3_f32 v48, v40, s55, v228
	v_mul_f32_e32 v40, 0.5, v45
	v_med3_f32 v45, v40, s55, v228
	v_mul_f32_e32 v40, 0.5, v41
	v_med3_f32 v49, v40, s55, v228
	v_mov_b32_e32 v41, v65
	v_cvt_pk_fp8_f32 v41, v48, v49
	v_mul_f32_e32 v40, 0.5, v46
	v_med3_f32 v46, v40, s55, v228
	v_mul_f32_e32 v40, 0.5, v42
	v_mul_f32_e32 v43, 0.5, v43
	v_mul_f32_e32 v44, 0.5, v44
	v_med3_f32 v42, v40, s55, v228
	v_mul_f32_e32 v40, 0.5, v47
	v_med3_f32 v43, v43, s55, v228
	v_mul_f32_e32 v36, 0.5, v36
	v_mul_f32_e32 v32, 0.5, v32
	v_mul_f32_e32 v37, 0.5, v37
	v_mul_f32_e32 v33, 0.5, v33
	v_med3_f32 v44, v44, s55, v228
	v_med3_f32 v47, v40, s55, v228
	v_mov_b32_e32 v40, v65
	v_cvt_pk_fp8_f32 v41, v42, v43 op_sel:[0,0,1]
	v_med3_f32 v36, v36, s55, v228
	v_med3_f32 v32, v32, s55, v228
	v_med3_f32 v37, v37, s55, v228
	v_med3_f32 v33, v33, s55, v228
	v_mov_b32_e32 v42, v65
	v_mov_b32_e32 v43, v65
	v_cvt_pk_fp8_f32 v40, v44, v45
	v_cvt_pk_fp8_f32 v42, v36, v37
	v_cvt_pk_fp8_f32 v43, v32, v33
	v_mul_f32_e32 v38, 0.5, v38
	v_mul_f32_e32 v34, 0.5, v34
	v_mul_f32_e32 v39, 0.5, v39
	v_mul_f32_e32 v32, 0.5, v35
	v_med3_f32 v38, v38, s55, v228
	v_med3_f32 v34, v34, s55, v228
	v_med3_f32 v39, v39, s55, v228
	v_med3_f32 v32, v32, s55, v228
	v_cvt_pk_fp8_f32 v40, v46, v47 op_sel:[0,0,1]
	v_cvt_pk_fp8_f32 v42, v38, v39 op_sel:[0,0,1]
	v_cvt_pk_fp8_f32 v43, v34, v32 op_sel:[0,0,1]
	s_mov_b32 s20, 0x24000
	v_add_co_u32_e32 v32, vcc, s20, v114
	v_mul_f32_e32 v24, 0.5, v24
	s_nop 0
	v_addc_co_u32_e32 v33, vcc, 0, v115, vcc
	global_store_dwordx4 v[32:33], v[40:43], off nt sc1
	v_med3_f32 v32, v24, s55, v228
	v_mul_f32_e32 v24, 0.5, v29
	v_med3_f32 v29, v24, s55, v228
	v_mul_f32_e32 v24, 0.5, v25
	v_med3_f32 v33, v24, s55, v228
	v_mov_b32_e32 v25, v65
	v_cvt_pk_fp8_f32 v25, v32, v33
	v_mul_f32_e32 v24, 0.5, v30
	v_med3_f32 v30, v24, s55, v228
	v_mul_f32_e32 v24, 0.5, v26
	v_mul_f32_e32 v27, 0.5, v27
	v_mul_f32_e32 v28, 0.5, v28
	v_med3_f32 v26, v24, s55, v228
	v_mul_f32_e32 v24, 0.5, v31
	v_med3_f32 v27, v27, s55, v228
	v_mul_f32_e32 v20, 0.5, v20
	v_mul_f32_e32 v16, 0.5, v16
	v_mul_f32_e32 v21, 0.5, v21
	v_mul_f32_e32 v17, 0.5, v17
	v_med3_f32 v28, v28, s55, v228
	v_med3_f32 v31, v24, s55, v228
	v_mov_b32_e32 v24, v65
	v_cvt_pk_fp8_f32 v25, v26, v27 op_sel:[0,0,1]
	v_med3_f32 v20, v20, s55, v228
	v_med3_f32 v16, v16, s55, v228
	v_med3_f32 v21, v21, s55, v228
	v_med3_f32 v17, v17, s55, v228
	v_mov_b32_e32 v26, v65
	v_mov_b32_e32 v27, v65
	v_cvt_pk_fp8_f32 v24, v28, v29
	v_cvt_pk_fp8_f32 v26, v20, v21
	v_cvt_pk_fp8_f32 v27, v16, v17
	v_mul_f32_e32 v22, 0.5, v22
	v_mul_f32_e32 v18, 0.5, v18
	v_mul_f32_e32 v23, 0.5, v23
	v_mul_f32_e32 v16, 0.5, v19
	v_med3_f32 v22, v22, s55, v228
	v_med3_f32 v18, v18, s55, v228
	v_med3_f32 v23, v23, s55, v228
	v_med3_f32 v16, v16, s55, v228
	v_cvt_pk_fp8_f32 v24, v30, v31 op_sel:[0,0,1]
	v_cvt_pk_fp8_f32 v26, v22, v23 op_sel:[0,0,1]
	v_cvt_pk_fp8_f32 v27, v18, v16 op_sel:[0,0,1]
	s_mov_b32 s20, 0x28000
	v_add_co_u32_e32 v16, vcc, s20, v114
	v_mul_f32_e32 v8, 0.5, v8
	s_nop 0
	v_addc_co_u32_e32 v17, vcc, 0, v115, vcc
	global_store_dwordx4 v[16:17], v[24:27], off nt sc1
	v_med3_f32 v16, v8, s55, v228
	v_mul_f32_e32 v8, 0.5, v13
	v_med3_f32 v13, v8, s55, v228
	v_mul_f32_e32 v8, 0.5, v9
	v_med3_f32 v17, v8, s55, v228
	v_mov_b32_e32 v9, v65
	v_cvt_pk_fp8_f32 v9, v16, v17
	v_mul_f32_e32 v8, 0.5, v14
	v_med3_f32 v14, v8, s55, v228
	v_mul_f32_e32 v8, 0.5, v10
	v_mul_f32_e32 v11, 0.5, v11
	v_mul_f32_e32 v12, 0.5, v12
	v_med3_f32 v10, v8, s55, v228
	v_mul_f32_e32 v8, 0.5, v15
	v_med3_f32 v11, v11, s55, v228
	v_mul_f32_e32 v4, 0.5, v4
	v_mul_f32_e32 v0, 0.5, v0
	v_mul_f32_e32 v5, 0.5, v5
	v_mul_f32_e32 v1, 0.5, v1
	v_med3_f32 v12, v12, s55, v228
	v_med3_f32 v15, v8, s55, v228
	v_mov_b32_e32 v8, v65
	v_cvt_pk_fp8_f32 v9, v10, v11 op_sel:[0,0,1]
	v_med3_f32 v4, v4, s55, v228
	v_med3_f32 v0, v0, s55, v228
	v_med3_f32 v5, v5, s55, v228
	v_med3_f32 v1, v1, s55, v228
	v_mov_b32_e32 v10, v65
	v_mov_b32_e32 v11, v65
	v_cvt_pk_fp8_f32 v8, v12, v13
	v_cvt_pk_fp8_f32 v10, v4, v5
	v_cvt_pk_fp8_f32 v11, v0, v1
	v_mul_f32_e32 v119, 0.5, v120
	v_mul_f32_e32 v120, 0.5, v121
	v_mul_f32_e32 v6, 0.5, v6
	v_mul_f32_e32 v2, 0.5, v2
	v_mul_f32_e32 v7, 0.5, v7
	v_mul_f32_e32 v0, 0.5, v3
	v_med3_f32 v119, v119, s55, v228
	v_med3_f32 v120, v120, s55, v228
	v_med3_f32 v6, v6, s55, v228
	v_med3_f32 v2, v2, s55, v228
	v_med3_f32 v7, v7, s55, v228
	v_med3_f32 v0, v0, s55, v228
	v_cvt_pk_fp8_f32 v122, v128, v129 op_sel:[0,0,1]
	v_cvt_pk_fp8_f32 v124, v119, v120 op_sel:[0,0,1]
	v_cvt_pk_fp8_f32 v8, v14, v15 op_sel:[0,0,1]
	v_cvt_pk_fp8_f32 v10, v6, v7 op_sel:[0,0,1]
	v_cvt_pk_fp8_f32 v11, v2, v0 op_sel:[0,0,1]
	v_add_co_u32_e32 v0, vcc, 0x2c000, v114
	global_store_dwordx4 v[114:115], v[122:125], off nt sc1
	s_nop 0
	v_addc_co_u32_e32 v1, vcc, 0, v115, vcc
	s_and_b64 vcc, exec, s[4:5]
	s_mov_b64 s[4:5], -1
	global_store_dwordx4 v[0:1], v[8:11], off nt sc1
	s_cbranch_vccnz .LBB0_896
	s_andn2_b64 vcc, exec, s[10:11]
	s_cbranch_vccnz .LBB0_895
	s_barrier
	s_branch .LBB0_895

.LBB0_965:
	s_add_i32 s7, s5, 1
	v_readlane_b32 s6, v56, s5
	s_add_i32 s8, s5, 2
	s_add_i32 s10, s5, 3
	v_readlane_b32 s14, v56, s7
	v_readlane_b32 s12, v54, s7
	s_ashr_i32 s7, s6, 31
	v_readlane_b32 s16, v56, s8
	v_readlane_b32 s18, v56, s10
	s_ashr_i32 s15, s14, 31
	s_lshl_b64 s[6:7], s[6:7], 10
	s_ashr_i32 s17, s16, 31
	s_ashr_i32 s19, s18, 31
	s_lshl_b64 s[14:15], s[14:15], 10
	global_load_dwordx2 v[38:39], v[36:37], off offset:-3584 nt
	global_load_dwordx2 v[40:41], v[36:37], off offset:-3072 nt
	global_load_dwordx2 v[42:43], v[36:37], off offset:-2560 nt
	global_load_dwordx2 v[44:45], v[36:37], off offset:-2048 nt
	global_load_dwordx2 v[46:47], v[36:37], off offset:-1536 nt
	global_load_dwordx2 v[48:49], v[36:37], off offset:-1024 nt
	global_load_dwordx2 v[50:51], v[36:37], off offset:-512 nt
	global_load_dwordx2 v[52:53], v[36:37], off nt
	v_lshl_add_u64 v[58:59], v[32:33], 0, s[6:7]
	s_lshl_b64 s[6:7], s[16:17], 10
	s_lshl_b64 s[16:17], s[18:19], 10
	v_lshl_add_u64 v[60:61], v[32:33], 0, s[14:15]
	global_load_dword v57, v[58:59], off nt
	global_load_dword v80, v[58:59], off offset:256 nt
	global_load_dword v84, v[58:59], off offset:512 nt
	v_lshl_add_u64 v[62:63], v[32:33], 0, s[6:7]
	v_lshl_add_u64 v[64:65], v[32:33], 0, s[16:17]
	global_load_dword v88, v[60:61], off nt
	global_load_dword v92, v[60:61], off offset:256 nt
	global_load_dword v96, v[60:61], off offset:512 nt
	global_load_dword v104, v[60:61], off offset:768 nt
	global_load_dword v100, v[58:59], off offset:768 nt
	global_load_dword v108, v[62:63], off nt
	global_load_dword v112, v[64:65], off nt
	global_load_dword v116, v[62:63], off offset:256 nt
	global_load_dword v120, v[64:65], off offset:256 nt
	global_load_dword v124, v[62:63], off offset:512 nt
	global_load_dword v128, v[64:65], off offset:512 nt
	global_load_dword v136, v[64:65], off offset:768 nt
	global_load_dword v132, v[62:63], off offset:768 nt
	v_readlane_b32 s4, v54, s5
	s_add_i32 s5, s5, 4
	v_readlane_b32 s10, v54, s10
	s_add_i32 s9, s9, 2
	v_readlane_b32 s8, v54, s8
	v_lshl_add_u64 v[36:37], v[36:37], 0, s[0:1]
	s_cmp_lt_u32 s9, 30
	s_waitcnt vmcnt(12)
	v_cvt_pk_f32_fp8_e32 v[86:87], v88
	v_cvt_pk_f32_fp8_sdwa v[88:89], v88 src0_sel:WORD_1
	s_waitcnt vmcnt(11)
	v_cvt_pk_f32_fp8_e32 v[90:91], v92
	v_cvt_pk_f32_fp8_sdwa v[92:93], v92 src0_sel:WORD_1
	v_cvt_f32_f16_sdwa v59, v39 dst_sel:DWORD dst_unused:UNUSED_PAD src0_sel:WORD_1
	v_cvt_f32_f16_sdwa v61, v38 dst_sel:DWORD dst_unused:UNUSED_PAD src0_sel:WORD_1
	v_cvt_f32_f16_e32 v58, v39
	v_cvt_f32_f16_e32 v60, v38
	v_cvt_f32_f16_sdwa v39, v41 dst_sel:DWORD dst_unused:UNUSED_PAD src0_sel:WORD_1
	v_cvt_f32_f16_sdwa v63, v40 dst_sel:DWORD dst_unused:UNUSED_PAD src0_sel:WORD_1
	v_cvt_f32_f16_e32 v38, v41
	v_cvt_f32_f16_e32 v62, v40
	v_cvt_f32_f16_sdwa v41, v42 dst_sel:DWORD dst_unused:UNUSED_PAD src0_sel:WORD_1
	v_cvt_f32_f16_sdwa v65, v43 dst_sel:DWORD dst_unused:UNUSED_PAD src0_sel:WORD_1
	v_cvt_f32_f16_e32 v40, v42
	v_cvt_f32_f16_e32 v64, v43
	v_cvt_f32_f16_sdwa v43, v44 dst_sel:DWORD dst_unused:UNUSED_PAD src0_sel:WORD_1
	v_cvt_f32_f16_sdwa v67, v45 dst_sel:DWORD dst_unused:UNUSED_PAD src0_sel:WORD_1
	v_cvt_f32_f16_e32 v42, v44
	v_cvt_f32_f16_e32 v66, v45
	v_cvt_f32_f16_sdwa v45, v47 dst_sel:DWORD dst_unused:UNUSED_PAD src0_sel:WORD_1
	v_cvt_f32_f16_sdwa v69, v46 dst_sel:DWORD dst_unused:UNUSED_PAD src0_sel:WORD_1
	v_cvt_f32_f16_e32 v44, v47
	v_cvt_f32_f16_e32 v68, v46
	v_cvt_f32_f16_sdwa v47, v49 dst_sel:DWORD dst_unused:UNUSED_PAD src0_sel:WORD_1
	v_cvt_f32_f16_sdwa v71, v48 dst_sel:DWORD dst_unused:UNUSED_PAD src0_sel:WORD_1
	v_cvt_f32_f16_e32 v46, v49
	v_cvt_f32_f16_e32 v70, v48
	v_cvt_f32_f16_sdwa v49, v50 dst_sel:DWORD dst_unused:UNUSED_PAD src0_sel:WORD_1
	v_cvt_f32_f16_sdwa v73, v51 dst_sel:DWORD dst_unused:UNUSED_PAD src0_sel:WORD_1
	v_cvt_f32_f16_e32 v48, v50
	v_cvt_f32_f16_e32 v72, v51
	v_cvt_f32_f16_sdwa v51, v52 dst_sel:DWORD dst_unused:UNUSED_PAD src0_sel:WORD_1
	v_cvt_f32_f16_sdwa v75, v53 dst_sel:DWORD dst_unused:UNUSED_PAD src0_sel:WORD_1
	v_cvt_f32_f16_e32 v50, v52
	v_cvt_f32_f16_e32 v74, v53
	v_cvt_pk_f32_fp8_e32 v[52:53], v57
	v_cvt_pk_f32_fp8_sdwa v[76:77], v57 src0_sel:WORD_1
	v_cvt_pk_f32_fp8_e32 v[78:79], v80
	v_cvt_pk_f32_fp8_sdwa v[80:81], v80 src0_sel:WORD_1
	s_waitcnt vmcnt(10)
	v_cvt_pk_f32_fp8_e32 v[94:95], v96
	v_cvt_pk_f32_fp8_sdwa v[96:97], v96 src0_sel:WORD_1
	s_waitcnt vmcnt(9)
	v_cvt_pk_f32_fp8_e32 v[102:103], v104
	v_cvt_pk_f32_fp8_sdwa v[104:105], v104 src0_sel:WORD_1
	s_waitcnt vmcnt(6)
	v_cvt_pk_f32_fp8_e32 v[110:111], v112
	v_cvt_pk_f32_fp8_sdwa v[112:113], v112 src0_sel:WORD_1
	s_waitcnt vmcnt(4)
	v_cvt_pk_f32_fp8_e32 v[118:119], v120
	v_cvt_pk_f32_fp8_sdwa v[120:121], v120 src0_sel:WORD_1
	s_waitcnt vmcnt(2)
	v_cvt_pk_f32_fp8_e32 v[126:127], v128
	v_cvt_pk_f32_fp8_sdwa v[128:129], v128 src0_sel:WORD_1
	s_waitcnt vmcnt(1)
	v_cvt_pk_f32_fp8_e32 v[134:135], v136
	v_cvt_pk_f32_fp8_sdwa v[136:137], v136 src0_sel:WORD_1
	v_cvt_pk_f32_fp8_e32 v[82:83], v84
	v_cvt_pk_f32_fp8_sdwa v[84:85], v84 src0_sel:WORD_1
	v_cvt_pk_f32_fp8_e32 v[98:99], v100
	v_cvt_pk_f32_fp8_sdwa v[100:101], v100 src0_sel:WORD_1
	v_cvt_pk_f32_fp8_e32 v[106:107], v108
	v_cvt_pk_f32_fp8_sdwa v[108:109], v108 src0_sel:WORD_1
	v_cvt_pk_f32_fp8_e32 v[114:115], v116
	v_cvt_pk_f32_fp8_sdwa v[116:117], v116 src0_sel:WORD_1
	v_cvt_pk_f32_fp8_e32 v[122:123], v124
	v_cvt_pk_f32_fp8_sdwa v[124:125], v124 src0_sel:WORD_1
	s_waitcnt vmcnt(0)
	v_cvt_pk_f32_fp8_e32 v[130:131], v132
	v_cvt_pk_f32_fp8_sdwa v[132:133], v132 src0_sel:WORD_1
	v_pk_mul_f32 v[86:87], v[86:87], s[12:13] op_sel_hi:[1,0]
	v_pk_mul_f32 v[88:89], v[88:89], s[12:13] op_sel_hi:[1,0]
	v_pk_mul_f32 v[90:91], v[90:91], s[12:13] op_sel_hi:[1,0]
	v_pk_mul_f32 v[92:93], v[92:93], s[12:13] op_sel_hi:[1,0]
	v_pk_mul_f32 v[96:97], v[96:97], s[12:13] op_sel_hi:[1,0]
	v_pk_mul_f32 v[94:95], v[94:95], s[12:13] op_sel_hi:[1,0]
	v_pk_mul_f32 v[104:105], v[104:105], s[12:13] op_sel_hi:[1,0]
	v_pk_mul_f32 v[110:111], v[110:111], s[10:11] op_sel_hi:[1,0]
	v_pk_mul_f32 v[112:113], v[112:113], s[10:11] op_sel_hi:[1,0]
	v_pk_mul_f32 v[118:119], v[118:119], s[10:11] op_sel_hi:[1,0]
	v_pk_mul_f32 v[120:121], v[120:121], s[10:11] op_sel_hi:[1,0]
	v_pk_mul_f32 v[128:129], v[128:129], s[10:11] op_sel_hi:[1,0]
	v_pk_mul_f32 v[136:137], v[136:137], s[10:11] op_sel_hi:[1,0]
	v_pk_fma_f32 v[76:77], v[76:77], s[4:5], v[88:89] op_sel_hi:[1,0,1]
	v_pk_fma_f32 v[52:53], v[52:53], s[4:5], v[86:87] op_sel_hi:[1,0,1]
	v_pk_fma_f32 v[80:81], v[80:81], s[4:5], v[92:93] op_sel_hi:[1,0,1]
	v_pk_fma_f32 v[78:79], v[78:79], s[4:5], v[90:91] op_sel_hi:[1,0,1]
	v_pk_mul_f32 v[102:103], v[102:103], s[12:13] op_sel_hi:[1,0]
	v_pk_mul_f32 v[126:127], v[126:127], s[10:11] op_sel_hi:[1,0]
	v_pk_fma_f32 v[82:83], v[82:83], s[4:5], v[94:95] op_sel_hi:[1,0,1]
	v_pk_fma_f32 v[84:85], v[84:85], s[4:5], v[96:97] op_sel_hi:[1,0,1]
	v_pk_fma_f32 v[88:89], v[100:101], s[4:5], v[104:105] op_sel_hi:[1,0,1]
	v_pk_fma_f32 v[90:91], v[108:109], s[8:9], v[112:113] op_sel_hi:[1,0,1]
	v_pk_fma_f32 v[92:93], v[106:107], s[8:9], v[110:111] op_sel_hi:[1,0,1]
	v_pk_fma_f32 v[94:95], v[116:117], s[8:9], v[120:121] op_sel_hi:[1,0,1]
	v_pk_fma_f32 v[96:97], v[114:115], s[8:9], v[118:119] op_sel_hi:[1,0,1]
	v_pk_fma_f32 v[100:101], v[124:125], s[8:9], v[128:129] op_sel_hi:[1,0,1]
	v_pk_fma_f32 v[104:105], v[132:133], s[8:9], v[136:137] op_sel_hi:[1,0,1]
	v_pk_fma_f32 v[52:53], v[16:17], v[52:53], v[60:61]
	v_pk_fma_f32 v[58:59], v[18:19], v[76:77], v[58:59]
	v_pk_fma_f32 v[60:61], v[24:25], v[78:79], v[62:63]
	v_pk_fma_f32 v[38:39], v[26:27], v[80:81], v[38:39]
	v_pk_fma_f32 v[86:87], v[98:99], s[4:5], v[102:103] op_sel_hi:[1,0,1]
	v_pk_fma_f32 v[98:99], v[122:123], s[8:9], v[126:127] op_sel_hi:[1,0,1]
	v_pk_fma_f32 v[62:63], v[22:23], v[84:85], v[64:65]
	v_pk_fma_f32 v[40:41], v[20:21], v[82:83], v[40:41]
	v_pk_fma_f32 v[64:65], v[30:31], v[88:89], v[66:67]
	v_pk_fma_f32 v[66:67], v[16:17], v[92:93], v[68:69]
	v_pk_fma_f32 v[44:45], v[18:19], v[90:91], v[44:45]
	v_pk_fma_f32 v[68:69], v[24:25], v[96:97], v[70:71]
	v_pk_fma_f32 v[46:47], v[26:27], v[94:95], v[46:47]
	v_pk_fma_f32 v[70:71], v[22:23], v[100:101], v[72:73]
	v_pk_fma_f32 v[72:73], v[30:31], v[104:105], v[74:75]
	v_pk_mul_f32 v[74:75], v[58:59], v[58:59]
	v_pk_mul_f32 v[76:77], v[52:53], v[52:53]
	v_pk_mul_f32 v[78:79], v[38:39], v[38:39]
	v_pk_mul_f32 v[80:81], v[60:61], v[60:61]
	v_pk_mul_f32 v[134:135], v[134:135], s[10:11] op_sel_hi:[1,0]
	v_pk_fma_f32 v[42:43], v[28:29], v[86:87], v[42:43]
	v_pk_fma_f32 v[48:49], v[20:21], v[98:99], v[48:49]
	v_mul_f32_e32 v82, v41, v41
	v_mul_f32_e32 v84, v63, v63
	v_pk_mul_f32 v[86:87], v[44:45], v[44:45]
	v_pk_mul_f32 v[88:89], v[66:67], v[66:67]
	v_pk_mul_f32 v[90:91], v[46:47], v[46:47]
	v_pk_mul_f32 v[92:93], v[68:69], v[68:69]
	v_pk_mov_b32 v[98:99], v[76:77], v[74:75] op_sel:[1,0]
	v_mov_b32_e32 v77, v75
	v_pk_mov_b32 v[74:75], v[80:81], v[78:79] op_sel:[1,0]
	v_mov_b32_e32 v81, v79
	v_pk_fma_f32 v[102:103], v[130:131], s[8:9], v[134:135] op_sel_hi:[1,0,1]
	v_mul_f32_e32 v100, v64, v64
	v_mul_f32_e32 v101, v65, v65
	v_pk_fma_f32 v[78:79], v[40:41], v[40:41], v[82:83] op_sel_hi:[1,1,0]
	v_pk_fma_f32 v[82:83], v[62:63], v[62:63], v[84:85] op_sel_hi:[1,1,0]
	v_pk_mov_b32 v[84:85], v[88:89], v[86:87] op_sel:[1,0]
	v_mov_b32_e32 v89, v87
	v_pk_mov_b32 v[86:87], v[92:93], v[90:91] op_sel:[1,0]
	v_mov_b32_e32 v93, v91
	v_pk_add_f32 v[76:77], v[98:99], v[76:77]
	v_pk_add_f32 v[74:75], v[74:75], v[80:81]
	v_pk_fma_f32 v[50:51], v[28:29], v[102:103], v[50:51]
	v_mul_f32_e32 v57, v42, v42
	v_mul_f32_e32 v97, v43, v43
	v_mul_f32_e32 v94, v49, v49
	v_mul_f32_e32 v96, v71, v71
	v_mov_b32_e32 v79, v100
	v_mov_b32_e32 v83, v101
	v_pk_add_f32 v[80:81], v[84:85], v[88:89]
	v_pk_add_f32 v[84:85], v[86:87], v[92:93]
	v_pk_add_f32 v[76:77], v[76:77], v[76:77] op_sel:[0,1] op_sel_hi:[1,0]
	v_pk_add_f32 v[74:75], v[74:75], v[74:75] op_sel:[0,1] op_sel_hi:[1,0]
	v_mul_f32_e32 v102, v50, v50
	v_mul_f32_e32 v103, v51, v51
	v_mul_f32_e32 v104, v72, v72
	v_mul_f32_e32 v105, v73, v73
	v_pk_fma_f32 v[90:91], v[48:49], v[48:49], v[94:95] op_sel_hi:[1,1,0]
	v_pk_fma_f32 v[94:95], v[70:71], v[70:71], v[96:97] op_sel_hi:[1,1,0]
	v_pk_add_f32 v[78:79], v[78:79], v[82:83]
	v_pk_add_f32 v[80:81], v[80:81], v[80:81] op_sel:[0,1] op_sel_hi:[1,0]
	v_pk_add_f32 v[82:83], v[84:85], v[84:85] op_sel:[0,1] op_sel_hi:[1,0]
	v_mov_b32_e32 v77, v57
	v_mov_b32_e32 v75, v97
	v_mov_b32_e32 v91, v104
	v_mov_b32_e32 v95, v105
	v_mov_b32_e32 v81, v102
	v_mov_b32_e32 v83, v103
	v_pk_add_f32 v[74:75], v[76:77], v[74:75]
	v_pk_add_f32 v[84:85], v[90:91], v[94:95]
	v_pk_add_f32 v[76:77], v[80:81], v[82:83]
	v_pk_add_f32 v[74:75], v[74:75], v[78:79]
	v_pk_add_f32 v[76:77], v[76:77], v[84:85]
	v_add_f32_e32 v57, v74, v75
	v_add_f32_e32 v74, v76, v77
	s_nop 0
	v_add_f32_dpp v57, v57, v57 quad_perm:[1,0,3,2] row_mask:0xf bank_mask:0xf bound_ctrl:1
	v_add_f32_dpp v74, v74, v74 quad_perm:[1,0,3,2] row_mask:0xf bank_mask:0xf bound_ctrl:1
	s_nop 0
	v_add_f32_dpp v57, v57, v57 quad_perm:[2,3,0,1] row_mask:0xf bank_mask:0xf bound_ctrl:1
	v_add_f32_dpp v74, v74, v74 quad_perm:[2,3,0,1] row_mask:0xf bank_mask:0xf bound_ctrl:1
	s_nop 0
	v_add_f32_dpp v57, v57, v57 row_half_mirror row_mask:0xf bank_mask:0xf bound_ctrl:1
	v_add_f32_dpp v74, v74, v74 row_half_mirror row_mask:0xf bank_mask:0xf bound_ctrl:1
	s_nop 0
	v_add_f32_dpp v57, v57, v57 row_mirror row_mask:0xf bank_mask:0xf bound_ctrl:1
	v_add_f32_dpp v74, v74, v74 row_mirror row_mask:0xf bank_mask:0xf bound_ctrl:1
	v_readlane_b32 s4, v57, 16
	v_readlane_b32 s8, v57, 48
	v_readlane_b32 s6, v57, 0
	v_readlane_b32 s7, v57, 32
	v_readlane_b32 s10, v74, 0
	v_readlane_b32 s12, v74, 16
	v_readlane_b32 s11, v74, 32
	v_readlane_b32 s13, v74, 48
	v_mov_b32_e32 v74, s4
	v_mov_b32_e32 v75, s8
	v_mov_b32_e32 v76, s12
	v_mov_b32_e32 v77, s13
	v_pk_add_f32 v[74:75], s[6:7], v[74:75]
	v_pk_add_f32 v[76:77], s[10:11], v[76:77]
	v_add_f32_e32 v57, v74, v75
	v_add_f32_e32 v74, v76, v77
	v_fmamk_f32 v57, v57, 0x3a800000, v55
	v_fmamk_f32 v75, v74, 0x3a800000, v55
	v_rsq_f32_e32 v74, v57
	v_rsq_f32_e32 v76, v75
	v_pk_mul_f32 v[52:53], v[52:53], v[74:75] op_sel_hi:[1,0]
	v_pk_mul_f32 v[58:59], v[58:59], v[74:75] op_sel_hi:[1,0]
	v_pk_mul_f32 v[60:61], v[60:61], v[74:75] op_sel_hi:[1,0]
	v_pk_mul_f32 v[78:79], v[38:39], v[74:75] op_sel_hi:[1,0]
	v_pk_mul_f32 v[80:81], v[40:41], v[74:75] op_sel_hi:[1,0]
	v_pk_mul_f32 v[62:63], v[62:63], v[74:75] op_sel_hi:[1,0]
	v_pk_mul_f32 v[82:83], v[42:43], v[74:75] op_sel_hi:[1,0]
	v_pk_mul_f32 v[64:65], v[64:65], v[74:75] op_sel_hi:[1,0]
	v_pk_mul_f32 v[66:67], v[66:67], v[76:77] op_sel_hi:[1,0]
	v_pk_mul_f32 v[74:75], v[44:45], v[76:77] op_sel_hi:[1,0]
	v_pk_mul_f32 v[68:69], v[68:69], v[76:77] op_sel_hi:[1,0]
	v_pk_mul_f32 v[84:85], v[46:47], v[76:77] op_sel_hi:[1,0]
	v_pk_mul_f32 v[86:87], v[48:49], v[76:77] op_sel_hi:[1,0]
	v_pk_mul_f32 v[70:71], v[70:71], v[76:77] op_sel_hi:[1,0]
	v_pk_mul_f32 v[88:89], v[50:51], v[76:77] op_sel_hi:[1,0]
	v_pk_mul_f32 v[72:73], v[72:73], v[76:77] op_sel_hi:[1,0]
	v_pk_mul_f32 v[40:41], v[2:3], v[58:59]
	v_pk_mul_f32 v[38:39], v[0:1], v[52:53]
	v_pk_mul_f32 v[44:45], v[6:7], v[78:79]
	v_pk_mul_f32 v[42:43], v[4:5], v[60:61]
	v_pk_mul_f32 v[48:49], v[10:11], v[62:63]
	v_pk_mul_f32 v[46:47], v[8:9], v[80:81]
	v_pk_mul_f32 v[52:53], v[14:15], v[64:65]
	v_pk_mul_f32 v[50:51], v[12:13], v[82:83]
	v_pk_mul_f32 v[60:61], v[2:3], v[74:75]
	v_pk_mul_f32 v[58:59], v[0:1], v[66:67]
	v_pk_mul_f32 v[64:65], v[6:7], v[84:85]
	v_pk_mul_f32 v[62:63], v[4:5], v[68:69]
	v_pk_mul_f32 v[68:69], v[10:11], v[70:71]
	v_pk_mul_f32 v[66:67], v[8:9], v[86:87]
	v_pk_mul_f32 v[72:73], v[14:15], v[72:73]
	v_pk_mul_f32 v[70:71], v[12:13], v[88:89]
	global_store_dwordx4 v[34:35], v[38:41], off offset:-4096 nt sc1
	global_store_dwordx4 v[34:35], v[42:45], off offset:-3072 nt sc1
	global_store_dwordx4 v[34:35], v[46:49], off offset:-2048 nt sc1
	global_store_dwordx4 v[34:35], v[50:53], off offset:-1024 nt sc1
	global_store_dwordx4 v[34:35], v[58:61], off nt sc1
	global_store_dwordx4 v[34:35], v[62:65], off offset:1024 nt sc1
	global_store_dwordx4 v[34:35], v[66:69], off offset:2048 nt sc1
	global_store_dwordx4 v[34:35], v[70:73], off offset:3072 nt sc1
	v_lshl_add_u64 v[34:35], v[34:35], 0, s[2:3]
	s_cbranch_scc1 .LBB0_965
	s_endpgm
